# K-loop back-edge rotation on all six GEMM loops: loop-counter/pointer SALU moved from after the last barrier and the loop head into the last MFMA block
# speedup vs baseline: 1.0059x; 1.0003x over previous
; #define PG8_STAGE(bufoff, gbase, voff) do { _Pragma("unroll") for (int _i = 0; _i < 2; ++_i) \
;         __builtin_amdgcn_global_load_lds((const unsigned*)((const char*)(gbase) + (voff)[_i]), (PG8_LAS unsigned*)(lds + (bufoff) + ldsw + _i * 8192), 16, 0, 0); } while (0)
; #define PG8_LDA(dst, b, h) do { _Pragma("unroll") for (int m = 0; m < 4; ++m) _Pragma("unroll") for (int k = 0; k < 2; ++k) dst[m][k] = *(const PG8_LAS bf16x8*)(lds + PG8_SA(b, h) + aoff + m * 2048 + k * 1024); } while (0)
; #define PG8_LDB(dst, b, h) do { _Pragma("unroll") for (int n = 0; n < 2; ++n) _Pragma("unroll") for (int k = 0; k < 2; ++k) dst[n][k] = *(const PG8_LAS bf16x8*)(lds + PG8_SB(b, h) + boff + n * 2048 + k * 1024); } while (0)
; #define PG8_WAIT_V(n) asm volatile("s_waitcnt vmcnt(" #n ")" ::: "memory")
; #define PG8_WAIT_L(n) asm volatile("s_waitcnt lgkmcnt(" #n ")" ::: "memory")
; #define PG8_BAR __builtin_amdgcn_s_barrier()
; template <class Epi, class Sched, bool ALIGN_EPI = false, bool SP2 = false>
; __device__ __forceinline__ void gemm_phase(PG8_LAS unsigned char* lds, const Gemm g, const Sched& S, const Epi& E, const int tid) {
;     ...
;         const bool has_next = S.next(ui + 1, nxt);
;         const char* nA = has_next ? (const char*)g.A + (size_t)nxt.pm * tstep : cA; const char* nB = has_next ? (const char*)g.Bt + (size_t)nxt.pn * tstep : cB;
;         for (int t = 0; t < nt; t += 2) {
;             const bool last = (t == nt - 2);
;             const char* a1 = cA + (size_t)(t + 1) * kstep;
;             const char* a2 = last ? nA : cA + (size_t)(t + 2) * kstep; const char* b2 = last ? nB : cB + (size_t)(t + 2) * kstep;
;             const char* a3 = a2 + kstep; const char* b3 = b2 + kstep;
;             if (last && has_next) S.a_ready(nxt);
;             if constexpr (SP2) {
;             PG8_LDB(B0, 0, 0); PG8_LDB(B1, 0, 1); PG8_SCHED; PG8_LDA(At, 0, 0); PG8_STAGE(PG8_SA(1, 1), a1 + hstep, voffA);
;             PG8_WAIT_V(8); PG8_WAIT_L(0); PG8_BAR; PG8_MMA(0, 0, At, B0); PG8_MMA(0, 1, At, B1); PG8_BAR; PG8_SCHED;
;     ...
;         for (int a = 0; a < 2; ++a)
; #pragma unroll
;             for (int b = 0; b < 2; ++b)
; #pragma unroll
;                 for (int m = 0; m < 4; ++m)
; #pragma unroll
;                     for (int n = 0; n < 2; ++n) acc[a][b][m][n] = (f32x4){0.f, 0.f, 0.f, 0.f};
;         cur = nxt; cA = nA; cB = nB; ++ui;
.LBB0_100:
	s_ashr_i32 s15, s14, 31
	s_lshl_b64 s[36:37], s[14:15], 19
	s_add_u32 s44, s39, s36
	s_addc_u32 s45, s43, s37
	s_and_b64 s[36:37], s[2:3], exec
	s_cselect_b32 s15, s45, s55
	s_cselect_b32 s42, s44, s54
	s_ashr_i32 s13, s12, 31
	s_lshl_b64 s[36:37], s[12:13], 19
	s_add_u32 s46, s49, s36
	s_addc_u32 s47, s50, s37
	s_and_b64 s[36:37], s[2:3], exec
	s_cselect_b32 s13, s47, s57
	s_cselect_b32 s58, s46, s56
	s_add_u32 s54, s54, 0x40080
	s_addc_u32 s55, s55, 0
	s_add_u32 s56, s56, 0x100
	v_mov_b32_e32 v4, 0
	s_addc_u32 s57, s57, 0
	s_mov_b32 s59, -2
	v_mov_b32_e32 v5, v4
	v_mov_b32_e32 v6, v4
	v_mov_b32_e32 v7, v4
	v_mov_b32_e32 v12, v4
	v_mov_b32_e32 v13, v4
	v_mov_b32_e32 v14, v4
	v_mov_b32_e32 v15, v4
	v_mov_b32_e32 v20, v4
	v_mov_b32_e32 v21, v4
	v_mov_b32_e32 v22, v4
	v_mov_b32_e32 v23, v4
	v_mov_b32_e32 v28, v4
	v_mov_b32_e32 v29, v4
	v_mov_b32_e32 v30, v4
	v_mov_b32_e32 v31, v4
	v_mov_b32_e32 v36, v4
	v_mov_b32_e32 v37, v4
	v_mov_b32_e32 v38, v4
	v_mov_b32_e32 v39, v4
	v_mov_b32_e32 v44, v4
	v_mov_b32_e32 v45, v4
	v_mov_b32_e32 v46, v4
	v_mov_b32_e32 v47, v4
	v_mov_b32_e32 v52, v4
	v_mov_b32_e32 v53, v4
	v_mov_b32_e32 v54, v4
	v_mov_b32_e32 v55, v4
	v_mov_b32_e32 v60, v4
	v_mov_b32_e32 v61, v4
	v_mov_b32_e32 v62, v4
	v_mov_b32_e32 v63, v4
	v_mov_b32_e32 v8, v4
	v_mov_b32_e32 v9, v4
	v_mov_b32_e32 v10, v4
	v_mov_b32_e32 v11, v4
	v_mov_b32_e32 v16, v4
	v_mov_b32_e32 v17, v4
	v_mov_b32_e32 v18, v4
	v_mov_b32_e32 v19, v4
	v_mov_b32_e32 v24, v4
	v_mov_b32_e32 v25, v4
	v_mov_b32_e32 v26, v4
	v_mov_b32_e32 v27, v4
	v_mov_b32_e32 v32, v4
	v_mov_b32_e32 v33, v4
	v_mov_b32_e32 v34, v4
	v_mov_b32_e32 v35, v4
	v_mov_b32_e32 v40, v4
	v_mov_b32_e32 v41, v4
	v_mov_b32_e32 v42, v4
	v_mov_b32_e32 v43, v4
	v_mov_b32_e32 v48, v4
	v_mov_b32_e32 v49, v4
	v_mov_b32_e32 v50, v4
	v_mov_b32_e32 v51, v4
	v_mov_b32_e32 v56, v4
	v_mov_b32_e32 v57, v4
	v_mov_b32_e32 v58, v4
	v_mov_b32_e32 v59, v4
	v_mov_b32_e32 v64, v4
	v_mov_b32_e32 v65, v4
	v_mov_b32_e32 v66, v4
	v_mov_b32_e32 v67, v4
	v_mov_b32_e32 v68, v4
	v_mov_b32_e32 v69, v4
	v_mov_b32_e32 v70, v4
	v_mov_b32_e32 v71, v4
	v_mov_b32_e32 v76, v4
	v_mov_b32_e32 v77, v4
	v_mov_b32_e32 v78, v4
	v_mov_b32_e32 v79, v4
	v_mov_b32_e32 v84, v4
	v_mov_b32_e32 v85, v4
	v_mov_b32_e32 v86, v4
	v_mov_b32_e32 v87, v4
	v_mov_b32_e32 v92, v4
	v_mov_b32_e32 v93, v4
	v_mov_b32_e32 v94, v4
	v_mov_b32_e32 v95, v4
	v_mov_b32_e32 v100, v4
	v_mov_b32_e32 v101, v4
	v_mov_b32_e32 v102, v4
	v_mov_b32_e32 v103, v4
	v_mov_b32_e32 v108, v4
	v_mov_b32_e32 v109, v4
	v_mov_b32_e32 v110, v4
	v_mov_b32_e32 v111, v4
	v_mov_b32_e32 v116, v4
	v_mov_b32_e32 v117, v4
	v_mov_b32_e32 v118, v4
	v_mov_b32_e32 v119, v4
	v_mov_b32_e32 v124, v4
	v_mov_b32_e32 v125, v4
	v_mov_b32_e32 v126, v4
	v_mov_b32_e32 v127, v4
	v_mov_b32_e32 v72, v4
	v_mov_b32_e32 v73, v4
	v_mov_b32_e32 v74, v4
	v_mov_b32_e32 v75, v4
	v_mov_b32_e32 v80, v4
	v_mov_b32_e32 v81, v4
	v_mov_b32_e32 v82, v4
	v_mov_b32_e32 v83, v4
	v_mov_b32_e32 v88, v4
	v_mov_b32_e32 v89, v4
	v_mov_b32_e32 v90, v4
	v_mov_b32_e32 v91, v4
	v_mov_b32_e32 v96, v4
	v_mov_b32_e32 v97, v4
	v_mov_b32_e32 v98, v4
	v_mov_b32_e32 v99, v4
	v_mov_b32_e32 v104, v4
	v_mov_b32_e32 v105, v4
	v_mov_b32_e32 v106, v4
	v_mov_b32_e32 v107, v4
	v_mov_b32_e32 v112, v4
	v_mov_b32_e32 v113, v4
	v_mov_b32_e32 v114, v4
	v_mov_b32_e32 v115, v4
	v_mov_b32_e32 v120, v4
	v_mov_b32_e32 v121, v4
	v_mov_b32_e32 v122, v4
	v_mov_b32_e32 v123, v4
	v_mov_b32_e32 v128, v4
	v_mov_b32_e32 v129, v4
	v_mov_b32_e32 v130, v4
	v_mov_b32_e32 v131, v4
	s_add_u32 s36, s54, 0xfffc0080
	s_addc_u32 s37, s55, -1
	s_add_i32 s70, 0, 0x10000
	s_cmp_eq_u32 s59, 12
	s_cselect_b32 s37, s15, s37
	s_cselect_b32 s36, s42, s36
	s_cselect_b32 s73, s13, s57
	s_cselect_b32 s72, s58, s56
	s_add_i32 s71, 0, 0x14000
.LBB0_101:
	v_add_u32_e32 v161, s70, v149
	ds_read_b128 v[144:147], v161
	ds_read_b128 v[162:165], v161 offset:1024
	ds_read_b128 v[166:169], v161 offset:2048
	ds_read_b128 v[170:173], v161 offset:3072
	v_add_u32_e32 v161, s71, v149
	ds_read_b128 v[174:177], v161
	ds_read_b128 v[178:181], v161 offset:1024
	ds_read_b128 v[182:185], v161 offset:2048
	ds_read_b128 v[186:189], v161 offset:3072
	v_lshl_add_u64 v[198:199], s[54:55], 0, v[140:141]
	s_add_i32 m0, s51, 0xc000
	ds_read_b128 v[190:193], v160
	ds_read_b128 v[194:197], v160 offset:1024
	ds_read_b128 v[212:215], v160 offset:2048
	ds_read_b128 v[216:219], v160 offset:3072
	ds_read_b128 v[220:223], v160 offset:4096
	ds_read_b128 v[224:227], v160 offset:5120
	ds_read_b128 v[228:231], v160 offset:6144
	ds_read_b128 v[242:245], v160 offset:7168
	global_load_lds_dwordx4 v[198:199], off
	v_lshl_add_u64 v[198:199], s[54:55], 0, v[142:143]
	s_add_i32 m0, s51, 0xe000
	s_nop 0
	global_load_lds_dwordx4 v[198:199], off
	s_waitcnt vmcnt(8)
	s_waitcnt lgkmcnt(0)
	s_barrier
; #define PG8_STAGE(bufoff, gbase, voff) do { _Pragma("unroll") for (int _i = 0; _i < 2; ++_i) \
;         __builtin_amdgcn_global_load_lds((const unsigned*)((const char*)(gbase) + (voff)[_i]), (PG8_LAS unsigned*)(lds + (bufoff) + ldsw + _i * 8192), 16, 0, 0); } while (0)
; #define PG8_LDA(dst, b, h) do { _Pragma("unroll") for (int m = 0; m < 4; ++m) _Pragma("unroll") for (int k = 0; k < 2; ++k) dst[m][k] = *(const PG8_LAS bf16x8*)(lds + PG8_SA(b, h) + aoff + m * 2048 + k * 1024); } while (0)
; #define PG8_LDB(dst, b, h) do { _Pragma("unroll") for (int n = 0; n < 2; ++n) _Pragma("unroll") for (int k = 0; k < 2; ++k) dst[n][k] = *(const PG8_LAS bf16x8*)(lds + PG8_SB(b, h) + boff + n * 2048 + k * 1024); } while (0)
; #define PG8_MMA(ai, bj, At, Bt) do { __builtin_amdgcn_s_setprio(1); _Pragma("unroll") for (int m = 0; m < 4; ++m) _Pragma("unroll") for (int n = 0; n < 2; ++n) _Pragma("unroll") for (int k = 0; k < 2; ++k) \
;         acc[ai][bj][m][n] = __builtin_amdgcn_mfma_f32_16x16x32_bf16(Bt[n][k], At[m][k], acc[ai][bj][m][n], 0, 0, 0); __builtin_amdgcn_s_setprio(0); } while (0)
; #define PG8_WAIT_V(n) asm volatile("s_waitcnt vmcnt(" #n ")" ::: "memory")
; #define PG8_WAIT_L(n) asm volatile("s_waitcnt lgkmcnt(" #n ")" ::: "memory")
; #define PG8_BAR __builtin_amdgcn_s_barrier()
; #define PG8_SCHED __builtin_amdgcn_sched_barrier(0)
; template <class Epi, class Sched, bool ALIGN_EPI = false, bool SP2 = false>
; __device__ __forceinline__ void gemm_phase(PG8_LAS unsigned char* lds, const Gemm g, const Sched& S, const Epi& E, const int tid) {
;     ...
;             PG8_LDB(B0, 0, 0); PG8_LDB(B1, 0, 1); PG8_SCHED; PG8_LDA(At, 0, 0); PG8_STAGE(PG8_SA(1, 1), a1 + hstep, voffA);
;             PG8_WAIT_V(8); PG8_WAIT_L(0); PG8_BAR; PG8_MMA(0, 0, At, B0); PG8_MMA(0, 1, At, B1); PG8_BAR; PG8_SCHED;
;             PG8_LDA(At, 0, 1); PG8_STAGE(PG8_SB(0, 0), b2, voffB); PG8_STAGE(PG8_SB(0, 1), b2, voffB1); PG8_STAGE(PG8_SA(0, 0), a2, voffA);
;             PG8_WAIT_V(8); PG8_WAIT_L(0); PG8_BAR; PG8_MMA(1, 0, At, B0); PG8_MMA(1, 1, At, B1); PG8_BAR; PG8_SCHED;
	s_setprio 1
	s_waitcnt lgkmcnt(0)
	v_mfma_f32_16x16x32_bf16 v[128:131], v[144:147], v[190:193], v[128:131]
	v_mfma_f32_16x16x32_bf16 v[120:123], v[166:169], v[190:193], v[120:123]
	v_mfma_f32_16x16x32_bf16 v[112:115], v[144:147], v[212:215], v[112:115]
	v_mfma_f32_16x16x32_bf16 v[104:107], v[166:169], v[212:215], v[104:107]
	v_mfma_f32_16x16x32_bf16 v[96:99], v[144:147], v[220:223], v[96:99]
	v_mfma_f32_16x16x32_bf16 v[88:91], v[166:169], v[220:223], v[88:91]
	v_mfma_f32_16x16x32_bf16 v[80:83], v[144:147], v[228:231], v[80:83]
	v_mfma_f32_16x16x32_bf16 v[72:75], v[166:169], v[228:231], v[72:75]
	v_mfma_f32_16x16x32_bf16 v[128:131], v[162:165], v[194:197], v[128:131]
	v_mfma_f32_16x16x32_bf16 v[120:123], v[170:173], v[194:197], v[120:123]
	v_mfma_f32_16x16x32_bf16 v[112:115], v[162:165], v[216:219], v[112:115]
	v_mfma_f32_16x16x32_bf16 v[104:107], v[170:173], v[216:219], v[104:107]
	v_mfma_f32_16x16x32_bf16 v[96:99], v[162:165], v[224:227], v[96:99]
	v_mfma_f32_16x16x32_bf16 v[88:91], v[170:173], v[224:227], v[88:91]
	v_mfma_f32_16x16x32_bf16 v[80:83], v[162:165], v[242:245], v[80:83]
	v_mfma_f32_16x16x32_bf16 v[72:75], v[170:173], v[242:245], v[72:75]
	s_setprio 0
	s_setprio 1
	v_mfma_f32_16x16x32_bf16 v[124:127], v[174:177], v[190:193], v[124:127]
	v_mfma_f32_16x16x32_bf16 v[116:119], v[182:185], v[190:193], v[116:119]
	v_mfma_f32_16x16x32_bf16 v[108:111], v[174:177], v[212:215], v[108:111]
	v_mfma_f32_16x16x32_bf16 v[100:103], v[182:185], v[212:215], v[100:103]
	v_mfma_f32_16x16x32_bf16 v[92:95], v[174:177], v[220:223], v[92:95]
	v_mfma_f32_16x16x32_bf16 v[84:87], v[182:185], v[220:223], v[84:87]
	v_mfma_f32_16x16x32_bf16 v[76:79], v[174:177], v[228:231], v[76:79]
	v_mfma_f32_16x16x32_bf16 v[68:71], v[182:185], v[228:231], v[68:71]
	v_mfma_f32_16x16x32_bf16 v[124:127], v[178:181], v[194:197], v[124:127]
	v_mfma_f32_16x16x32_bf16 v[116:119], v[186:189], v[194:197], v[116:119]
	v_mfma_f32_16x16x32_bf16 v[108:111], v[178:181], v[216:219], v[108:111]
	v_mfma_f32_16x16x32_bf16 v[100:103], v[186:189], v[216:219], v[100:103]
	v_mfma_f32_16x16x32_bf16 v[92:95], v[178:181], v[224:227], v[92:95]
	v_mfma_f32_16x16x32_bf16 v[84:87], v[186:189], v[224:227], v[84:87]
	v_mfma_f32_16x16x32_bf16 v[76:79], v[178:181], v[242:245], v[76:79]
	v_mfma_f32_16x16x32_bf16 v[68:71], v[186:189], v[242:245], v[68:71]
	s_setprio 0
	s_barrier
	s_add_i32 s70, s70, s48
	v_lshl_add_u64 v[198:199], s[72:73], 0, v[2:3]
	s_mov_b32 m0, s70
	ds_read_b128 v[190:193], v160 offset:16384
	ds_read_b128 v[194:197], v160 offset:17408
	ds_read_b128 v[212:215], v160 offset:18432
	ds_read_b128 v[216:219], v160 offset:19456
	ds_read_b128 v[220:223], v160 offset:20480
	ds_read_b128 v[224:227], v160 offset:21504
	ds_read_b128 v[228:231], v160 offset:22528
	ds_read_b128 v[242:245], v160 offset:23552
	global_load_lds_dwordx4 v[198:199], off
	v_lshl_add_u64 v[200:201], s[72:73], 0, v[136:137]
	s_add_i32 m0, s70, 0x2000
	s_add_i32 s70, s71, s48
	global_load_lds_dwordx4 v[200:201], off
	v_lshl_add_u64 v[202:203], s[72:73], 0, v[132:133]
	s_mov_b32 m0, s70
	v_lshl_add_u64 v[204:205], s[72:73], 0, v[138:139]
	global_load_lds_dwordx4 v[202:203], off
	s_add_i32 m0, s70, 0x2000
	v_lshl_add_u64 v[208:209], s[36:37], 0, v[0:1]
	global_load_lds_dwordx4 v[204:205], off
	s_mov_b32 m0, s51
	v_lshl_add_u64 v[210:211], s[36:37], 0, v[134:135]
	global_load_lds_dwordx4 v[208:209], off
	s_mov_b32 m0, s53
	s_nop 0
	global_load_lds_dwordx4 v[210:211], off
	s_waitcnt vmcnt(8)
	s_waitcnt lgkmcnt(0)
	s_barrier
	s_setprio 1
	s_waitcnt lgkmcnt(0)
	v_mfma_f32_16x16x32_bf16 v[64:67], v[144:147], v[190:193], v[64:67]
	v_mfma_f32_16x16x32_bf16 v[56:59], v[166:169], v[190:193], v[56:59]
	v_mfma_f32_16x16x32_bf16 v[48:51], v[144:147], v[212:215], v[48:51]
	v_mfma_f32_16x16x32_bf16 v[40:43], v[166:169], v[212:215], v[40:43]
	v_mfma_f32_16x16x32_bf16 v[32:35], v[144:147], v[220:223], v[32:35]
	v_mfma_f32_16x16x32_bf16 v[24:27], v[166:169], v[220:223], v[24:27]
	v_mfma_f32_16x16x32_bf16 v[16:19], v[144:147], v[228:231], v[16:19]
	v_mfma_f32_16x16x32_bf16 v[8:11], v[166:169], v[228:231], v[8:11]
	v_mfma_f32_16x16x32_bf16 v[64:67], v[162:165], v[194:197], v[64:67]
	v_mfma_f32_16x16x32_bf16 v[56:59], v[170:173], v[194:197], v[56:59]
	v_mfma_f32_16x16x32_bf16 v[48:51], v[162:165], v[216:219], v[48:51]
	v_mfma_f32_16x16x32_bf16 v[40:43], v[170:173], v[216:219], v[40:43]
	v_mfma_f32_16x16x32_bf16 v[32:35], v[162:165], v[224:227], v[32:35]
	v_mfma_f32_16x16x32_bf16 v[24:27], v[170:173], v[224:227], v[24:27]
	v_mfma_f32_16x16x32_bf16 v[16:19], v[162:165], v[242:245], v[16:19]
	v_mfma_f32_16x16x32_bf16 v[8:11], v[170:173], v[242:245], v[8:11]
	s_setprio 0
	s_setprio 1
	v_mfma_f32_16x16x32_bf16 v[60:63], v[174:177], v[190:193], v[60:63]
	v_mfma_f32_16x16x32_bf16 v[52:55], v[182:185], v[190:193], v[52:55]
	v_mfma_f32_16x16x32_bf16 v[44:47], v[174:177], v[212:215], v[44:47]
	v_mfma_f32_16x16x32_bf16 v[36:39], v[182:185], v[212:215], v[36:39]
	v_mfma_f32_16x16x32_bf16 v[28:31], v[174:177], v[220:223], v[28:31]
	v_mfma_f32_16x16x32_bf16 v[20:23], v[182:185], v[220:223], v[20:23]
	v_mfma_f32_16x16x32_bf16 v[12:15], v[174:177], v[228:231], v[12:15]
	v_mfma_f32_16x16x32_bf16 v[4:7], v[182:185], v[228:231], v[4:7]
	v_mfma_f32_16x16x32_bf16 v[60:63], v[178:181], v[194:197], v[60:63]
	v_mfma_f32_16x16x32_bf16 v[52:55], v[186:189], v[194:197], v[52:55]
	v_mfma_f32_16x16x32_bf16 v[44:47], v[178:181], v[216:219], v[44:47]
	v_mfma_f32_16x16x32_bf16 v[36:39], v[186:189], v[216:219], v[36:39]
	v_mfma_f32_16x16x32_bf16 v[28:31], v[178:181], v[224:227], v[28:31]
	v_mfma_f32_16x16x32_bf16 v[20:23], v[186:189], v[224:227], v[20:23]
	v_mfma_f32_16x16x32_bf16 v[12:15], v[178:181], v[242:245], v[12:15]
	v_mfma_f32_16x16x32_bf16 v[4:7], v[186:189], v[242:245], v[4:7]
	s_setprio 0
	s_barrier
; #define PG8_STAGE(bufoff, gbase, voff) do { _Pragma("unroll") for (int _i = 0; _i < 2; ++_i) \
;         __builtin_amdgcn_global_load_lds((const unsigned*)((const char*)(gbase) + (voff)[_i]), (PG8_LAS unsigned*)(lds + (bufoff) + ldsw + _i * 8192), 16, 0, 0); } while (0)
; #define PG8_LDA(dst, b, h) do { _Pragma("unroll") for (int m = 0; m < 4; ++m) _Pragma("unroll") for (int k = 0; k < 2; ++k) dst[m][k] = *(const PG8_LAS bf16x8*)(lds + PG8_SA(b, h) + aoff + m * 2048 + k * 1024); } while (0)
; #define PG8_LDB(dst, b, h) do { _Pragma("unroll") for (int n = 0; n < 2; ++n) _Pragma("unroll") for (int k = 0; k < 2; ++k) dst[n][k] = *(const PG8_LAS bf16x8*)(lds + PG8_SB(b, h) + boff + n * 2048 + k * 1024); } while (0)
; #define PG8_MMA(ai, bj, At, Bt) do { __builtin_amdgcn_s_setprio(1); _Pragma("unroll") for (int m = 0; m < 4; ++m) _Pragma("unroll") for (int n = 0; n < 2; ++n) _Pragma("unroll") for (int k = 0; k < 2; ++k) \
;         acc[ai][bj][m][n] = __builtin_amdgcn_mfma_f32_16x16x32_bf16(Bt[n][k], At[m][k], acc[ai][bj][m][n], 0, 0, 0); __builtin_amdgcn_s_setprio(0); } while (0)
; #define PG8_WAIT_V(n) asm volatile("s_waitcnt vmcnt(" #n ")" ::: "memory")
; #define PG8_WAIT_L(n) asm volatile("s_waitcnt lgkmcnt(" #n ")" ::: "memory")
; #define PG8_BAR __builtin_amdgcn_s_barrier()
; #define PG8_SCHED __builtin_amdgcn_sched_barrier(0)
; template <class Epi, class Sched, bool ALIGN_EPI = false, bool SP2 = false>
; __device__ __forceinline__ void gemm_phase(PG8_LAS unsigned char* lds, const Gemm g, const Sched& S, const Epi& E, const int tid) {
;     ...
;             PG8_LDB(B0, 1, 0); PG8_LDB(B1, 1, 1); PG8_SCHED; PG8_LDA(At, 1, 0); PG8_STAGE(PG8_SA(0, 1), a2 + hstep, voffA);
;             PG8_WAIT_V(8); PG8_WAIT_L(0); PG8_BAR; PG8_MMA(0, 0, At, B0); PG8_MMA(0, 1, At, B1); PG8_BAR; PG8_SCHED;
	s_add_i32 s70, 0, 0x18000
	v_add_u32_e32 v161, s70, v149
	s_add_i32 s71, 0, 0x1c000
	ds_read_b128 v[144:147], v161
	ds_read_b128 v[162:165], v161 offset:1024
	ds_read_b128 v[166:169], v161 offset:2048
	ds_read_b128 v[170:173], v161 offset:3072
	v_add_u32_e32 v161, s71, v149
	ds_read_b128 v[174:177], v161
	ds_read_b128 v[178:181], v161 offset:1024
	ds_read_b128 v[182:185], v161 offset:2048
	ds_read_b128 v[186:189], v161 offset:3072
	s_add_u32 s36, s36, 0x40000
	s_addc_u32 s37, s37, 0
	s_mov_b32 m0, s60
	v_lshl_add_u64 v[232:233], s[36:37], 0, v[0:1]
	ds_read_b128 v[190:193], v160 offset:32768
	ds_read_b128 v[194:197], v160 offset:33792
	ds_read_b128 v[212:215], v160 offset:34816
	ds_read_b128 v[216:219], v160 offset:35840
	ds_read_b128 v[220:223], v160 offset:36864
	ds_read_b128 v[224:227], v160 offset:37888
	ds_read_b128 v[228:231], v160 offset:38912
	ds_read_b128 v[242:245], v160 offset:39936
	global_load_lds_dwordx4 v[232:233], off
	v_lshl_add_u64 v[232:233], s[36:37], 0, v[134:135]
	s_mov_b32 m0, s62
	s_nop 0
	global_load_lds_dwordx4 v[232:233], off
	s_waitcnt vmcnt(8)
	s_waitcnt lgkmcnt(0)
	s_barrier
	s_setprio 1
	s_waitcnt lgkmcnt(0)
	v_mfma_f32_16x16x32_bf16 v[128:131], v[144:147], v[190:193], v[128:131]
	v_mfma_f32_16x16x32_bf16 v[120:123], v[166:169], v[190:193], v[120:123]
	v_mfma_f32_16x16x32_bf16 v[112:115], v[144:147], v[212:215], v[112:115]
	v_mfma_f32_16x16x32_bf16 v[104:107], v[166:169], v[212:215], v[104:107]
	v_mfma_f32_16x16x32_bf16 v[96:99], v[144:147], v[220:223], v[96:99]
	v_mfma_f32_16x16x32_bf16 v[88:91], v[166:169], v[220:223], v[88:91]
	v_mfma_f32_16x16x32_bf16 v[80:83], v[144:147], v[228:231], v[80:83]
	v_mfma_f32_16x16x32_bf16 v[72:75], v[166:169], v[228:231], v[72:75]
	v_mfma_f32_16x16x32_bf16 v[128:131], v[162:165], v[194:197], v[128:131]
	v_mfma_f32_16x16x32_bf16 v[120:123], v[170:173], v[194:197], v[120:123]
	v_mfma_f32_16x16x32_bf16 v[112:115], v[162:165], v[216:219], v[112:115]
	v_mfma_f32_16x16x32_bf16 v[104:107], v[170:173], v[216:219], v[104:107]
	v_mfma_f32_16x16x32_bf16 v[96:99], v[162:165], v[224:227], v[96:99]
	v_mfma_f32_16x16x32_bf16 v[88:91], v[170:173], v[224:227], v[88:91]
	v_mfma_f32_16x16x32_bf16 v[80:83], v[162:165], v[242:245], v[80:83]
	v_mfma_f32_16x16x32_bf16 v[72:75], v[170:173], v[242:245], v[72:75]
	s_setprio 0
	s_setprio 1
	v_mfma_f32_16x16x32_bf16 v[124:127], v[174:177], v[190:193], v[124:127]
	v_mfma_f32_16x16x32_bf16 v[116:119], v[182:185], v[190:193], v[116:119]
	v_mfma_f32_16x16x32_bf16 v[108:111], v[174:177], v[212:215], v[108:111]
	v_mfma_f32_16x16x32_bf16 v[100:103], v[182:185], v[212:215], v[100:103]
	v_mfma_f32_16x16x32_bf16 v[92:95], v[174:177], v[220:223], v[92:95]
	v_mfma_f32_16x16x32_bf16 v[84:87], v[182:185], v[220:223], v[84:87]
	v_mfma_f32_16x16x32_bf16 v[76:79], v[174:177], v[228:231], v[76:79]
	v_mfma_f32_16x16x32_bf16 v[68:71], v[182:185], v[228:231], v[68:71]
	v_mfma_f32_16x16x32_bf16 v[124:127], v[178:181], v[194:197], v[124:127]
	v_mfma_f32_16x16x32_bf16 v[116:119], v[186:189], v[194:197], v[116:119]
	v_mfma_f32_16x16x32_bf16 v[108:111], v[178:181], v[216:219], v[108:111]
	v_mfma_f32_16x16x32_bf16 v[100:103], v[186:189], v[216:219], v[100:103]
	v_mfma_f32_16x16x32_bf16 v[92:95], v[178:181], v[224:227], v[92:95]
	v_mfma_f32_16x16x32_bf16 v[84:87], v[186:189], v[224:227], v[84:87]
	v_mfma_f32_16x16x32_bf16 v[76:79], v[178:181], v[242:245], v[76:79]
	v_mfma_f32_16x16x32_bf16 v[68:71], v[186:189], v[242:245], v[68:71]
	s_setprio 0
	s_barrier
; #define PG8_STAGE(bufoff, gbase, voff) do { _Pragma("unroll") for (int _i = 0; _i < 2; ++_i) \
;         __builtin_amdgcn_global_load_lds((const unsigned*)((const char*)(gbase) + (voff)[_i]), (PG8_LAS unsigned*)(lds + (bufoff) + ldsw + _i * 8192), 16, 0, 0); } while (0)
; #define PG8_LDA(dst, b, h) do { _Pragma("unroll") for (int m = 0; m < 4; ++m) _Pragma("unroll") for (int k = 0; k < 2; ++k) dst[m][k] = *(const PG8_LAS bf16x8*)(lds + PG8_SA(b, h) + aoff + m * 2048 + k * 1024); } while (0)
; #define PG8_MMA(ai, bj, At, Bt) do { __builtin_amdgcn_s_setprio(1); _Pragma("unroll") for (int m = 0; m < 4; ++m) _Pragma("unroll") for (int n = 0; n < 2; ++n) _Pragma("unroll") for (int k = 0; k < 2; ++k) \
;         acc[ai][bj][m][n] = __builtin_amdgcn_mfma_f32_16x16x32_bf16(Bt[n][k], At[m][k], acc[ai][bj][m][n], 0, 0, 0); __builtin_amdgcn_s_setprio(0); } while (0)
; #define PG8_WAIT_V(n) asm volatile("s_waitcnt vmcnt(" #n ")" ::: "memory")
; #define PG8_WAIT_L(n) asm volatile("s_waitcnt lgkmcnt(" #n ")" ::: "memory")
; #define PG8_BAR __builtin_amdgcn_s_barrier()
; #define PG8_SCHED __builtin_amdgcn_sched_barrier(0)
; template <class Epi, class Sched, bool ALIGN_EPI = false, bool SP2 = false>
; __device__ __forceinline__ void gemm_phase(PG8_LAS unsigned char* lds, const Gemm g, const Sched& S, const Epi& E, const int tid) {
;     ...
;         for (int t = 0; t < nt; t += 2) {
;             const bool last = (t == nt - 2);
;             const char* a1 = cA + (size_t)(t + 1) * kstep;
;             const char* a2 = last ? nA : cA + (size_t)(t + 2) * kstep; const char* b2 = last ? nB : cB + (size_t)(t + 2) * kstep;
;             const char* a3 = a2 + kstep; const char* b3 = b2 + kstep;
;     ...
;             PG8_LDA(At, 1, 1); PG8_STAGE(PG8_SB(1, 0), b3, voffB); PG8_STAGE(PG8_SB(1, 1), b3, voffB1); PG8_STAGE(PG8_SA(1, 0), a3, voffA);
;             PG8_WAIT_V(8); PG8_WAIT_L(0); PG8_BAR; PG8_MMA(1, 0, At, B0); PG8_MMA(1, 1, At, B1); PG8_BAR; PG8_SCHED;
	s_add_i32 s36, s70, s48
	v_lshl_add_u64 v[198:199], v[198:199], 0, s[66:67]
	s_mov_b32 m0, s36
	ds_read_b128 v[190:193], v160 offset:49152
	ds_read_b128 v[194:197], v160 offset:50176
	ds_read_b128 v[212:215], v160 offset:51200
	ds_read_b128 v[216:219], v160 offset:52224
	ds_read_b128 v[220:223], v160 offset:53248
	ds_read_b128 v[224:227], v160 offset:54272
	ds_read_b128 v[228:231], v160 offset:55296
	ds_read_b128 v[242:245], v160 offset:56320
	global_load_lds_dwordx4 v[198:199], off
	v_lshl_add_u64 v[198:199], v[200:201], 0, s[66:67]
	s_add_i32 m0, s36, 0x2000
	s_add_i32 s36, s71, s48
	global_load_lds_dwordx4 v[198:199], off
	v_lshl_add_u64 v[198:199], v[202:203], 0, s[66:67]
	s_mov_b32 m0, s36
	s_nop 0
	global_load_lds_dwordx4 v[198:199], off
	v_lshl_add_u64 v[198:199], v[204:205], 0, s[66:67]
	s_add_i32 m0, s36, 0x2000
	s_nop 0
	global_load_lds_dwordx4 v[198:199], off
	v_lshl_add_u64 v[198:199], v[208:209], 0, s[66:67]
	s_mov_b32 m0, s63
	s_nop 0
	global_load_lds_dwordx4 v[198:199], off
	v_lshl_add_u64 v[198:199], v[210:211], 0, s[66:67]
	s_mov_b32 m0, s68
	s_nop 0
	global_load_lds_dwordx4 v[198:199], off
	s_waitcnt vmcnt(8)
	s_waitcnt lgkmcnt(0)
	s_barrier
	s_setprio 1
	s_waitcnt lgkmcnt(0)
	v_mfma_f32_16x16x32_bf16 v[64:67], v[144:147], v[190:193], v[64:67]
	v_mfma_f32_16x16x32_bf16 v[56:59], v[166:169], v[190:193], v[56:59]
	v_mfma_f32_16x16x32_bf16 v[48:51], v[144:147], v[212:215], v[48:51]
	v_mfma_f32_16x16x32_bf16 v[40:43], v[166:169], v[212:215], v[40:43]
	v_mfma_f32_16x16x32_bf16 v[32:35], v[144:147], v[220:223], v[32:35]
	v_mfma_f32_16x16x32_bf16 v[24:27], v[166:169], v[220:223], v[24:27]
	v_mfma_f32_16x16x32_bf16 v[16:19], v[144:147], v[228:231], v[16:19]
	v_mfma_f32_16x16x32_bf16 v[8:11], v[166:169], v[228:231], v[8:11]
	v_mfma_f32_16x16x32_bf16 v[64:67], v[162:165], v[194:197], v[64:67]
	s_add_i32 s59, s59, 2
	v_mfma_f32_16x16x32_bf16 v[56:59], v[170:173], v[194:197], v[56:59]
	s_add_u32 s54, s54, 0x100
	v_mfma_f32_16x16x32_bf16 v[48:51], v[162:165], v[216:219], v[48:51]
	s_addc_u32 s55, s55, 0
	v_mfma_f32_16x16x32_bf16 v[40:43], v[170:173], v[216:219], v[40:43]
	s_add_u32 s56, s56, 0x100
	v_mfma_f32_16x16x32_bf16 v[32:35], v[162:165], v[224:227], v[32:35]
	s_addc_u32 s57, s57, 0
	v_mfma_f32_16x16x32_bf16 v[24:27], v[170:173], v[224:227], v[24:27]
	s_add_u32 s36, s54, 0xfffc0080
	v_mfma_f32_16x16x32_bf16 v[16:19], v[162:165], v[242:245], v[16:19]
	s_addc_u32 s37, s55, -1
	v_mfma_f32_16x16x32_bf16 v[8:11], v[170:173], v[242:245], v[8:11]
	s_add_i32 s70, 0, 0x10000
	s_setprio 0
	s_setprio 1
	v_mfma_f32_16x16x32_bf16 v[60:63], v[174:177], v[190:193], v[60:63]
	s_cmp_eq_u32 s59, 12
	v_mfma_f32_16x16x32_bf16 v[52:55], v[182:185], v[190:193], v[52:55]
	s_cselect_b32 s37, s15, s37
	v_mfma_f32_16x16x32_bf16 v[44:47], v[174:177], v[212:215], v[44:47]
	s_cselect_b32 s36, s42, s36
	v_mfma_f32_16x16x32_bf16 v[36:39], v[182:185], v[212:215], v[36:39]
	s_cselect_b32 s73, s13, s57
	v_mfma_f32_16x16x32_bf16 v[28:31], v[174:177], v[220:223], v[28:31]
	s_cselect_b32 s72, s58, s56
	v_mfma_f32_16x16x32_bf16 v[20:23], v[182:185], v[220:223], v[20:23]
	s_add_i32 s71, 0, 0x14000
	v_mfma_f32_16x16x32_bf16 v[12:15], v[174:177], v[228:231], v[12:15]
	s_cmp_gt_u32 s59, 13
	v_mfma_f32_16x16x32_bf16 v[4:7], v[182:185], v[228:231], v[4:7]
	v_mfma_f32_16x16x32_bf16 v[60:63], v[178:181], v[194:197], v[60:63]
	v_mfma_f32_16x16x32_bf16 v[52:55], v[186:189], v[194:197], v[52:55]
	v_mfma_f32_16x16x32_bf16 v[44:47], v[178:181], v[216:219], v[44:47]
	v_mfma_f32_16x16x32_bf16 v[36:39], v[186:189], v[216:219], v[36:39]
	v_mfma_f32_16x16x32_bf16 v[28:31], v[178:181], v[224:227], v[28:31]
	v_mfma_f32_16x16x32_bf16 v[20:23], v[186:189], v[224:227], v[20:23]
	v_mfma_f32_16x16x32_bf16 v[12:15], v[178:181], v[242:245], v[12:15]
	v_mfma_f32_16x16x32_bf16 v[4:7], v[186:189], v[242:245], v[4:7]
	s_setprio 0
	s_barrier
	s_cbranch_scc0 .LBB0_101
	s_and_b64 vcc, exec, s[10:11]
	s_cbranch_vccz .LBB0_104
	s_barrier

; #define PG8_STAGE(bufoff, gbase, voff) do { _Pragma("unroll") for (int _i = 0; _i < 2; ++_i) \
;         __builtin_amdgcn_global_load_lds((const unsigned*)((const char*)(gbase) + (voff)[_i]), (PG8_LAS unsigned*)(lds + (bufoff) + ldsw + _i * 8192), 16, 0, 0); } while (0)
; #define PG8_LDA(dst, b, h) do { _Pragma("unroll") for (int m = 0; m < 4; ++m) _Pragma("unroll") for (int k = 0; k < 2; ++k) dst[m][k] = *(const PG8_LAS bf16x8*)(lds + PG8_SA(b, h) + aoff + m * 2048 + k * 1024); } while (0)
; #define PG8_LDB(dst, b, h) do { _Pragma("unroll") for (int n = 0; n < 2; ++n) _Pragma("unroll") for (int k = 0; k < 2; ++k) dst[n][k] = *(const PG8_LAS bf16x8*)(lds + PG8_SB(b, h) + boff + n * 2048 + k * 1024); } while (0)
; #define PG8_WAIT_V(n) asm volatile("s_waitcnt vmcnt(" #n ")" ::: "memory")
; #define PG8_WAIT_L(n) asm volatile("s_waitcnt lgkmcnt(" #n ")" ::: "memory")
; #define PG8_BAR __builtin_amdgcn_s_barrier()
; template <class Epi, class Sched, bool ALIGN_EPI = false, bool SP2 = false>
; __device__ __forceinline__ void gemm_phase(PG8_LAS unsigned char* lds, const Gemm g, const Sched& S, const Epi& E, const int tid) {
;     ...
;         const bool has_next = S.next(ui + 1, nxt);
;         const char* nA = has_next ? (const char*)g.A + (size_t)nxt.pm * tstep : cA; const char* nB = has_next ? (const char*)g.Bt + (size_t)nxt.pn * tstep : cB;
;         for (int t = 0; t < nt; t += 2) {
;             const bool last = (t == nt - 2);
;             const char* a1 = cA + (size_t)(t + 1) * kstep;
;             const char* a2 = last ? nA : cA + (size_t)(t + 2) * kstep; const char* b2 = last ? nB : cB + (size_t)(t + 2) * kstep;
;             const char* a3 = a2 + kstep; const char* b3 = b2 + kstep;
;             if (last && has_next) S.a_ready(nxt);
;             if constexpr (SP2) {
;             PG8_LDB(B0, 0, 0); PG8_LDB(B1, 0, 1); PG8_SCHED; PG8_LDA(At, 0, 0); PG8_STAGE(PG8_SA(1, 1), a1 + hstep, voffA);
;             PG8_WAIT_V(8); PG8_WAIT_L(0); PG8_BAR; PG8_MMA(0, 0, At, B0); PG8_MMA(0, 1, At, B1); PG8_BAR; PG8_SCHED;
;     ...
; #pragma unroll
;         for (int a = 0; a < 2; ++a)
; #pragma unroll
;             for (int b = 0; b < 2; ++b)
; #pragma unroll
;                 for (int m = 0; m < 4; ++m)
; #pragma unroll
;                     for (int n = 0; n < 2; ++n) acc[a][b][m][n] = (f32x4){0.f, 0.f, 0.f, 0.f};
;         cur = nxt; cA = nA; cB = nB; ++ui;
.LBB0_140:
	s_ashr_i32 s15, s14, 31
	s_lshl_b64 s[36:37], s[14:15], 19
	s_add_u32 s44, s33, s36
	s_addc_u32 s45, s38, s37
	s_and_b64 s[36:37], s[2:3], exec
	s_cselect_b32 s15, s45, s53
	s_cselect_b32 s59, s44, s52
	s_ashr_i32 s11, s10, 31
	s_lshl_b64 s[36:37], s[10:11], 19
	s_add_u32 s46, s39, s36
	s_addc_u32 s47, s43, s37
	s_and_b64 s[36:37], s[2:3], exec
	s_cselect_b32 s11, s47, s55
	s_cselect_b32 s60, s46, s54
	s_add_u32 s52, s52, 0x40080
	s_addc_u32 s53, s53, 0
	s_add_u32 s54, s54, 0x100
	v_mov_b32_e32 v4, 0
	s_addc_u32 s55, s55, 0
	s_mov_b32 s62, -2
	v_mov_b32_e32 v5, v4
	v_mov_b32_e32 v6, v4
	v_mov_b32_e32 v7, v4
	v_mov_b32_e32 v8, v4
	v_mov_b32_e32 v9, v4
	v_mov_b32_e32 v10, v4
	v_mov_b32_e32 v11, v4
	v_mov_b32_e32 v12, v4
	v_mov_b32_e32 v13, v4
	v_mov_b32_e32 v14, v4
	v_mov_b32_e32 v15, v4
	v_mov_b32_e32 v20, v4
	v_mov_b32_e32 v21, v4
	v_mov_b32_e32 v22, v4
	v_mov_b32_e32 v23, v4
	v_mov_b32_e32 v28, v4
	v_mov_b32_e32 v29, v4
	v_mov_b32_e32 v30, v4
	v_mov_b32_e32 v31, v4
	v_mov_b32_e32 v36, v4
	v_mov_b32_e32 v37, v4
	v_mov_b32_e32 v38, v4
	v_mov_b32_e32 v39, v4
	v_mov_b32_e32 v44, v4
	v_mov_b32_e32 v45, v4
	v_mov_b32_e32 v46, v4
	v_mov_b32_e32 v47, v4
	v_mov_b32_e32 v52, v4
	v_mov_b32_e32 v53, v4
	v_mov_b32_e32 v54, v4
	v_mov_b32_e32 v55, v4
	v_mov_b32_e32 v16, v4
	v_mov_b32_e32 v17, v4
	v_mov_b32_e32 v18, v4
	v_mov_b32_e32 v19, v4
	v_mov_b32_e32 v24, v4
	v_mov_b32_e32 v25, v4
	v_mov_b32_e32 v26, v4
	v_mov_b32_e32 v27, v4
	v_mov_b32_e32 v32, v4
	v_mov_b32_e32 v33, v4
	v_mov_b32_e32 v34, v4
	v_mov_b32_e32 v35, v4
	v_mov_b32_e32 v40, v4
	v_mov_b32_e32 v41, v4
	v_mov_b32_e32 v42, v4
	v_mov_b32_e32 v43, v4
	v_mov_b32_e32 v48, v4
	v_mov_b32_e32 v49, v4
	v_mov_b32_e32 v50, v4
	v_mov_b32_e32 v51, v4
	v_mov_b32_e32 v56, v4
	v_mov_b32_e32 v57, v4
	v_mov_b32_e32 v58, v4
	v_mov_b32_e32 v59, v4
	v_mov_b32_e32 v60, v4
	v_mov_b32_e32 v61, v4
	v_mov_b32_e32 v62, v4
	v_mov_b32_e32 v63, v4
	v_mov_b32_e32 v64, v4
	v_mov_b32_e32 v65, v4
	v_mov_b32_e32 v66, v4
	v_mov_b32_e32 v67, v4
	v_mov_b32_e32 v68, v4
	v_mov_b32_e32 v69, v4
	v_mov_b32_e32 v70, v4
	v_mov_b32_e32 v71, v4
	v_mov_b32_e32 v72, v4
	v_mov_b32_e32 v73, v4
	v_mov_b32_e32 v74, v4
	v_mov_b32_e32 v75, v4
	v_mov_b32_e32 v76, v4
	v_mov_b32_e32 v77, v4
	v_mov_b32_e32 v78, v4
	v_mov_b32_e32 v79, v4
	v_mov_b32_e32 v84, v4
	v_mov_b32_e32 v85, v4
	v_mov_b32_e32 v86, v4
	v_mov_b32_e32 v87, v4
	v_mov_b32_e32 v92, v4
	v_mov_b32_e32 v93, v4
	v_mov_b32_e32 v94, v4
	v_mov_b32_e32 v95, v4
	v_mov_b32_e32 v100, v4
	v_mov_b32_e32 v101, v4
	v_mov_b32_e32 v102, v4
	v_mov_b32_e32 v103, v4
	v_mov_b32_e32 v112, v4
	v_mov_b32_e32 v113, v4
	v_mov_b32_e32 v114, v4
	v_mov_b32_e32 v115, v4
	v_mov_b32_e32 v120, v4
	v_mov_b32_e32 v121, v4
	v_mov_b32_e32 v122, v4
	v_mov_b32_e32 v123, v4
	v_mov_b32_e32 v80, v4
	v_mov_b32_e32 v81, v4
	v_mov_b32_e32 v82, v4
	v_mov_b32_e32 v83, v4
	v_mov_b32_e32 v88, v4
	v_mov_b32_e32 v89, v4
	v_mov_b32_e32 v90, v4
	v_mov_b32_e32 v91, v4
	v_mov_b32_e32 v96, v4
	v_mov_b32_e32 v97, v4
	v_mov_b32_e32 v98, v4
	v_mov_b32_e32 v99, v4
	v_mov_b32_e32 v104, v4
	v_mov_b32_e32 v105, v4
	v_mov_b32_e32 v106, v4
	v_mov_b32_e32 v107, v4
	v_mov_b32_e32 v108, v4
	v_mov_b32_e32 v109, v4
	v_mov_b32_e32 v110, v4
	v_mov_b32_e32 v111, v4
	v_mov_b32_e32 v116, v4
	v_mov_b32_e32 v117, v4
	v_mov_b32_e32 v118, v4
	v_mov_b32_e32 v119, v4
	v_mov_b32_e32 v124, v4
	v_mov_b32_e32 v125, v4
	v_mov_b32_e32 v126, v4
	v_mov_b32_e32 v127, v4
	v_mov_b32_e32 v128, v4
	v_mov_b32_e32 v129, v4
	v_mov_b32_e32 v130, v4
	v_mov_b32_e32 v131, v4
	s_add_u32 s36, s52, 0xfffc0080
	s_addc_u32 s37, s53, -1
	s_add_i32 s63, 0, 0x10000
	s_cmp_eq_u32 s62, 12
	s_cselect_b32 s37, s15, s37
	s_cselect_b32 s36, s59, s36
	s_cselect_b32 s73, s11, s55
	s_cselect_b32 s72, s60, s54
	s_add_i32 s68, 0, 0x14000
.LBB0_141:
	v_add_u32_e32 v144, s63, v164
	v_add_u32_e32 v162, s68, v164
	ds_read_b128 v[132:135], v144
	ds_read_b128 v[136:139], v144 offset:1024
	ds_read_b128 v[140:143], v144 offset:2048
	ds_read_b128 v[144:147], v144 offset:3072
	ds_read_b128 v[168:171], v162
	ds_read_b128 v[172:175], v162 offset:1024
	ds_read_b128 v[176:179], v162 offset:2048
	ds_read_b128 v[180:183], v162 offset:3072
	v_lshl_add_u64 v[162:163], s[52:53], 0, v[158:159]
	s_add_i32 m0, s13, 0xc000
	ds_read_b128 v[184:187], v166
	ds_read_b128 v[188:191], v166 offset:1024
	ds_read_b128 v[192:195], v166 offset:2048
	ds_read_b128 v[196:199], v166 offset:3072
	ds_read_b128 v[212:215], v166 offset:4096
	ds_read_b128 v[216:219], v166 offset:5120
	ds_read_b128 v[220:223], v166 offset:6144
	ds_read_b128 v[224:227], v166 offset:7168
	global_load_lds_dwordx4 v[162:163], off
	v_lshl_add_u64 v[162:163], s[52:53], 0, v[160:161]
	s_add_i32 m0, s13, 0xe000
	s_nop 0
	global_load_lds_dwordx4 v[162:163], off
	s_waitcnt vmcnt(8)
	s_waitcnt lgkmcnt(0)
	s_barrier
; #define PG8_STAGE(bufoff, gbase, voff) do { _Pragma("unroll") for (int _i = 0; _i < 2; ++_i) \
;         __builtin_amdgcn_global_load_lds((const unsigned*)((const char*)(gbase) + (voff)[_i]), (PG8_LAS unsigned*)(lds + (bufoff) + ldsw + _i * 8192), 16, 0, 0); } while (0)
; #define PG8_LDA(dst, b, h) do { _Pragma("unroll") for (int m = 0; m < 4; ++m) _Pragma("unroll") for (int k = 0; k < 2; ++k) dst[m][k] = *(const PG8_LAS bf16x8*)(lds + PG8_SA(b, h) + aoff + m * 2048 + k * 1024); } while (0)
; #define PG8_MMA(ai, bj, At, Bt) do { __builtin_amdgcn_s_setprio(1); _Pragma("unroll") for (int m = 0; m < 4; ++m) _Pragma("unroll") for (int n = 0; n < 2; ++n) _Pragma("unroll") for (int k = 0; k < 2; ++k) \
;         acc[ai][bj][m][n] = __builtin_amdgcn_mfma_f32_16x16x32_bf16(Bt[n][k], At[m][k], acc[ai][bj][m][n], 0, 0, 0); __builtin_amdgcn_s_setprio(0); } while (0)
; #define PG8_WAIT_V(n) asm volatile("s_waitcnt vmcnt(" #n ")" ::: "memory")
; #define PG8_WAIT_L(n) asm volatile("s_waitcnt lgkmcnt(" #n ")" ::: "memory")
; #define PG8_BAR __builtin_amdgcn_s_barrier()
; #define PG8_SCHED __builtin_amdgcn_sched_barrier(0)
; template <class Epi, class Sched, bool ALIGN_EPI = false, bool SP2 = false>
; __device__ __forceinline__ void gemm_phase(PG8_LAS unsigned char* lds, const Gemm g, const Sched& S, const Epi& E, const int tid) {
;     ...
;             PG8_WAIT_V(8); PG8_WAIT_L(0); PG8_BAR; PG8_MMA(0, 0, At, B0); PG8_MMA(0, 1, At, B1); PG8_BAR; PG8_SCHED;
;             PG8_LDA(At, 0, 1); PG8_STAGE(PG8_SB(0, 0), b2, voffB); PG8_STAGE(PG8_SB(0, 1), b2, voffB1); PG8_STAGE(PG8_SA(0, 0), a2, voffA);
;             PG8_WAIT_V(8); PG8_WAIT_L(0); PG8_BAR; PG8_MMA(1, 0, At, B0); PG8_MMA(1, 1, At, B1); PG8_BAR; PG8_SCHED;
	s_setprio 1
	s_waitcnt lgkmcnt(0)
	v_mfma_f32_16x16x32_bf16 v[128:131], v[132:135], v[184:187], v[128:131]
	v_mfma_f32_16x16x32_bf16 v[124:127], v[140:143], v[184:187], v[124:127]
	v_mfma_f32_16x16x32_bf16 v[116:119], v[132:135], v[192:195], v[116:119]
	v_mfma_f32_16x16x32_bf16 v[108:111], v[140:143], v[192:195], v[108:111]
	v_mfma_f32_16x16x32_bf16 v[104:107], v[132:135], v[212:215], v[104:107]
	v_mfma_f32_16x16x32_bf16 v[96:99], v[140:143], v[212:215], v[96:99]
	v_mfma_f32_16x16x32_bf16 v[88:91], v[132:135], v[220:223], v[88:91]
	v_mfma_f32_16x16x32_bf16 v[80:83], v[140:143], v[220:223], v[80:83]
	v_mfma_f32_16x16x32_bf16 v[128:131], v[136:139], v[188:191], v[128:131]
	v_mfma_f32_16x16x32_bf16 v[124:127], v[144:147], v[188:191], v[124:127]
	v_mfma_f32_16x16x32_bf16 v[116:119], v[136:139], v[196:199], v[116:119]
	v_mfma_f32_16x16x32_bf16 v[108:111], v[144:147], v[196:199], v[108:111]
	v_mfma_f32_16x16x32_bf16 v[104:107], v[136:139], v[216:219], v[104:107]
	v_mfma_f32_16x16x32_bf16 v[96:99], v[144:147], v[216:219], v[96:99]
	v_mfma_f32_16x16x32_bf16 v[88:91], v[136:139], v[224:227], v[88:91]
	v_mfma_f32_16x16x32_bf16 v[80:83], v[144:147], v[224:227], v[80:83]
	s_setprio 0
	s_setprio 1
	v_mfma_f32_16x16x32_bf16 v[120:123], v[168:171], v[184:187], v[120:123]
	v_mfma_f32_16x16x32_bf16 v[112:115], v[176:179], v[184:187], v[112:115]
	v_mfma_f32_16x16x32_bf16 v[100:103], v[168:171], v[192:195], v[100:103]
	v_mfma_f32_16x16x32_bf16 v[92:95], v[176:179], v[192:195], v[92:95]
	v_mfma_f32_16x16x32_bf16 v[84:87], v[168:171], v[212:215], v[84:87]
	v_mfma_f32_16x16x32_bf16 v[76:79], v[176:179], v[212:215], v[76:79]
	v_mfma_f32_16x16x32_bf16 v[72:75], v[168:171], v[220:223], v[72:75]
	v_mfma_f32_16x16x32_bf16 v[68:71], v[176:179], v[220:223], v[68:71]
	v_mfma_f32_16x16x32_bf16 v[120:123], v[172:175], v[188:191], v[120:123]
	v_mfma_f32_16x16x32_bf16 v[112:115], v[180:183], v[188:191], v[112:115]
	v_mfma_f32_16x16x32_bf16 v[100:103], v[172:175], v[196:199], v[100:103]
	v_mfma_f32_16x16x32_bf16 v[92:95], v[180:183], v[196:199], v[92:95]
	v_mfma_f32_16x16x32_bf16 v[84:87], v[172:175], v[216:219], v[84:87]
	v_mfma_f32_16x16x32_bf16 v[76:79], v[180:183], v[216:219], v[76:79]
	v_mfma_f32_16x16x32_bf16 v[72:75], v[172:175], v[224:227], v[72:75]
	v_mfma_f32_16x16x32_bf16 v[68:71], v[180:183], v[224:227], v[68:71]
	s_setprio 0
	s_barrier
	s_add_i32 s63, s63, s1
	v_lshl_add_u64 v[162:163], s[72:73], 0, v[2:3]
	s_mov_b32 m0, s63
	ds_read_b128 v[184:187], v166 offset:16384
	ds_read_b128 v[188:191], v166 offset:17408
	ds_read_b128 v[192:195], v166 offset:18432
	ds_read_b128 v[196:199], v166 offset:19456
	ds_read_b128 v[212:215], v166 offset:20480
	ds_read_b128 v[216:219], v166 offset:21504
	ds_read_b128 v[220:223], v166 offset:22528
	ds_read_b128 v[224:227], v166 offset:23552
	global_load_lds_dwordx4 v[162:163], off
	v_lshl_add_u64 v[200:201], s[72:73], 0, v[152:153]
	s_add_i32 m0, s63, 0x2000
	s_add_i32 s63, s68, s1
	global_load_lds_dwordx4 v[200:201], off
	v_lshl_add_u64 v[202:203], s[72:73], 0, v[148:149]
	s_mov_b32 m0, s63
	v_lshl_add_u64 v[204:205], s[72:73], 0, v[154:155]
	global_load_lds_dwordx4 v[202:203], off
	s_add_i32 m0, s63, 0x2000
	v_lshl_add_u64 v[208:209], s[36:37], 0, v[0:1]
	global_load_lds_dwordx4 v[204:205], off
	s_mov_b32 m0, s13
	v_lshl_add_u64 v[210:211], s[36:37], 0, v[150:151]
	global_load_lds_dwordx4 v[208:209], off
	s_mov_b32 m0, s40
	s_nop 0
	global_load_lds_dwordx4 v[210:211], off
	s_waitcnt vmcnt(8)
	s_waitcnt lgkmcnt(0)
	s_barrier
	s_setprio 1
	s_waitcnt lgkmcnt(0)
	v_mfma_f32_16x16x32_bf16 v[64:67], v[132:135], v[184:187], v[64:67]
	v_mfma_f32_16x16x32_bf16 v[60:63], v[140:143], v[184:187], v[60:63]
	v_mfma_f32_16x16x32_bf16 v[56:59], v[132:135], v[192:195], v[56:59]
	v_mfma_f32_16x16x32_bf16 v[48:51], v[140:143], v[192:195], v[48:51]
	v_mfma_f32_16x16x32_bf16 v[40:43], v[132:135], v[212:215], v[40:43]
	v_mfma_f32_16x16x32_bf16 v[32:35], v[140:143], v[212:215], v[32:35]
	v_mfma_f32_16x16x32_bf16 v[24:27], v[132:135], v[220:223], v[24:27]
	v_mfma_f32_16x16x32_bf16 v[16:19], v[140:143], v[220:223], v[16:19]
	v_mfma_f32_16x16x32_bf16 v[64:67], v[136:139], v[188:191], v[64:67]
	v_mfma_f32_16x16x32_bf16 v[60:63], v[144:147], v[188:191], v[60:63]
	v_mfma_f32_16x16x32_bf16 v[56:59], v[136:139], v[196:199], v[56:59]
	v_mfma_f32_16x16x32_bf16 v[48:51], v[144:147], v[196:199], v[48:51]
	v_mfma_f32_16x16x32_bf16 v[40:43], v[136:139], v[216:219], v[40:43]
	v_mfma_f32_16x16x32_bf16 v[32:35], v[144:147], v[216:219], v[32:35]
	v_mfma_f32_16x16x32_bf16 v[24:27], v[136:139], v[224:227], v[24:27]
	v_mfma_f32_16x16x32_bf16 v[16:19], v[144:147], v[224:227], v[16:19]
	s_setprio 0
	s_setprio 1
	v_mfma_f32_16x16x32_bf16 v[52:55], v[168:171], v[184:187], v[52:55]
	v_mfma_f32_16x16x32_bf16 v[44:47], v[176:179], v[184:187], v[44:47]
	v_mfma_f32_16x16x32_bf16 v[36:39], v[168:171], v[192:195], v[36:39]
	v_mfma_f32_16x16x32_bf16 v[28:31], v[176:179], v[192:195], v[28:31]
	v_mfma_f32_16x16x32_bf16 v[20:23], v[168:171], v[212:215], v[20:23]
	v_mfma_f32_16x16x32_bf16 v[12:15], v[176:179], v[212:215], v[12:15]
	v_mfma_f32_16x16x32_bf16 v[8:11], v[168:171], v[220:223], v[8:11]
	v_mfma_f32_16x16x32_bf16 v[4:7], v[176:179], v[220:223], v[4:7]
	v_mfma_f32_16x16x32_bf16 v[52:55], v[172:175], v[188:191], v[52:55]
	v_mfma_f32_16x16x32_bf16 v[44:47], v[180:183], v[188:191], v[44:47]
	v_mfma_f32_16x16x32_bf16 v[36:39], v[172:175], v[196:199], v[36:39]
	v_mfma_f32_16x16x32_bf16 v[28:31], v[180:183], v[196:199], v[28:31]
	v_mfma_f32_16x16x32_bf16 v[20:23], v[172:175], v[216:219], v[20:23]
	v_mfma_f32_16x16x32_bf16 v[12:15], v[180:183], v[216:219], v[12:15]
	v_mfma_f32_16x16x32_bf16 v[8:11], v[172:175], v[224:227], v[8:11]
	v_mfma_f32_16x16x32_bf16 v[4:7], v[180:183], v[224:227], v[4:7]
	s_setprio 0
	s_barrier
; #define PG8_STAGE(bufoff, gbase, voff) do { _Pragma("unroll") for (int _i = 0; _i < 2; ++_i) \
;         __builtin_amdgcn_global_load_lds((const unsigned*)((const char*)(gbase) + (voff)[_i]), (PG8_LAS unsigned*)(lds + (bufoff) + ldsw + _i * 8192), 16, 0, 0); } while (0)
; #define PG8_LDA(dst, b, h) do { _Pragma("unroll") for (int m = 0; m < 4; ++m) _Pragma("unroll") for (int k = 0; k < 2; ++k) dst[m][k] = *(const PG8_LAS bf16x8*)(lds + PG8_SA(b, h) + aoff + m * 2048 + k * 1024); } while (0)
; #define PG8_LDB(dst, b, h) do { _Pragma("unroll") for (int n = 0; n < 2; ++n) _Pragma("unroll") for (int k = 0; k < 2; ++k) dst[n][k] = *(const PG8_LAS bf16x8*)(lds + PG8_SB(b, h) + boff + n * 2048 + k * 1024); } while (0)
; #define PG8_MMA(ai, bj, At, Bt) do { __builtin_amdgcn_s_setprio(1); _Pragma("unroll") for (int m = 0; m < 4; ++m) _Pragma("unroll") for (int n = 0; n < 2; ++n) _Pragma("unroll") for (int k = 0; k < 2; ++k) \
;         acc[ai][bj][m][n] = __builtin_amdgcn_mfma_f32_16x16x32_bf16(Bt[n][k], At[m][k], acc[ai][bj][m][n], 0, 0, 0); __builtin_amdgcn_s_setprio(0); } while (0)
; #define PG8_WAIT_V(n) asm volatile("s_waitcnt vmcnt(" #n ")" ::: "memory")
; #define PG8_WAIT_L(n) asm volatile("s_waitcnt lgkmcnt(" #n ")" ::: "memory")
; #define PG8_BAR __builtin_amdgcn_s_barrier()
; #define PG8_SCHED __builtin_amdgcn_sched_barrier(0)
; template <class Epi, class Sched, bool ALIGN_EPI = false, bool SP2 = false>
; __device__ __forceinline__ void gemm_phase(PG8_LAS unsigned char* lds, const Gemm g, const Sched& S, const Epi& E, const int tid) {
;     ...
;             PG8_LDB(B0, 1, 0); PG8_LDB(B1, 1, 1); PG8_SCHED; PG8_LDA(At, 1, 0); PG8_STAGE(PG8_SA(0, 1), a2 + hstep, voffA);
;             PG8_WAIT_V(8); PG8_WAIT_L(0); PG8_BAR; PG8_MMA(0, 0, At, B0); PG8_MMA(0, 1, At, B1); PG8_BAR; PG8_SCHED;
	s_add_i32 s63, 0, 0x18000
	s_add_i32 s68, 0, 0x1c000
	v_add_u32_e32 v144, s63, v164
	v_add_u32_e32 v167, s68, v164
	ds_read_b128 v[132:135], v144
	ds_read_b128 v[136:139], v144 offset:1024
	ds_read_b128 v[140:143], v144 offset:2048
	ds_read_b128 v[144:147], v144 offset:3072
	ds_read_b128 v[168:171], v167
	ds_read_b128 v[172:175], v167 offset:1024
	ds_read_b128 v[176:179], v167 offset:2048
	ds_read_b128 v[180:183], v167 offset:3072
	s_add_u32 s36, s36, 0x40000
	s_addc_u32 s37, s37, 0
	s_mov_b32 m0, s41
	v_lshl_add_u64 v[228:229], s[36:37], 0, v[0:1]
	ds_read_b128 v[184:187], v166 offset:32768
	ds_read_b128 v[188:191], v166 offset:33792
	ds_read_b128 v[192:195], v166 offset:34816
	ds_read_b128 v[196:199], v166 offset:35840
	ds_read_b128 v[212:215], v166 offset:36864
	ds_read_b128 v[216:219], v166 offset:37888
	ds_read_b128 v[220:223], v166 offset:38912
	ds_read_b128 v[224:227], v166 offset:39936
	global_load_lds_dwordx4 v[228:229], off
	v_lshl_add_u64 v[228:229], s[36:37], 0, v[150:151]
	s_mov_b32 m0, s42
	s_nop 0
	global_load_lds_dwordx4 v[228:229], off
	s_waitcnt vmcnt(8)
	s_waitcnt lgkmcnt(0)
	s_barrier
	s_setprio 1
	s_waitcnt lgkmcnt(0)
	v_mfma_f32_16x16x32_bf16 v[128:131], v[132:135], v[184:187], v[128:131]
	v_mfma_f32_16x16x32_bf16 v[124:127], v[140:143], v[184:187], v[124:127]
	v_mfma_f32_16x16x32_bf16 v[116:119], v[132:135], v[192:195], v[116:119]
	v_mfma_f32_16x16x32_bf16 v[108:111], v[140:143], v[192:195], v[108:111]
	v_mfma_f32_16x16x32_bf16 v[104:107], v[132:135], v[212:215], v[104:107]
	v_mfma_f32_16x16x32_bf16 v[96:99], v[140:143], v[212:215], v[96:99]
	v_mfma_f32_16x16x32_bf16 v[88:91], v[132:135], v[220:223], v[88:91]
	v_mfma_f32_16x16x32_bf16 v[80:83], v[140:143], v[220:223], v[80:83]
	v_mfma_f32_16x16x32_bf16 v[128:131], v[136:139], v[188:191], v[128:131]
	v_mfma_f32_16x16x32_bf16 v[124:127], v[144:147], v[188:191], v[124:127]
	v_mfma_f32_16x16x32_bf16 v[116:119], v[136:139], v[196:199], v[116:119]
	v_mfma_f32_16x16x32_bf16 v[108:111], v[144:147], v[196:199], v[108:111]
	v_mfma_f32_16x16x32_bf16 v[104:107], v[136:139], v[216:219], v[104:107]
	v_mfma_f32_16x16x32_bf16 v[96:99], v[144:147], v[216:219], v[96:99]
	v_mfma_f32_16x16x32_bf16 v[88:91], v[136:139], v[224:227], v[88:91]
	v_mfma_f32_16x16x32_bf16 v[80:83], v[144:147], v[224:227], v[80:83]
	s_setprio 0
	s_setprio 1
	v_mfma_f32_16x16x32_bf16 v[120:123], v[168:171], v[184:187], v[120:123]
	v_mfma_f32_16x16x32_bf16 v[112:115], v[176:179], v[184:187], v[112:115]
	v_mfma_f32_16x16x32_bf16 v[100:103], v[168:171], v[192:195], v[100:103]
	v_mfma_f32_16x16x32_bf16 v[92:95], v[176:179], v[192:195], v[92:95]
	v_mfma_f32_16x16x32_bf16 v[84:87], v[168:171], v[212:215], v[84:87]
	v_mfma_f32_16x16x32_bf16 v[76:79], v[176:179], v[212:215], v[76:79]
	v_mfma_f32_16x16x32_bf16 v[72:75], v[168:171], v[220:223], v[72:75]
	v_mfma_f32_16x16x32_bf16 v[68:71], v[176:179], v[220:223], v[68:71]
	v_mfma_f32_16x16x32_bf16 v[120:123], v[172:175], v[188:191], v[120:123]
	v_mfma_f32_16x16x32_bf16 v[112:115], v[180:183], v[188:191], v[112:115]
	v_mfma_f32_16x16x32_bf16 v[100:103], v[172:175], v[196:199], v[100:103]
	v_mfma_f32_16x16x32_bf16 v[92:95], v[180:183], v[196:199], v[92:95]
	v_mfma_f32_16x16x32_bf16 v[84:87], v[172:175], v[216:219], v[84:87]
	v_mfma_f32_16x16x32_bf16 v[76:79], v[180:183], v[216:219], v[76:79]
	v_mfma_f32_16x16x32_bf16 v[72:75], v[172:175], v[224:227], v[72:75]
	v_mfma_f32_16x16x32_bf16 v[68:71], v[180:183], v[224:227], v[68:71]
	s_setprio 0
	s_barrier
; #define PG8_STAGE(bufoff, gbase, voff) do { _Pragma("unroll") for (int _i = 0; _i < 2; ++_i) \
;         __builtin_amdgcn_global_load_lds((const unsigned*)((const char*)(gbase) + (voff)[_i]), (PG8_LAS unsigned*)(lds + (bufoff) + ldsw + _i * 8192), 16, 0, 0); } while (0)
; #define PG8_LDA(dst, b, h) do { _Pragma("unroll") for (int m = 0; m < 4; ++m) _Pragma("unroll") for (int k = 0; k < 2; ++k) dst[m][k] = *(const PG8_LAS bf16x8*)(lds + PG8_SA(b, h) + aoff + m * 2048 + k * 1024); } while (0)
; #define PG8_MMA(ai, bj, At, Bt) do { __builtin_amdgcn_s_setprio(1); _Pragma("unroll") for (int m = 0; m < 4; ++m) _Pragma("unroll") for (int n = 0; n < 2; ++n) _Pragma("unroll") for (int k = 0; k < 2; ++k) \
;         acc[ai][bj][m][n] = __builtin_amdgcn_mfma_f32_16x16x32_bf16(Bt[n][k], At[m][k], acc[ai][bj][m][n], 0, 0, 0); __builtin_amdgcn_s_setprio(0); } while (0)
; #define PG8_WAIT_V(n) asm volatile("s_waitcnt vmcnt(" #n ")" ::: "memory")
; #define PG8_WAIT_L(n) asm volatile("s_waitcnt lgkmcnt(" #n ")" ::: "memory")
; #define PG8_BAR __builtin_amdgcn_s_barrier()
; #define PG8_SCHED __builtin_amdgcn_sched_barrier(0)
; template <class Epi, class Sched, bool ALIGN_EPI = false, bool SP2 = false>
; __device__ __forceinline__ void gemm_phase(PG8_LAS unsigned char* lds, const Gemm g, const Sched& S, const Epi& E, const int tid) {
;     ...
;         for (int t = 0; t < nt; t += 2) {
;             const bool last = (t == nt - 2);
;             const char* a1 = cA + (size_t)(t + 1) * kstep;
;             const char* a2 = last ? nA : cA + (size_t)(t + 2) * kstep; const char* b2 = last ? nB : cB + (size_t)(t + 2) * kstep;
;             const char* a3 = a2 + kstep; const char* b3 = b2 + kstep;
;     ...
;             PG8_LDA(At, 1, 1); PG8_STAGE(PG8_SB(1, 0), b3, voffB); PG8_STAGE(PG8_SB(1, 1), b3, voffB1); PG8_STAGE(PG8_SA(1, 0), a3, voffA);
;             PG8_WAIT_V(8); PG8_WAIT_L(0); PG8_BAR; PG8_MMA(1, 0, At, B0); PG8_MMA(1, 1, At, B1); PG8_BAR; PG8_SCHED;
	s_add_i32 s36, s63, s1
	v_lshl_add_u64 v[162:163], v[162:163], 0, s[66:67]
	s_mov_b32 m0, s36
	ds_read_b128 v[184:187], v166 offset:49152
	ds_read_b128 v[188:191], v166 offset:50176
	ds_read_b128 v[192:195], v166 offset:51200
	ds_read_b128 v[196:199], v166 offset:52224
	ds_read_b128 v[212:215], v166 offset:53248
	ds_read_b128 v[216:219], v166 offset:54272
	ds_read_b128 v[220:223], v166 offset:55296
	ds_read_b128 v[224:227], v166 offset:56320
	global_load_lds_dwordx4 v[162:163], off
	v_lshl_add_u64 v[162:163], v[200:201], 0, s[66:67]
	s_add_i32 m0, s36, 0x2000
	s_add_i32 s36, s68, s1
	global_load_lds_dwordx4 v[162:163], off
	v_lshl_add_u64 v[162:163], v[202:203], 0, s[66:67]
	s_mov_b32 m0, s36
	s_nop 0
	global_load_lds_dwordx4 v[162:163], off
	v_lshl_add_u64 v[162:163], v[204:205], 0, s[66:67]
	s_add_i32 m0, s36, 0x2000
	s_nop 0
	global_load_lds_dwordx4 v[162:163], off
	v_lshl_add_u64 v[162:163], v[208:209], 0, s[66:67]
	s_mov_b32 m0, s48
	s_nop 0
	global_load_lds_dwordx4 v[162:163], off
	v_lshl_add_u64 v[162:163], v[210:211], 0, s[66:67]
	s_mov_b32 m0, s49
	s_nop 0
	global_load_lds_dwordx4 v[162:163], off
	s_waitcnt vmcnt(8)
	s_waitcnt lgkmcnt(0)
	s_barrier
	s_setprio 1
	s_waitcnt lgkmcnt(0)
	v_mfma_f32_16x16x32_bf16 v[64:67], v[132:135], v[184:187], v[64:67]
	v_mfma_f32_16x16x32_bf16 v[60:63], v[140:143], v[184:187], v[60:63]
	v_mfma_f32_16x16x32_bf16 v[56:59], v[132:135], v[192:195], v[56:59]
	v_mfma_f32_16x16x32_bf16 v[48:51], v[140:143], v[192:195], v[48:51]
	v_mfma_f32_16x16x32_bf16 v[40:43], v[132:135], v[212:215], v[40:43]
	v_mfma_f32_16x16x32_bf16 v[32:35], v[140:143], v[212:215], v[32:35]
	v_mfma_f32_16x16x32_bf16 v[24:27], v[132:135], v[220:223], v[24:27]
	v_mfma_f32_16x16x32_bf16 v[16:19], v[140:143], v[220:223], v[16:19]
	v_mfma_f32_16x16x32_bf16 v[64:67], v[136:139], v[188:191], v[64:67]
	s_add_i32 s62, s62, 2
	v_mfma_f32_16x16x32_bf16 v[60:63], v[144:147], v[188:191], v[60:63]
	s_add_u32 s52, s52, 0x100
	v_mfma_f32_16x16x32_bf16 v[56:59], v[136:139], v[196:199], v[56:59]
	s_addc_u32 s53, s53, 0
	v_mfma_f32_16x16x32_bf16 v[48:51], v[144:147], v[196:199], v[48:51]
	s_add_u32 s54, s54, 0x100
	v_mfma_f32_16x16x32_bf16 v[40:43], v[136:139], v[216:219], v[40:43]
	s_addc_u32 s55, s55, 0
	v_mfma_f32_16x16x32_bf16 v[32:35], v[144:147], v[216:219], v[32:35]
	s_add_u32 s36, s52, 0xfffc0080
	v_mfma_f32_16x16x32_bf16 v[24:27], v[136:139], v[224:227], v[24:27]
	s_addc_u32 s37, s53, -1
	v_mfma_f32_16x16x32_bf16 v[16:19], v[144:147], v[224:227], v[16:19]
	s_add_i32 s63, 0, 0x10000
	s_setprio 0
	s_setprio 1
	v_mfma_f32_16x16x32_bf16 v[52:55], v[168:171], v[184:187], v[52:55]
	s_cmp_eq_u32 s62, 12
	v_mfma_f32_16x16x32_bf16 v[44:47], v[176:179], v[184:187], v[44:47]
	s_cselect_b32 s37, s15, s37
	v_mfma_f32_16x16x32_bf16 v[36:39], v[168:171], v[192:195], v[36:39]
	s_cselect_b32 s36, s59, s36
	v_mfma_f32_16x16x32_bf16 v[28:31], v[176:179], v[192:195], v[28:31]
	s_cselect_b32 s73, s11, s55
	v_mfma_f32_16x16x32_bf16 v[20:23], v[168:171], v[212:215], v[20:23]
	s_cselect_b32 s72, s60, s54
	v_mfma_f32_16x16x32_bf16 v[12:15], v[176:179], v[212:215], v[12:15]
	s_add_i32 s68, 0, 0x14000
	v_mfma_f32_16x16x32_bf16 v[8:11], v[168:171], v[220:223], v[8:11]
	s_cmp_gt_u32 s62, 13
	v_mfma_f32_16x16x32_bf16 v[4:7], v[176:179], v[220:223], v[4:7]
	v_mfma_f32_16x16x32_bf16 v[52:55], v[172:175], v[188:191], v[52:55]
	v_mfma_f32_16x16x32_bf16 v[44:47], v[180:183], v[188:191], v[44:47]
	v_mfma_f32_16x16x32_bf16 v[36:39], v[172:175], v[196:199], v[36:39]
	v_mfma_f32_16x16x32_bf16 v[28:31], v[180:183], v[196:199], v[28:31]
	v_mfma_f32_16x16x32_bf16 v[20:23], v[172:175], v[216:219], v[20:23]
	v_mfma_f32_16x16x32_bf16 v[12:15], v[180:183], v[216:219], v[12:15]
	v_mfma_f32_16x16x32_bf16 v[8:11], v[172:175], v[224:227], v[8:11]
	v_mfma_f32_16x16x32_bf16 v[4:7], v[180:183], v[224:227], v[4:7]
	s_setprio 0
	s_barrier
	s_cbranch_scc0 .LBB0_141
	s_and_b64 vcc, exec, s[8:9]
	s_cbranch_vccz .LBB0_144
	s_barrier

; template <class Epi, class Sched, bool ALIGN_EPI = false, bool SP2 = false>
; __device__ __forceinline__ void gemm_phase(PG8_LAS unsigned char* lds, const Gemm g, const Sched& S, const Epi& E, const int tid) {
;     ...
;         const bool has_next = S.next(ui + 1, nxt);
;         const char* nA = has_next ? (const char*)g.A + (size_t)nxt.pm * tstep : cA; const char* nB = has_next ? (const char*)g.Bt + (size_t)nxt.pn * tstep : cB;
;         for (int t = 0; t < nt; t += 2) {
;             const bool last = (t == nt - 2);
;             const char* a1 = cA + (size_t)(t + 1) * kstep;
;             const char* a2 = last ? nA : cA + (size_t)(t + 2) * kstep; const char* b2 = last ? nB : cB + (size_t)(t + 2) * kstep;
;             const char* a3 = a2 + kstep; const char* b3 = b2 + kstep;
;     ...
; #pragma unroll
;         for (int a = 0; a < 2; ++a)
; #pragma unroll
;             for (int b = 0; b < 2; ++b)
; #pragma unroll
;                 for (int m = 0; m < 4; ++m)
; #pragma unroll
;                     for (int n = 0; n < 2; ++n) acc[a][b][m][n] = (f32x4){0.f, 0.f, 0.f, 0.f};
;         cur = nxt; cA = nA; cB = nB; ++ui;
.LBB0_298:
	s_ashr_i32 s11, s10, 31
	s_lshl_b64 s[12:13], s[10:11], 19
	s_add_u32 s12, s1, s12
	s_addc_u32 s13, s33, s13
	s_and_b64 s[14:15], s[2:3], exec
	s_cselect_b32 s11, s13, s47
	s_cselect_b32 s68, s12, s46
	s_ashr_i32 s9, s8, 31
	s_lshl_b64 s[14:15], s[8:9], 19
	s_add_u32 s14, s38, s14
	s_addc_u32 s15, s39, s15
	s_and_b64 s[36:37], s[2:3], exec
	s_cselect_b32 s9, s15, s53
	s_cselect_b32 s72, s14, s52
	s_add_u32 s46, s46, 0x40080
	s_addc_u32 s47, s47, 0
	s_add_u32 s52, s52, 0x100
	v_mov_b32_e32 v4, 0
	s_addc_u32 s53, s53, 0
	s_mov_b32 s73, -2
	v_mov_b32_e32 v5, v4
	v_mov_b32_e32 v6, v4
	v_mov_b32_e32 v7, v4
	v_mov_b32_e32 v8, v4
	v_mov_b32_e32 v9, v4
	v_mov_b32_e32 v10, v4
	v_mov_b32_e32 v11, v4
	v_mov_b32_e32 v20, v4
	v_mov_b32_e32 v21, v4
	v_mov_b32_e32 v22, v4
	v_mov_b32_e32 v23, v4
	v_mov_b32_e32 v24, v4
	v_mov_b32_e32 v25, v4
	v_mov_b32_e32 v26, v4
	v_mov_b32_e32 v27, v4
	v_mov_b32_e32 v36, v4
	v_mov_b32_e32 v37, v4
	v_mov_b32_e32 v38, v4
	v_mov_b32_e32 v39, v4
	v_mov_b32_e32 v40, v4
	v_mov_b32_e32 v41, v4
	v_mov_b32_e32 v42, v4
	v_mov_b32_e32 v43, v4
	v_mov_b32_e32 v52, v4
	v_mov_b32_e32 v53, v4
	v_mov_b32_e32 v54, v4
	v_mov_b32_e32 v55, v4
	v_mov_b32_e32 v56, v4
	v_mov_b32_e32 v57, v4
	v_mov_b32_e32 v58, v4
	v_mov_b32_e32 v59, v4
	v_mov_b32_e32 v12, v4
	v_mov_b32_e32 v13, v4
	v_mov_b32_e32 v14, v4
	v_mov_b32_e32 v15, v4
	v_mov_b32_e32 v16, v4
	v_mov_b32_e32 v17, v4
	v_mov_b32_e32 v18, v4
	v_mov_b32_e32 v19, v4
	v_mov_b32_e32 v28, v4
	v_mov_b32_e32 v29, v4
	v_mov_b32_e32 v30, v4
	v_mov_b32_e32 v31, v4
	v_mov_b32_e32 v32, v4
	v_mov_b32_e32 v33, v4
	v_mov_b32_e32 v34, v4
	v_mov_b32_e32 v35, v4
	v_mov_b32_e32 v44, v4
	v_mov_b32_e32 v45, v4
	v_mov_b32_e32 v46, v4
	v_mov_b32_e32 v47, v4
	v_mov_b32_e32 v48, v4
	v_mov_b32_e32 v49, v4
	v_mov_b32_e32 v50, v4
	v_mov_b32_e32 v51, v4
	v_mov_b32_e32 v60, v4
	v_mov_b32_e32 v61, v4
	v_mov_b32_e32 v62, v4
	v_mov_b32_e32 v63, v4
	v_mov_b32_e32 v64, v4
	v_mov_b32_e32 v65, v4
	v_mov_b32_e32 v66, v4
	v_mov_b32_e32 v67, v4
	v_mov_b32_e32 v68, v4
	v_mov_b32_e32 v69, v4
	v_mov_b32_e32 v70, v4
	v_mov_b32_e32 v71, v4
	v_mov_b32_e32 v72, v4
	v_mov_b32_e32 v73, v4
	v_mov_b32_e32 v74, v4
	v_mov_b32_e32 v75, v4
	v_mov_b32_e32 v84, v4
	v_mov_b32_e32 v85, v4
	v_mov_b32_e32 v86, v4
	v_mov_b32_e32 v87, v4
	v_mov_b32_e32 v88, v4
	v_mov_b32_e32 v89, v4
	v_mov_b32_e32 v90, v4
	v_mov_b32_e32 v91, v4
	v_mov_b32_e32 v100, v4
	v_mov_b32_e32 v101, v4
	v_mov_b32_e32 v102, v4
	v_mov_b32_e32 v103, v4
	v_mov_b32_e32 v104, v4
	v_mov_b32_e32 v105, v4
	v_mov_b32_e32 v106, v4
	v_mov_b32_e32 v107, v4
	v_mov_b32_e32 v116, v4
	v_mov_b32_e32 v117, v4
	v_mov_b32_e32 v118, v4
	v_mov_b32_e32 v119, v4
	v_mov_b32_e32 v120, v4
	v_mov_b32_e32 v121, v4
	v_mov_b32_e32 v122, v4
	v_mov_b32_e32 v123, v4
	v_mov_b32_e32 v76, v4
	v_mov_b32_e32 v77, v4
	v_mov_b32_e32 v78, v4
	v_mov_b32_e32 v79, v4
	v_mov_b32_e32 v80, v4
	v_mov_b32_e32 v81, v4
	v_mov_b32_e32 v82, v4
	v_mov_b32_e32 v83, v4
	v_mov_b32_e32 v92, v4
	v_mov_b32_e32 v93, v4
	v_mov_b32_e32 v94, v4
	v_mov_b32_e32 v95, v4
	v_mov_b32_e32 v96, v4
	v_mov_b32_e32 v97, v4
	v_mov_b32_e32 v98, v4
	v_mov_b32_e32 v99, v4
	v_mov_b32_e32 v108, v4
	v_mov_b32_e32 v109, v4
	v_mov_b32_e32 v110, v4
	v_mov_b32_e32 v111, v4
	v_mov_b32_e32 v112, v4
	v_mov_b32_e32 v113, v4
	v_mov_b32_e32 v114, v4
	v_mov_b32_e32 v115, v4
	v_mov_b32_e32 v124, v4
	v_mov_b32_e32 v125, v4
	v_mov_b32_e32 v126, v4
	v_mov_b32_e32 v127, v4
	v_mov_b32_e32 v128, v4
	v_mov_b32_e32 v129, v4
	v_mov_b32_e32 v130, v4
	v_mov_b32_e32 v131, v4
	s_add_u32 s36, s46, 0xfffc0080
	s_addc_u32 s37, s47, -1
	s_add_i32 s76, 0, 0x10000
	s_cmp_eq_u32 s73, 12
	s_cselect_b32 s37, s11, s37
	s_cselect_b32 s36, s68, s36
	s_cselect_b32 s75, s9, s53
	s_cselect_b32 s74, s72, s52
	s_add_i32 s77, 0, 0x14000
.LBB0_299:
	v_add_u32_e32 v162, s76, v147
	v_add_u32_e32 v178, s77, v147
	ds_read_b128 v[150:153], v162
	ds_read_b128 v[154:157], v162 offset:1024
	ds_read_b128 v[158:161], v162 offset:2048
	ds_read_b128 v[162:165], v162 offset:3072
	ds_read_b128 v[166:169], v178
	ds_read_b128 v[170:173], v178 offset:1024
	ds_read_b128 v[174:177], v178 offset:2048
	ds_read_b128 v[178:181], v178 offset:3072
	v_lshl_add_u64 v[198:199], s[46:47], 0, v[142:143]
	s_add_i32 m0, s41, 0xc000
	ds_read_b128 v[182:185], v149
	ds_read_b128 v[186:189], v149 offset:1024
	ds_read_b128 v[190:193], v149 offset:2048
	ds_read_b128 v[194:197], v149 offset:3072
	ds_read_b128 v[212:215], v149 offset:4096
	ds_read_b128 v[216:219], v149 offset:5120
	ds_read_b128 v[220:223], v149 offset:6144
	ds_read_b128 v[224:227], v149 offset:7168
	global_load_lds_dwordx4 v[198:199], off
	v_lshl_add_u64 v[198:199], s[46:47], 0, v[144:145]
	s_add_i32 m0, s41, 0xe000
	s_nop 0
	global_load_lds_dwordx4 v[198:199], off
	s_waitcnt vmcnt(8)
	s_waitcnt lgkmcnt(0)
	s_barrier
; #define PG8_STAGE(bufoff, gbase, voff) do { _Pragma("unroll") for (int _i = 0; _i < 2; ++_i) \
;         __builtin_amdgcn_global_load_lds((const unsigned*)((const char*)(gbase) + (voff)[_i]), (PG8_LAS unsigned*)(lds + (bufoff) + ldsw + _i * 8192), 16, 0, 0); } while (0)
; #define PG8_LDA(dst, b, h) do { _Pragma("unroll") for (int m = 0; m < 4; ++m) _Pragma("unroll") for (int k = 0; k < 2; ++k) dst[m][k] = *(const PG8_LAS bf16x8*)(lds + PG8_SA(b, h) + aoff + m * 2048 + k * 1024); } while (0)
; #define PG8_MMA(ai, bj, At, Bt) do { __builtin_amdgcn_s_setprio(1); _Pragma("unroll") for (int m = 0; m < 4; ++m) _Pragma("unroll") for (int n = 0; n < 2; ++n) _Pragma("unroll") for (int k = 0; k < 2; ++k) \
;         acc[ai][bj][m][n] = __builtin_amdgcn_mfma_f32_16x16x32_bf16(Bt[n][k], At[m][k], acc[ai][bj][m][n], 0, 0, 0); __builtin_amdgcn_s_setprio(0); } while (0)
; #define PG8_WAIT_V(n) asm volatile("s_waitcnt vmcnt(" #n ")" ::: "memory")
; #define PG8_WAIT_L(n) asm volatile("s_waitcnt lgkmcnt(" #n ")" ::: "memory")
; #define PG8_BAR __builtin_amdgcn_s_barrier()
; #define PG8_SCHED __builtin_amdgcn_sched_barrier(0)
; template <class Epi, class Sched, bool ALIGN_EPI = false, bool SP2 = false>
; __device__ __forceinline__ void gemm_phase(PG8_LAS unsigned char* lds, const Gemm g, const Sched& S, const Epi& E, const int tid) {
;     ...
;             PG8_WAIT_V(8); PG8_WAIT_L(0); PG8_BAR; PG8_MMA(0, 0, At, B0); PG8_MMA(0, 1, At, B1); PG8_BAR; PG8_SCHED;
;             PG8_LDA(At, 0, 1); PG8_STAGE(PG8_SB(0, 0), b2, voffB); PG8_STAGE(PG8_SB(0, 1), b2, voffB1); PG8_STAGE(PG8_SA(0, 0), a2, voffA);
;             PG8_WAIT_V(8); PG8_WAIT_L(0); PG8_BAR; PG8_MMA(1, 0, At, B0); PG8_MMA(1, 1, At, B1); PG8_BAR; PG8_SCHED;
	s_setprio 1
	s_waitcnt lgkmcnt(0)
	v_mfma_f32_16x16x32_bf16 v[128:131], v[150:153], v[182:185], v[128:131]
	v_mfma_f32_16x16x32_bf16 v[124:127], v[158:161], v[182:185], v[124:127]
	v_mfma_f32_16x16x32_bf16 v[112:115], v[150:153], v[190:193], v[112:115]
	v_mfma_f32_16x16x32_bf16 v[108:111], v[158:161], v[190:193], v[108:111]
	v_mfma_f32_16x16x32_bf16 v[96:99], v[150:153], v[212:215], v[96:99]
	v_mfma_f32_16x16x32_bf16 v[92:95], v[158:161], v[212:215], v[92:95]
	v_mfma_f32_16x16x32_bf16 v[80:83], v[150:153], v[220:223], v[80:83]
	v_mfma_f32_16x16x32_bf16 v[76:79], v[158:161], v[220:223], v[76:79]
	v_mfma_f32_16x16x32_bf16 v[128:131], v[154:157], v[186:189], v[128:131]
	v_mfma_f32_16x16x32_bf16 v[124:127], v[162:165], v[186:189], v[124:127]
	v_mfma_f32_16x16x32_bf16 v[112:115], v[154:157], v[194:197], v[112:115]
	v_mfma_f32_16x16x32_bf16 v[108:111], v[162:165], v[194:197], v[108:111]
	v_mfma_f32_16x16x32_bf16 v[96:99], v[154:157], v[216:219], v[96:99]
	v_mfma_f32_16x16x32_bf16 v[92:95], v[162:165], v[216:219], v[92:95]
	v_mfma_f32_16x16x32_bf16 v[80:83], v[154:157], v[224:227], v[80:83]
	v_mfma_f32_16x16x32_bf16 v[76:79], v[162:165], v[224:227], v[76:79]
	s_setprio 0
	s_setprio 1
	v_mfma_f32_16x16x32_bf16 v[120:123], v[166:169], v[182:185], v[120:123]
	v_mfma_f32_16x16x32_bf16 v[116:119], v[174:177], v[182:185], v[116:119]
	v_mfma_f32_16x16x32_bf16 v[104:107], v[166:169], v[190:193], v[104:107]
	v_mfma_f32_16x16x32_bf16 v[100:103], v[174:177], v[190:193], v[100:103]
	v_mfma_f32_16x16x32_bf16 v[88:91], v[166:169], v[212:215], v[88:91]
	v_mfma_f32_16x16x32_bf16 v[84:87], v[174:177], v[212:215], v[84:87]
	v_mfma_f32_16x16x32_bf16 v[72:75], v[166:169], v[220:223], v[72:75]
	v_mfma_f32_16x16x32_bf16 v[68:71], v[174:177], v[220:223], v[68:71]
	v_mfma_f32_16x16x32_bf16 v[120:123], v[170:173], v[186:189], v[120:123]
	v_mfma_f32_16x16x32_bf16 v[116:119], v[178:181], v[186:189], v[116:119]
	v_mfma_f32_16x16x32_bf16 v[104:107], v[170:173], v[194:197], v[104:107]
	v_mfma_f32_16x16x32_bf16 v[100:103], v[178:181], v[194:197], v[100:103]
	v_mfma_f32_16x16x32_bf16 v[88:91], v[170:173], v[216:219], v[88:91]
	v_mfma_f32_16x16x32_bf16 v[84:87], v[178:181], v[216:219], v[84:87]
	v_mfma_f32_16x16x32_bf16 v[72:75], v[170:173], v[224:227], v[72:75]
	v_mfma_f32_16x16x32_bf16 v[68:71], v[178:181], v[224:227], v[68:71]
	s_setprio 0
	s_barrier
	s_add_i32 s76, s76, s0
	v_lshl_add_u64 v[198:199], s[74:75], 0, v[138:139]
	s_mov_b32 m0, s76
	ds_read_b128 v[182:185], v149 offset:16384
	ds_read_b128 v[186:189], v149 offset:17408
	ds_read_b128 v[190:193], v149 offset:18432
	ds_read_b128 v[194:197], v149 offset:19456
	ds_read_b128 v[212:215], v149 offset:20480
	ds_read_b128 v[216:219], v149 offset:21504
	ds_read_b128 v[220:223], v149 offset:22528
	ds_read_b128 v[224:227], v149 offset:23552
	global_load_lds_dwordx4 v[198:199], off
	v_lshl_add_u64 v[200:201], s[74:75], 0, v[132:133]
	s_add_i32 m0, s76, 0x2000
	s_add_i32 s76, s77, s0
	global_load_lds_dwordx4 v[200:201], off
	v_lshl_add_u64 v[202:203], s[74:75], 0, v[136:137]
	s_mov_b32 m0, s76
	v_lshl_add_u64 v[204:205], s[74:75], 0, v[0:1]
	global_load_lds_dwordx4 v[202:203], off
	s_add_i32 m0, s76, 0x2000
	v_lshl_add_u64 v[208:209], s[36:37], 0, v[140:141]
	global_load_lds_dwordx4 v[204:205], off
	s_mov_b32 m0, s41
	v_lshl_add_u64 v[210:211], s[36:37], 0, v[134:135]
	global_load_lds_dwordx4 v[208:209], off
	s_mov_b32 m0, s42
	s_nop 0
	global_load_lds_dwordx4 v[210:211], off
	s_waitcnt vmcnt(8)
	s_waitcnt lgkmcnt(0)
	s_barrier
	s_setprio 1
	s_waitcnt lgkmcnt(0)
	v_mfma_f32_16x16x32_bf16 v[64:67], v[150:153], v[182:185], v[64:67]
	v_mfma_f32_16x16x32_bf16 v[60:63], v[158:161], v[182:185], v[60:63]
	v_mfma_f32_16x16x32_bf16 v[48:51], v[150:153], v[190:193], v[48:51]
	v_mfma_f32_16x16x32_bf16 v[44:47], v[158:161], v[190:193], v[44:47]
	v_mfma_f32_16x16x32_bf16 v[32:35], v[150:153], v[212:215], v[32:35]
	v_mfma_f32_16x16x32_bf16 v[28:31], v[158:161], v[212:215], v[28:31]
	v_mfma_f32_16x16x32_bf16 v[16:19], v[150:153], v[220:223], v[16:19]
	v_mfma_f32_16x16x32_bf16 v[12:15], v[158:161], v[220:223], v[12:15]
	v_mfma_f32_16x16x32_bf16 v[64:67], v[154:157], v[186:189], v[64:67]
	v_mfma_f32_16x16x32_bf16 v[60:63], v[162:165], v[186:189], v[60:63]
	v_mfma_f32_16x16x32_bf16 v[48:51], v[154:157], v[194:197], v[48:51]
	v_mfma_f32_16x16x32_bf16 v[44:47], v[162:165], v[194:197], v[44:47]
	v_mfma_f32_16x16x32_bf16 v[32:35], v[154:157], v[216:219], v[32:35]
	v_mfma_f32_16x16x32_bf16 v[28:31], v[162:165], v[216:219], v[28:31]
	v_mfma_f32_16x16x32_bf16 v[16:19], v[154:157], v[224:227], v[16:19]
	v_mfma_f32_16x16x32_bf16 v[12:15], v[162:165], v[224:227], v[12:15]
	s_setprio 0
	s_setprio 1
	v_mfma_f32_16x16x32_bf16 v[56:59], v[166:169], v[182:185], v[56:59]
	v_mfma_f32_16x16x32_bf16 v[52:55], v[174:177], v[182:185], v[52:55]
	v_mfma_f32_16x16x32_bf16 v[40:43], v[166:169], v[190:193], v[40:43]
	v_mfma_f32_16x16x32_bf16 v[36:39], v[174:177], v[190:193], v[36:39]
	v_mfma_f32_16x16x32_bf16 v[24:27], v[166:169], v[212:215], v[24:27]
	v_mfma_f32_16x16x32_bf16 v[20:23], v[174:177], v[212:215], v[20:23]
	v_mfma_f32_16x16x32_bf16 v[8:11], v[166:169], v[220:223], v[8:11]
	v_mfma_f32_16x16x32_bf16 v[4:7], v[174:177], v[220:223], v[4:7]
	v_mfma_f32_16x16x32_bf16 v[56:59], v[170:173], v[186:189], v[56:59]
	v_mfma_f32_16x16x32_bf16 v[52:55], v[178:181], v[186:189], v[52:55]
	v_mfma_f32_16x16x32_bf16 v[40:43], v[170:173], v[194:197], v[40:43]
	v_mfma_f32_16x16x32_bf16 v[36:39], v[178:181], v[194:197], v[36:39]
	v_mfma_f32_16x16x32_bf16 v[24:27], v[170:173], v[216:219], v[24:27]
	v_mfma_f32_16x16x32_bf16 v[20:23], v[178:181], v[216:219], v[20:23]
	v_mfma_f32_16x16x32_bf16 v[8:11], v[170:173], v[224:227], v[8:11]
	v_mfma_f32_16x16x32_bf16 v[4:7], v[178:181], v[224:227], v[4:7]
	s_setprio 0
	s_barrier
; #define PG8_STAGE(bufoff, gbase, voff) do { _Pragma("unroll") for (int _i = 0; _i < 2; ++_i) \
;         __builtin_amdgcn_global_load_lds((const unsigned*)((const char*)(gbase) + (voff)[_i]), (PG8_LAS unsigned*)(lds + (bufoff) + ldsw + _i * 8192), 16, 0, 0); } while (0)
; #define PG8_LDA(dst, b, h) do { _Pragma("unroll") for (int m = 0; m < 4; ++m) _Pragma("unroll") for (int k = 0; k < 2; ++k) dst[m][k] = *(const PG8_LAS bf16x8*)(lds + PG8_SA(b, h) + aoff + m * 2048 + k * 1024); } while (0)
; #define PG8_LDB(dst, b, h) do { _Pragma("unroll") for (int n = 0; n < 2; ++n) _Pragma("unroll") for (int k = 0; k < 2; ++k) dst[n][k] = *(const PG8_LAS bf16x8*)(lds + PG8_SB(b, h) + boff + n * 2048 + k * 1024); } while (0)
; #define PG8_MMA(ai, bj, At, Bt) do { __builtin_amdgcn_s_setprio(1); _Pragma("unroll") for (int m = 0; m < 4; ++m) _Pragma("unroll") for (int n = 0; n < 2; ++n) _Pragma("unroll") for (int k = 0; k < 2; ++k) \
;         acc[ai][bj][m][n] = __builtin_amdgcn_mfma_f32_16x16x32_bf16(Bt[n][k], At[m][k], acc[ai][bj][m][n], 0, 0, 0); __builtin_amdgcn_s_setprio(0); } while (0)
; #define PG8_WAIT_V(n) asm volatile("s_waitcnt vmcnt(" #n ")" ::: "memory")
; #define PG8_WAIT_L(n) asm volatile("s_waitcnt lgkmcnt(" #n ")" ::: "memory")
; #define PG8_BAR __builtin_amdgcn_s_barrier()
; #define PG8_SCHED __builtin_amdgcn_sched_barrier(0)
; template <class Epi, class Sched, bool ALIGN_EPI = false, bool SP2 = false>
; __device__ __forceinline__ void gemm_phase(PG8_LAS unsigned char* lds, const Gemm g, const Sched& S, const Epi& E, const int tid) {
;     ...
;             PG8_LDB(B0, 1, 0); PG8_LDB(B1, 1, 1); PG8_SCHED; PG8_LDA(At, 1, 0); PG8_STAGE(PG8_SA(0, 1), a2 + hstep, voffA);
;             PG8_WAIT_V(8); PG8_WAIT_L(0); PG8_BAR; PG8_MMA(0, 0, At, B0); PG8_MMA(0, 1, At, B1); PG8_BAR; PG8_SCHED;
	s_add_i32 s74, 0, 0x18000
	s_add_i32 s75, 0, 0x1c000
	v_add_u32_e32 v162, s74, v147
	v_add_u32_e32 v178, s75, v147
	ds_read_b128 v[150:153], v162
	ds_read_b128 v[154:157], v162 offset:1024
	ds_read_b128 v[158:161], v162 offset:2048
	ds_read_b128 v[162:165], v162 offset:3072
	ds_read_b128 v[166:169], v178
	ds_read_b128 v[170:173], v178 offset:1024
	ds_read_b128 v[174:177], v178 offset:2048
	ds_read_b128 v[178:181], v178 offset:3072
	s_add_u32 s36, s36, 0x40000
	s_addc_u32 s37, s37, 0
	s_mov_b32 m0, s43
	v_lshl_add_u64 v[228:229], s[36:37], 0, v[140:141]
	ds_read_b128 v[182:185], v149 offset:32768
	ds_read_b128 v[186:189], v149 offset:33792
	ds_read_b128 v[190:193], v149 offset:34816
	ds_read_b128 v[194:197], v149 offset:35840
	ds_read_b128 v[212:215], v149 offset:36864
	ds_read_b128 v[216:219], v149 offset:37888
	ds_read_b128 v[220:223], v149 offset:38912
	ds_read_b128 v[224:227], v149 offset:39936
	global_load_lds_dwordx4 v[228:229], off
	v_lshl_add_u64 v[228:229], s[36:37], 0, v[134:135]
	s_mov_b32 m0, s48
	s_nop 0
	global_load_lds_dwordx4 v[228:229], off
	s_waitcnt vmcnt(8)
	s_waitcnt lgkmcnt(0)
	s_barrier
	s_setprio 1
	s_waitcnt lgkmcnt(0)
	v_mfma_f32_16x16x32_bf16 v[128:131], v[150:153], v[182:185], v[128:131]
	v_mfma_f32_16x16x32_bf16 v[124:127], v[158:161], v[182:185], v[124:127]
	v_mfma_f32_16x16x32_bf16 v[112:115], v[150:153], v[190:193], v[112:115]
	v_mfma_f32_16x16x32_bf16 v[108:111], v[158:161], v[190:193], v[108:111]
	v_mfma_f32_16x16x32_bf16 v[96:99], v[150:153], v[212:215], v[96:99]
	v_mfma_f32_16x16x32_bf16 v[92:95], v[158:161], v[212:215], v[92:95]
	v_mfma_f32_16x16x32_bf16 v[80:83], v[150:153], v[220:223], v[80:83]
	v_mfma_f32_16x16x32_bf16 v[76:79], v[158:161], v[220:223], v[76:79]
	v_mfma_f32_16x16x32_bf16 v[128:131], v[154:157], v[186:189], v[128:131]
	v_mfma_f32_16x16x32_bf16 v[124:127], v[162:165], v[186:189], v[124:127]
	v_mfma_f32_16x16x32_bf16 v[112:115], v[154:157], v[194:197], v[112:115]
	v_mfma_f32_16x16x32_bf16 v[108:111], v[162:165], v[194:197], v[108:111]
	v_mfma_f32_16x16x32_bf16 v[96:99], v[154:157], v[216:219], v[96:99]
	v_mfma_f32_16x16x32_bf16 v[92:95], v[162:165], v[216:219], v[92:95]
	v_mfma_f32_16x16x32_bf16 v[80:83], v[154:157], v[224:227], v[80:83]
	v_mfma_f32_16x16x32_bf16 v[76:79], v[162:165], v[224:227], v[76:79]
	s_setprio 0
	s_setprio 1
	v_mfma_f32_16x16x32_bf16 v[120:123], v[166:169], v[182:185], v[120:123]
	v_mfma_f32_16x16x32_bf16 v[116:119], v[174:177], v[182:185], v[116:119]
	v_mfma_f32_16x16x32_bf16 v[104:107], v[166:169], v[190:193], v[104:107]
	v_mfma_f32_16x16x32_bf16 v[100:103], v[174:177], v[190:193], v[100:103]
	v_mfma_f32_16x16x32_bf16 v[88:91], v[166:169], v[212:215], v[88:91]
	v_mfma_f32_16x16x32_bf16 v[84:87], v[174:177], v[212:215], v[84:87]
	v_mfma_f32_16x16x32_bf16 v[72:75], v[166:169], v[220:223], v[72:75]
	v_mfma_f32_16x16x32_bf16 v[68:71], v[174:177], v[220:223], v[68:71]
	v_mfma_f32_16x16x32_bf16 v[120:123], v[170:173], v[186:189], v[120:123]
	v_mfma_f32_16x16x32_bf16 v[116:119], v[178:181], v[186:189], v[116:119]
	v_mfma_f32_16x16x32_bf16 v[104:107], v[170:173], v[194:197], v[104:107]
	v_mfma_f32_16x16x32_bf16 v[100:103], v[178:181], v[194:197], v[100:103]
	v_mfma_f32_16x16x32_bf16 v[88:91], v[170:173], v[216:219], v[88:91]
	v_mfma_f32_16x16x32_bf16 v[84:87], v[178:181], v[216:219], v[84:87]
	v_mfma_f32_16x16x32_bf16 v[72:75], v[170:173], v[224:227], v[72:75]
	v_mfma_f32_16x16x32_bf16 v[68:71], v[178:181], v[224:227], v[68:71]
	s_setprio 0
	s_barrier
; #define PG8_STAGE(bufoff, gbase, voff) do { _Pragma("unroll") for (int _i = 0; _i < 2; ++_i) \
;         __builtin_amdgcn_global_load_lds((const unsigned*)((const char*)(gbase) + (voff)[_i]), (PG8_LAS unsigned*)(lds + (bufoff) + ldsw + _i * 8192), 16, 0, 0); } while (0)
; #define PG8_LDA(dst, b, h) do { _Pragma("unroll") for (int m = 0; m < 4; ++m) _Pragma("unroll") for (int k = 0; k < 2; ++k) dst[m][k] = *(const PG8_LAS bf16x8*)(lds + PG8_SA(b, h) + aoff + m * 2048 + k * 1024); } while (0)
; #define PG8_MMA(ai, bj, At, Bt) do { __builtin_amdgcn_s_setprio(1); _Pragma("unroll") for (int m = 0; m < 4; ++m) _Pragma("unroll") for (int n = 0; n < 2; ++n) _Pragma("unroll") for (int k = 0; k < 2; ++k) \
;         acc[ai][bj][m][n] = __builtin_amdgcn_mfma_f32_16x16x32_bf16(Bt[n][k], At[m][k], acc[ai][bj][m][n], 0, 0, 0); __builtin_amdgcn_s_setprio(0); } while (0)
; #define PG8_WAIT_V(n) asm volatile("s_waitcnt vmcnt(" #n ")" ::: "memory")
; #define PG8_WAIT_L(n) asm volatile("s_waitcnt lgkmcnt(" #n ")" ::: "memory")
; #define PG8_BAR __builtin_amdgcn_s_barrier()
; #define PG8_SCHED __builtin_amdgcn_sched_barrier(0)
; template <class Epi, class Sched, bool ALIGN_EPI = false, bool SP2 = false>
; __device__ __forceinline__ void gemm_phase(PG8_LAS unsigned char* lds, const Gemm g, const Sched& S, const Epi& E, const int tid) {
;     ...
;         for (int t = 0; t < nt; t += 2) {
;             const bool last = (t == nt - 2);
;             const char* a1 = cA + (size_t)(t + 1) * kstep;
;             const char* a2 = last ? nA : cA + (size_t)(t + 2) * kstep; const char* b2 = last ? nB : cB + (size_t)(t + 2) * kstep;
;             const char* a3 = a2 + kstep; const char* b3 = b2 + kstep;
;     ...
;             PG8_LDA(At, 1, 1); PG8_STAGE(PG8_SB(1, 0), b3, voffB); PG8_STAGE(PG8_SB(1, 1), b3, voffB1); PG8_STAGE(PG8_SA(1, 0), a3, voffA);
;             PG8_WAIT_V(8); PG8_WAIT_L(0); PG8_BAR; PG8_MMA(1, 0, At, B0); PG8_MMA(1, 1, At, B1); PG8_BAR; PG8_SCHED;
	s_add_i32 s36, s74, s0
	v_lshl_add_u64 v[198:199], v[198:199], 0, s[66:67]
	s_mov_b32 m0, s36
	ds_read_b128 v[182:185], v149 offset:49152
	ds_read_b128 v[186:189], v149 offset:50176
	ds_read_b128 v[190:193], v149 offset:51200
	ds_read_b128 v[194:197], v149 offset:52224
	ds_read_b128 v[212:215], v149 offset:53248
	ds_read_b128 v[216:219], v149 offset:54272
	ds_read_b128 v[220:223], v149 offset:55296
	ds_read_b128 v[224:227], v149 offset:56320
	global_load_lds_dwordx4 v[198:199], off
	v_lshl_add_u64 v[198:199], v[200:201], 0, s[66:67]
	s_add_i32 m0, s36, 0x2000
	s_add_i32 s36, s75, s0
	global_load_lds_dwordx4 v[198:199], off
	v_lshl_add_u64 v[198:199], v[202:203], 0, s[66:67]
	s_mov_b32 m0, s36
	s_nop 0
	global_load_lds_dwordx4 v[198:199], off
	v_lshl_add_u64 v[198:199], v[204:205], 0, s[66:67]
	s_add_i32 m0, s36, 0x2000
	s_nop 0
	global_load_lds_dwordx4 v[198:199], off
	v_lshl_add_u64 v[198:199], v[208:209], 0, s[66:67]
	s_mov_b32 m0, s55
	s_nop 0
	global_load_lds_dwordx4 v[198:199], off
	v_lshl_add_u64 v[198:199], v[210:211], 0, s[66:67]
	s_mov_b32 m0, s56
	s_nop 0
	global_load_lds_dwordx4 v[198:199], off
	s_waitcnt vmcnt(8)
	s_waitcnt lgkmcnt(0)
	s_barrier
	s_setprio 1
	s_waitcnt lgkmcnt(0)
	v_mfma_f32_16x16x32_bf16 v[64:67], v[150:153], v[182:185], v[64:67]
	v_mfma_f32_16x16x32_bf16 v[60:63], v[158:161], v[182:185], v[60:63]
	v_mfma_f32_16x16x32_bf16 v[48:51], v[150:153], v[190:193], v[48:51]
	v_mfma_f32_16x16x32_bf16 v[44:47], v[158:161], v[190:193], v[44:47]
	v_mfma_f32_16x16x32_bf16 v[32:35], v[150:153], v[212:215], v[32:35]
	v_mfma_f32_16x16x32_bf16 v[28:31], v[158:161], v[212:215], v[28:31]
	v_mfma_f32_16x16x32_bf16 v[16:19], v[150:153], v[220:223], v[16:19]
	v_mfma_f32_16x16x32_bf16 v[12:15], v[158:161], v[220:223], v[12:15]
	v_mfma_f32_16x16x32_bf16 v[64:67], v[154:157], v[186:189], v[64:67]
	s_add_i32 s73, s73, 2
	v_mfma_f32_16x16x32_bf16 v[60:63], v[162:165], v[186:189], v[60:63]
	s_add_u32 s46, s46, 0x100
	v_mfma_f32_16x16x32_bf16 v[48:51], v[154:157], v[194:197], v[48:51]
	s_addc_u32 s47, s47, 0
	v_mfma_f32_16x16x32_bf16 v[44:47], v[162:165], v[194:197], v[44:47]
	s_add_u32 s52, s52, 0x100
	v_mfma_f32_16x16x32_bf16 v[32:35], v[154:157], v[216:219], v[32:35]
	s_addc_u32 s53, s53, 0
	v_mfma_f32_16x16x32_bf16 v[28:31], v[162:165], v[216:219], v[28:31]
	s_add_u32 s36, s46, 0xfffc0080
	v_mfma_f32_16x16x32_bf16 v[16:19], v[154:157], v[224:227], v[16:19]
	s_addc_u32 s37, s47, -1
	v_mfma_f32_16x16x32_bf16 v[12:15], v[162:165], v[224:227], v[12:15]
	s_add_i32 s76, 0, 0x10000
	s_setprio 0
	s_setprio 1
	v_mfma_f32_16x16x32_bf16 v[56:59], v[166:169], v[182:185], v[56:59]
	s_cmp_eq_u32 s73, 12
	v_mfma_f32_16x16x32_bf16 v[52:55], v[174:177], v[182:185], v[52:55]
	s_cselect_b32 s37, s11, s37
	v_mfma_f32_16x16x32_bf16 v[40:43], v[166:169], v[190:193], v[40:43]
	s_cselect_b32 s36, s68, s36
	v_mfma_f32_16x16x32_bf16 v[36:39], v[174:177], v[190:193], v[36:39]
	s_cselect_b32 s75, s9, s53
	v_mfma_f32_16x16x32_bf16 v[24:27], v[166:169], v[212:215], v[24:27]
	s_cselect_b32 s74, s72, s52
	v_mfma_f32_16x16x32_bf16 v[20:23], v[174:177], v[212:215], v[20:23]
	s_add_i32 s77, 0, 0x14000
	v_mfma_f32_16x16x32_bf16 v[8:11], v[166:169], v[220:223], v[8:11]
	s_cmp_gt_u32 s73, 13
	v_mfma_f32_16x16x32_bf16 v[4:7], v[174:177], v[220:223], v[4:7]
	v_mfma_f32_16x16x32_bf16 v[56:59], v[170:173], v[186:189], v[56:59]
	v_mfma_f32_16x16x32_bf16 v[52:55], v[178:181], v[186:189], v[52:55]
	v_mfma_f32_16x16x32_bf16 v[40:43], v[170:173], v[194:197], v[40:43]
	v_mfma_f32_16x16x32_bf16 v[36:39], v[178:181], v[194:197], v[36:39]
	v_mfma_f32_16x16x32_bf16 v[24:27], v[170:173], v[216:219], v[24:27]
	v_mfma_f32_16x16x32_bf16 v[20:23], v[178:181], v[216:219], v[20:23]
	v_mfma_f32_16x16x32_bf16 v[8:11], v[170:173], v[224:227], v[8:11]
	v_mfma_f32_16x16x32_bf16 v[4:7], v[178:181], v[224:227], v[4:7]
	s_setprio 0
	s_barrier
	s_cbranch_scc0 .LBB0_299
	s_and_b64 vcc, exec, s[6:7]
	s_cbranch_vccz .LBB0_302
	s_barrier

; template <class Epi, class Sched, bool ALIGN_EPI = false, bool SP2 = false>
; __device__ __forceinline__ void gemm_phase(PG8_LAS unsigned char* lds, const Gemm g, const Sched& S, const Epi& E, const int tid) {
;     ...
;         const bool has_next = S.next(ui + 1, nxt);
;         const char* nA = has_next ? (const char*)g.A + (size_t)nxt.pm * tstep : cA; const char* nB = has_next ? (const char*)g.Bt + (size_t)nxt.pn * tstep : cB;
;         for (int t = 0; t < nt; t += 2) {
;             const bool last = (t == nt - 2);
;             const char* a1 = cA + (size_t)(t + 1) * kstep;
;             const char* a2 = last ? nA : cA + (size_t)(t + 2) * kstep; const char* b2 = last ? nB : cB + (size_t)(t + 2) * kstep;
;             const char* a3 = a2 + kstep; const char* b3 = b2 + kstep;
;     ...
; #pragma unroll
;         for (int a = 0; a < 2; ++a)
; #pragma unroll
;             for (int b = 0; b < 2; ++b)
; #pragma unroll
;                 for (int m = 0; m < 4; ++m)
; #pragma unroll
;                     for (int n = 0; n < 2; ++n) acc[a][b][m][n] = (f32x4){0.f, 0.f, 0.f, 0.f};
;         cur = nxt; cA = nA; cB = nB; ++ui;
.LBB0_342:
	s_ashr_i32 s11, s10, 31
	s_lshl_b64 s[12:13], s[10:11], 19
	s_add_u32 s12, s42, s12
	s_addc_u32 s13, s43, s13
	s_and_b64 s[14:15], s[2:3], exec
	s_cselect_b32 s11, s13, s47
	s_cselect_b32 s40, s12, s46
	s_ashr_i32 s9, s8, 31
	s_lshl_b64 s[14:15], s[8:9], 19
	s_add_u32 s14, s48, s14
	s_addc_u32 s15, s54, s15
	s_and_b64 s[36:37], s[2:3], exec
	s_cselect_b32 s9, s15, s53
	s_cselect_b32 s45, s14, s52
	s_add_u32 s46, s46, 0x40080
	s_addc_u32 s47, s47, 0
	s_add_u32 s49, s52, 0x100
	v_mov_b32_e32 v4, 0
	s_addc_u32 s50, s53, 0
	s_mov_b32 s51, -2
	v_mov_b32_e32 v5, v4
	v_mov_b32_e32 v6, v4
	v_mov_b32_e32 v7, v4
	v_mov_b32_e32 v12, v4
	v_mov_b32_e32 v13, v4
	v_mov_b32_e32 v14, v4
	v_mov_b32_e32 v15, v4
	v_mov_b32_e32 v20, v4
	v_mov_b32_e32 v21, v4
	v_mov_b32_e32 v22, v4
	v_mov_b32_e32 v23, v4
	v_mov_b32_e32 v28, v4
	v_mov_b32_e32 v29, v4
	v_mov_b32_e32 v30, v4
	v_mov_b32_e32 v31, v4
	v_mov_b32_e32 v36, v4
	v_mov_b32_e32 v37, v4
	v_mov_b32_e32 v38, v4
	v_mov_b32_e32 v39, v4
	v_mov_b32_e32 v44, v4
	v_mov_b32_e32 v45, v4
	v_mov_b32_e32 v46, v4
	v_mov_b32_e32 v47, v4
	v_mov_b32_e32 v52, v4
	v_mov_b32_e32 v53, v4
	v_mov_b32_e32 v54, v4
	v_mov_b32_e32 v55, v4
	v_mov_b32_e32 v60, v4
	v_mov_b32_e32 v61, v4
	v_mov_b32_e32 v62, v4
	v_mov_b32_e32 v63, v4
	v_mov_b32_e32 v8, v4
	v_mov_b32_e32 v9, v4
	v_mov_b32_e32 v10, v4
	v_mov_b32_e32 v11, v4
	v_mov_b32_e32 v16, v4
	v_mov_b32_e32 v17, v4
	v_mov_b32_e32 v18, v4
	v_mov_b32_e32 v19, v4
	v_mov_b32_e32 v24, v4
	v_mov_b32_e32 v25, v4
	v_mov_b32_e32 v26, v4
	v_mov_b32_e32 v27, v4
	v_mov_b32_e32 v32, v4
	v_mov_b32_e32 v33, v4
	v_mov_b32_e32 v34, v4
	v_mov_b32_e32 v35, v4
	v_mov_b32_e32 v40, v4
	v_mov_b32_e32 v41, v4
	v_mov_b32_e32 v42, v4
	v_mov_b32_e32 v43, v4
	v_mov_b32_e32 v48, v4
	v_mov_b32_e32 v49, v4
	v_mov_b32_e32 v50, v4
	v_mov_b32_e32 v51, v4
	v_mov_b32_e32 v56, v4
	v_mov_b32_e32 v57, v4
	v_mov_b32_e32 v58, v4
	v_mov_b32_e32 v59, v4
	v_mov_b32_e32 v64, v4
	v_mov_b32_e32 v65, v4
	v_mov_b32_e32 v66, v4
	v_mov_b32_e32 v67, v4
	v_mov_b32_e32 v68, v4
	v_mov_b32_e32 v69, v4
	v_mov_b32_e32 v70, v4
	v_mov_b32_e32 v71, v4
	v_mov_b32_e32 v76, v4
	v_mov_b32_e32 v77, v4
	v_mov_b32_e32 v78, v4
	v_mov_b32_e32 v79, v4
	v_mov_b32_e32 v84, v4
	v_mov_b32_e32 v85, v4
	v_mov_b32_e32 v86, v4
	v_mov_b32_e32 v87, v4
	v_mov_b32_e32 v92, v4
	v_mov_b32_e32 v93, v4
	v_mov_b32_e32 v94, v4
	v_mov_b32_e32 v95, v4
	v_mov_b32_e32 v100, v4
	v_mov_b32_e32 v101, v4
	v_mov_b32_e32 v102, v4
	v_mov_b32_e32 v103, v4
	v_mov_b32_e32 v116, v4
	v_mov_b32_e32 v117, v4
	v_mov_b32_e32 v118, v4
	v_mov_b32_e32 v119, v4
	v_mov_b32_e32 v128, v4
	v_mov_b32_e32 v129, v4
	v_mov_b32_e32 v130, v4
	v_mov_b32_e32 v131, v4
	v_mov_b32_e32 v144, v4
	v_mov_b32_e32 v145, v4
	v_mov_b32_e32 v146, v4
	v_mov_b32_e32 v147, v4
	v_mov_b32_e32 v72, v4
	v_mov_b32_e32 v73, v4
	v_mov_b32_e32 v74, v4
	v_mov_b32_e32 v75, v4
	v_mov_b32_e32 v80, v4
	v_mov_b32_e32 v81, v4
	v_mov_b32_e32 v82, v4
	v_mov_b32_e32 v83, v4
	v_mov_b32_e32 v88, v4
	v_mov_b32_e32 v89, v4
	v_mov_b32_e32 v90, v4
	v_mov_b32_e32 v91, v4
	v_mov_b32_e32 v96, v4
	v_mov_b32_e32 v97, v4
	v_mov_b32_e32 v98, v4
	v_mov_b32_e32 v99, v4
	v_mov_b32_e32 v104, v4
	v_mov_b32_e32 v105, v4
	v_mov_b32_e32 v106, v4
	v_mov_b32_e32 v107, v4
	v_mov_b32_e32 v120, v4
	v_mov_b32_e32 v121, v4
	v_mov_b32_e32 v122, v4
	v_mov_b32_e32 v123, v4
	v_mov_b32_e32 v132, v4
	v_mov_b32_e32 v133, v4
	v_mov_b32_e32 v134, v4
	v_mov_b32_e32 v135, v4
	v_mov_b32_e32 v148, v4
	v_mov_b32_e32 v149, v4
	v_mov_b32_e32 v150, v4
	v_mov_b32_e32 v151, v4
	s_add_u32 s36, s46, 0xfffc0080
	s_addc_u32 s37, s47, -1
	s_add_i32 s58, 0, 0x10000
	s_cmp_eq_u32 s51, 12
	s_cselect_b32 s37, s11, s37
	s_cselect_b32 s36, s40, s36
	s_cselect_b32 s53, s9, s50
	s_cselect_b32 s52, s45, s49
	s_add_i32 s59, 0, 0x14000
.LBB0_343:
	v_add_u32_e32 v136, s58, v219
	v_add_u32_e32 v160, s59, v219
	ds_read_b128 v[108:111], v136
	ds_read_b128 v[112:115], v136 offset:1024
	ds_read_b128 v[124:127], v136 offset:2048
	ds_read_b128 v[136:139], v136 offset:3072
	ds_read_b128 v[140:143], v160
	ds_read_b128 v[152:155], v160 offset:1024
	ds_read_b128 v[156:159], v160 offset:2048
	ds_read_b128 v[160:163], v160 offset:3072
	v_lshl_add_u64 v[204:205], s[46:47], 0, v[184:185]
	s_add_i32 m0, s55, 0xc000
	ds_read_b128 v[164:167], v225
	ds_read_b128 v[168:171], v225 offset:1024
	ds_read_b128 v[172:175], v225 offset:2048
	ds_read_b128 v[188:191], v225 offset:3072
	ds_read_b128 v[192:195], v225 offset:4096
	ds_read_b128 v[196:199], v225 offset:5120
	ds_read_b128 v[200:203], v225 offset:6144
	ds_read_b128 v[208:211], v225 offset:7168
	global_load_lds_dwordx4 v[204:205], off
	v_lshl_add_u64 v[204:205], s[46:47], 0, v[186:187]
	s_add_i32 m0, s55, 0xe000
	s_nop 0
	global_load_lds_dwordx4 v[204:205], off
	s_waitcnt vmcnt(8)
	s_waitcnt lgkmcnt(0)
	s_barrier
; #define PG8_STAGE(bufoff, gbase, voff) do { _Pragma("unroll") for (int _i = 0; _i < 2; ++_i) \
;         __builtin_amdgcn_global_load_lds((const unsigned*)((const char*)(gbase) + (voff)[_i]), (PG8_LAS unsigned*)(lds + (bufoff) + ldsw + _i * 8192), 16, 0, 0); } while (0)
; #define PG8_LDA(dst, b, h) do { _Pragma("unroll") for (int m = 0; m < 4; ++m) _Pragma("unroll") for (int k = 0; k < 2; ++k) dst[m][k] = *(const PG8_LAS bf16x8*)(lds + PG8_SA(b, h) + aoff + m * 2048 + k * 1024); } while (0)
; #define PG8_MMA(ai, bj, At, Bt) do { __builtin_amdgcn_s_setprio(1); _Pragma("unroll") for (int m = 0; m < 4; ++m) _Pragma("unroll") for (int n = 0; n < 2; ++n) _Pragma("unroll") for (int k = 0; k < 2; ++k) \
;         acc[ai][bj][m][n] = __builtin_amdgcn_mfma_f32_16x16x32_bf16(Bt[n][k], At[m][k], acc[ai][bj][m][n], 0, 0, 0); __builtin_amdgcn_s_setprio(0); } while (0)
; #define PG8_WAIT_V(n) asm volatile("s_waitcnt vmcnt(" #n ")" ::: "memory")
; #define PG8_WAIT_L(n) asm volatile("s_waitcnt lgkmcnt(" #n ")" ::: "memory")
; #define PG8_BAR __builtin_amdgcn_s_barrier()
; #define PG8_SCHED __builtin_amdgcn_sched_barrier(0)
; template <class Epi, class Sched, bool ALIGN_EPI = false, bool SP2 = false>
; __device__ __forceinline__ void gemm_phase(PG8_LAS unsigned char* lds, const Gemm g, const Sched& S, const Epi& E, const int tid) {
;     ...
;             PG8_WAIT_V(8); PG8_WAIT_L(0); PG8_BAR; PG8_MMA(0, 0, At, B0); PG8_MMA(0, 1, At, B1); PG8_BAR; PG8_SCHED;
;             PG8_LDA(At, 0, 1); PG8_STAGE(PG8_SB(0, 0), b2, voffB); PG8_STAGE(PG8_SB(0, 1), b2, voffB1); PG8_STAGE(PG8_SA(0, 0), a2, voffA);
;             PG8_WAIT_V(8); PG8_WAIT_L(0); PG8_BAR; PG8_MMA(1, 0, At, B0); PG8_MMA(1, 1, At, B1); PG8_BAR; PG8_SCHED;
	s_setprio 1
	s_waitcnt lgkmcnt(0)
	v_mfma_f32_16x16x32_bf16 v[148:151], v[108:111], v[164:167], v[148:151]
	v_mfma_f32_16x16x32_bf16 v[132:135], v[124:127], v[164:167], v[132:135]
	v_mfma_f32_16x16x32_bf16 v[120:123], v[108:111], v[172:175], v[120:123]
	v_mfma_f32_16x16x32_bf16 v[104:107], v[124:127], v[172:175], v[104:107]
	v_mfma_f32_16x16x32_bf16 v[96:99], v[108:111], v[192:195], v[96:99]
	v_mfma_f32_16x16x32_bf16 v[88:91], v[124:127], v[192:195], v[88:91]
	v_mfma_f32_16x16x32_bf16 v[80:83], v[108:111], v[200:203], v[80:83]
	v_mfma_f32_16x16x32_bf16 v[72:75], v[124:127], v[200:203], v[72:75]
	v_mfma_f32_16x16x32_bf16 v[148:151], v[112:115], v[168:171], v[148:151]
	v_mfma_f32_16x16x32_bf16 v[132:135], v[136:139], v[168:171], v[132:135]
	v_mfma_f32_16x16x32_bf16 v[120:123], v[112:115], v[188:191], v[120:123]
	v_mfma_f32_16x16x32_bf16 v[104:107], v[136:139], v[188:191], v[104:107]
	v_mfma_f32_16x16x32_bf16 v[96:99], v[112:115], v[196:199], v[96:99]
	v_mfma_f32_16x16x32_bf16 v[88:91], v[136:139], v[196:199], v[88:91]
	v_mfma_f32_16x16x32_bf16 v[80:83], v[112:115], v[208:211], v[80:83]
	v_mfma_f32_16x16x32_bf16 v[72:75], v[136:139], v[208:211], v[72:75]
	s_setprio 0
	s_setprio 1
	v_mfma_f32_16x16x32_bf16 v[144:147], v[140:143], v[164:167], v[144:147]
	v_mfma_f32_16x16x32_bf16 v[128:131], v[156:159], v[164:167], v[128:131]
	v_mfma_f32_16x16x32_bf16 v[116:119], v[140:143], v[172:175], v[116:119]
	v_mfma_f32_16x16x32_bf16 v[100:103], v[156:159], v[172:175], v[100:103]
	v_mfma_f32_16x16x32_bf16 v[92:95], v[140:143], v[192:195], v[92:95]
	v_mfma_f32_16x16x32_bf16 v[84:87], v[156:159], v[192:195], v[84:87]
	v_mfma_f32_16x16x32_bf16 v[76:79], v[140:143], v[200:203], v[76:79]
	v_mfma_f32_16x16x32_bf16 v[68:71], v[156:159], v[200:203], v[68:71]
	v_mfma_f32_16x16x32_bf16 v[144:147], v[152:155], v[168:171], v[144:147]
	v_mfma_f32_16x16x32_bf16 v[128:131], v[160:163], v[168:171], v[128:131]
	v_mfma_f32_16x16x32_bf16 v[116:119], v[152:155], v[188:191], v[116:119]
	v_mfma_f32_16x16x32_bf16 v[100:103], v[160:163], v[188:191], v[100:103]
	v_mfma_f32_16x16x32_bf16 v[92:95], v[152:155], v[196:199], v[92:95]
	v_mfma_f32_16x16x32_bf16 v[84:87], v[160:163], v[196:199], v[84:87]
	v_mfma_f32_16x16x32_bf16 v[76:79], v[152:155], v[208:211], v[76:79]
	v_mfma_f32_16x16x32_bf16 v[68:71], v[160:163], v[208:211], v[68:71]
	s_setprio 0
	s_barrier
	s_add_i32 s58, s58, s41
	v_lshl_add_u64 v[204:205], s[52:53], 0, v[2:3]
	s_mov_b32 m0, s58
	ds_read_b128 v[164:167], v225 offset:16384
	ds_read_b128 v[168:171], v225 offset:17408
	ds_read_b128 v[172:175], v225 offset:18432
	ds_read_b128 v[188:191], v225 offset:19456
	ds_read_b128 v[192:195], v225 offset:20480
	ds_read_b128 v[196:199], v225 offset:21504
	ds_read_b128 v[200:203], v225 offset:22528
	ds_read_b128 v[208:211], v225 offset:23552
	global_load_lds_dwordx4 v[204:205], off
	v_lshl_add_u64 v[212:213], s[52:53], 0, v[180:181]
	s_add_i32 m0, s58, 0x2000
	s_add_i32 s58, s59, s41
	global_load_lds_dwordx4 v[212:213], off
	v_lshl_add_u64 v[214:215], s[52:53], 0, v[176:177]
	s_mov_b32 m0, s58
	v_lshl_add_u64 v[226:227], s[52:53], 0, v[182:183]
	global_load_lds_dwordx4 v[214:215], off
	s_add_i32 m0, s58, 0x2000
	v_lshl_add_u64 v[228:229], s[36:37], 0, v[0:1]
	global_load_lds_dwordx4 v[226:227], off
	s_mov_b32 m0, s55
	v_lshl_add_u64 v[230:231], s[36:37], 0, v[178:179]
	global_load_lds_dwordx4 v[228:229], off
	s_mov_b32 m0, s56
	s_nop 0
	global_load_lds_dwordx4 v[230:231], off
	s_waitcnt vmcnt(8)
	s_waitcnt lgkmcnt(0)
	s_barrier
	s_setprio 1
	s_waitcnt lgkmcnt(0)
	v_mfma_f32_16x16x32_bf16 v[64:67], v[108:111], v[164:167], v[64:67]
	v_mfma_f32_16x16x32_bf16 v[56:59], v[124:127], v[164:167], v[56:59]
	v_mfma_f32_16x16x32_bf16 v[48:51], v[108:111], v[172:175], v[48:51]
	v_mfma_f32_16x16x32_bf16 v[40:43], v[124:127], v[172:175], v[40:43]
	v_mfma_f32_16x16x32_bf16 v[32:35], v[108:111], v[192:195], v[32:35]
	v_mfma_f32_16x16x32_bf16 v[24:27], v[124:127], v[192:195], v[24:27]
	v_mfma_f32_16x16x32_bf16 v[16:19], v[108:111], v[200:203], v[16:19]
	v_mfma_f32_16x16x32_bf16 v[8:11], v[124:127], v[200:203], v[8:11]
	v_mfma_f32_16x16x32_bf16 v[64:67], v[112:115], v[168:171], v[64:67]
	v_mfma_f32_16x16x32_bf16 v[56:59], v[136:139], v[168:171], v[56:59]
	v_mfma_f32_16x16x32_bf16 v[48:51], v[112:115], v[188:191], v[48:51]
	v_mfma_f32_16x16x32_bf16 v[40:43], v[136:139], v[188:191], v[40:43]
	v_mfma_f32_16x16x32_bf16 v[32:35], v[112:115], v[196:199], v[32:35]
	v_mfma_f32_16x16x32_bf16 v[24:27], v[136:139], v[196:199], v[24:27]
	v_mfma_f32_16x16x32_bf16 v[16:19], v[112:115], v[208:211], v[16:19]
	v_mfma_f32_16x16x32_bf16 v[8:11], v[136:139], v[208:211], v[8:11]
	s_setprio 0
	s_setprio 1
	v_mfma_f32_16x16x32_bf16 v[60:63], v[140:143], v[164:167], v[60:63]
	v_mfma_f32_16x16x32_bf16 v[52:55], v[156:159], v[164:167], v[52:55]
	v_mfma_f32_16x16x32_bf16 v[44:47], v[140:143], v[172:175], v[44:47]
	v_mfma_f32_16x16x32_bf16 v[36:39], v[156:159], v[172:175], v[36:39]
	v_mfma_f32_16x16x32_bf16 v[28:31], v[140:143], v[192:195], v[28:31]
	v_mfma_f32_16x16x32_bf16 v[20:23], v[156:159], v[192:195], v[20:23]
	v_mfma_f32_16x16x32_bf16 v[12:15], v[140:143], v[200:203], v[12:15]
	v_mfma_f32_16x16x32_bf16 v[4:7], v[156:159], v[200:203], v[4:7]
	v_mfma_f32_16x16x32_bf16 v[60:63], v[152:155], v[168:171], v[60:63]
	v_mfma_f32_16x16x32_bf16 v[52:55], v[160:163], v[168:171], v[52:55]
	v_mfma_f32_16x16x32_bf16 v[44:47], v[152:155], v[188:191], v[44:47]
	v_mfma_f32_16x16x32_bf16 v[36:39], v[160:163], v[188:191], v[36:39]
	v_mfma_f32_16x16x32_bf16 v[28:31], v[152:155], v[196:199], v[28:31]
	v_mfma_f32_16x16x32_bf16 v[20:23], v[160:163], v[196:199], v[20:23]
	v_mfma_f32_16x16x32_bf16 v[12:15], v[152:155], v[208:211], v[12:15]
	v_mfma_f32_16x16x32_bf16 v[4:7], v[160:163], v[208:211], v[4:7]
	s_setprio 0
	s_barrier
; #define PG8_STAGE(bufoff, gbase, voff) do { _Pragma("unroll") for (int _i = 0; _i < 2; ++_i) \
;         __builtin_amdgcn_global_load_lds((const unsigned*)((const char*)(gbase) + (voff)[_i]), (PG8_LAS unsigned*)(lds + (bufoff) + ldsw + _i * 8192), 16, 0, 0); } while (0)
; #define PG8_LDA(dst, b, h) do { _Pragma("unroll") for (int m = 0; m < 4; ++m) _Pragma("unroll") for (int k = 0; k < 2; ++k) dst[m][k] = *(const PG8_LAS bf16x8*)(lds + PG8_SA(b, h) + aoff + m * 2048 + k * 1024); } while (0)
; #define PG8_LDB(dst, b, h) do { _Pragma("unroll") for (int n = 0; n < 2; ++n) _Pragma("unroll") for (int k = 0; k < 2; ++k) dst[n][k] = *(const PG8_LAS bf16x8*)(lds + PG8_SB(b, h) + boff + n * 2048 + k * 1024); } while (0)
; #define PG8_MMA(ai, bj, At, Bt) do { __builtin_amdgcn_s_setprio(1); _Pragma("unroll") for (int m = 0; m < 4; ++m) _Pragma("unroll") for (int n = 0; n < 2; ++n) _Pragma("unroll") for (int k = 0; k < 2; ++k) \
;         acc[ai][bj][m][n] = __builtin_amdgcn_mfma_f32_16x16x32_bf16(Bt[n][k], At[m][k], acc[ai][bj][m][n], 0, 0, 0); __builtin_amdgcn_s_setprio(0); } while (0)
; #define PG8_WAIT_V(n) asm volatile("s_waitcnt vmcnt(" #n ")" ::: "memory")
; #define PG8_WAIT_L(n) asm volatile("s_waitcnt lgkmcnt(" #n ")" ::: "memory")
; #define PG8_BAR __builtin_amdgcn_s_barrier()
; #define PG8_SCHED __builtin_amdgcn_sched_barrier(0)
; template <class Epi, class Sched, bool ALIGN_EPI = false, bool SP2 = false>
; __device__ __forceinline__ void gemm_phase(PG8_LAS unsigned char* lds, const Gemm g, const Sched& S, const Epi& E, const int tid) {
;     ...
;             PG8_LDB(B0, 1, 0); PG8_LDB(B1, 1, 1); PG8_SCHED; PG8_LDA(At, 1, 0); PG8_STAGE(PG8_SA(0, 1), a2 + hstep, voffA);
;             PG8_WAIT_V(8); PG8_WAIT_L(0); PG8_BAR; PG8_MMA(0, 0, At, B0); PG8_MMA(0, 1, At, B1); PG8_BAR; PG8_SCHED;
	s_add_i32 s52, 0, 0x18000
	s_add_i32 s53, 0, 0x1c000
	v_add_u32_e32 v136, s52, v219
	v_add_u32_e32 v160, s53, v219
	ds_read_b128 v[108:111], v136
	ds_read_b128 v[112:115], v136 offset:1024
	ds_read_b128 v[124:127], v136 offset:2048
	ds_read_b128 v[136:139], v136 offset:3072
	ds_read_b128 v[140:143], v160
	ds_read_b128 v[152:155], v160 offset:1024
	ds_read_b128 v[156:159], v160 offset:2048
	ds_read_b128 v[160:163], v160 offset:3072
	s_add_u32 s36, s36, 0x40000
	s_addc_u32 s37, s37, 0
	s_mov_b32 m0, s57
	v_lshl_add_u64 v[232:233], s[36:37], 0, v[0:1]
	ds_read_b128 v[164:167], v225 offset:32768
	ds_read_b128 v[168:171], v225 offset:33792
	ds_read_b128 v[172:175], v225 offset:34816
	ds_read_b128 v[188:191], v225 offset:35840
	ds_read_b128 v[192:195], v225 offset:36864
	ds_read_b128 v[196:199], v225 offset:37888
	ds_read_b128 v[200:203], v225 offset:38912
	ds_read_b128 v[208:211], v225 offset:39936
	global_load_lds_dwordx4 v[232:233], off
	v_lshl_add_u64 v[232:233], s[36:37], 0, v[178:179]
	s_mov_b32 m0, s60
	s_nop 0
	global_load_lds_dwordx4 v[232:233], off
	s_waitcnt vmcnt(8)
	s_waitcnt lgkmcnt(0)
	s_barrier
	s_setprio 1
	s_waitcnt lgkmcnt(0)
	v_mfma_f32_16x16x32_bf16 v[148:151], v[108:111], v[164:167], v[148:151]
	v_mfma_f32_16x16x32_bf16 v[132:135], v[124:127], v[164:167], v[132:135]
	v_mfma_f32_16x16x32_bf16 v[120:123], v[108:111], v[172:175], v[120:123]
	v_mfma_f32_16x16x32_bf16 v[104:107], v[124:127], v[172:175], v[104:107]
	v_mfma_f32_16x16x32_bf16 v[96:99], v[108:111], v[192:195], v[96:99]
	v_mfma_f32_16x16x32_bf16 v[88:91], v[124:127], v[192:195], v[88:91]
	v_mfma_f32_16x16x32_bf16 v[80:83], v[108:111], v[200:203], v[80:83]
	v_mfma_f32_16x16x32_bf16 v[72:75], v[124:127], v[200:203], v[72:75]
	v_mfma_f32_16x16x32_bf16 v[148:151], v[112:115], v[168:171], v[148:151]
	v_mfma_f32_16x16x32_bf16 v[132:135], v[136:139], v[168:171], v[132:135]
	v_mfma_f32_16x16x32_bf16 v[120:123], v[112:115], v[188:191], v[120:123]
	v_mfma_f32_16x16x32_bf16 v[104:107], v[136:139], v[188:191], v[104:107]
	v_mfma_f32_16x16x32_bf16 v[96:99], v[112:115], v[196:199], v[96:99]
	v_mfma_f32_16x16x32_bf16 v[88:91], v[136:139], v[196:199], v[88:91]
	v_mfma_f32_16x16x32_bf16 v[80:83], v[112:115], v[208:211], v[80:83]
	v_mfma_f32_16x16x32_bf16 v[72:75], v[136:139], v[208:211], v[72:75]
	s_setprio 0
	s_setprio 1
	v_mfma_f32_16x16x32_bf16 v[144:147], v[140:143], v[164:167], v[144:147]
	v_mfma_f32_16x16x32_bf16 v[128:131], v[156:159], v[164:167], v[128:131]
	v_mfma_f32_16x16x32_bf16 v[116:119], v[140:143], v[172:175], v[116:119]
	v_mfma_f32_16x16x32_bf16 v[100:103], v[156:159], v[172:175], v[100:103]
	v_mfma_f32_16x16x32_bf16 v[92:95], v[140:143], v[192:195], v[92:95]
	v_mfma_f32_16x16x32_bf16 v[84:87], v[156:159], v[192:195], v[84:87]
	v_mfma_f32_16x16x32_bf16 v[76:79], v[140:143], v[200:203], v[76:79]
	v_mfma_f32_16x16x32_bf16 v[68:71], v[156:159], v[200:203], v[68:71]
	v_mfma_f32_16x16x32_bf16 v[144:147], v[152:155], v[168:171], v[144:147]
	v_mfma_f32_16x16x32_bf16 v[128:131], v[160:163], v[168:171], v[128:131]
	v_mfma_f32_16x16x32_bf16 v[116:119], v[152:155], v[188:191], v[116:119]
	v_mfma_f32_16x16x32_bf16 v[100:103], v[160:163], v[188:191], v[100:103]
	v_mfma_f32_16x16x32_bf16 v[92:95], v[152:155], v[196:199], v[92:95]
	v_mfma_f32_16x16x32_bf16 v[84:87], v[160:163], v[196:199], v[84:87]
	v_mfma_f32_16x16x32_bf16 v[76:79], v[152:155], v[208:211], v[76:79]
	v_mfma_f32_16x16x32_bf16 v[68:71], v[160:163], v[208:211], v[68:71]
	s_setprio 0
	s_barrier
; #define PG8_STAGE(bufoff, gbase, voff) do { _Pragma("unroll") for (int _i = 0; _i < 2; ++_i) \
;         __builtin_amdgcn_global_load_lds((const unsigned*)((const char*)(gbase) + (voff)[_i]), (PG8_LAS unsigned*)(lds + (bufoff) + ldsw + _i * 8192), 16, 0, 0); } while (0)
; #define PG8_LDA(dst, b, h) do { _Pragma("unroll") for (int m = 0; m < 4; ++m) _Pragma("unroll") for (int k = 0; k < 2; ++k) dst[m][k] = *(const PG8_LAS bf16x8*)(lds + PG8_SA(b, h) + aoff + m * 2048 + k * 1024); } while (0)
; #define PG8_MMA(ai, bj, At, Bt) do { __builtin_amdgcn_s_setprio(1); _Pragma("unroll") for (int m = 0; m < 4; ++m) _Pragma("unroll") for (int n = 0; n < 2; ++n) _Pragma("unroll") for (int k = 0; k < 2; ++k) \
;         acc[ai][bj][m][n] = __builtin_amdgcn_mfma_f32_16x16x32_bf16(Bt[n][k], At[m][k], acc[ai][bj][m][n], 0, 0, 0); __builtin_amdgcn_s_setprio(0); } while (0)
; #define PG8_WAIT_V(n) asm volatile("s_waitcnt vmcnt(" #n ")" ::: "memory")
; #define PG8_WAIT_L(n) asm volatile("s_waitcnt lgkmcnt(" #n ")" ::: "memory")
; #define PG8_BAR __builtin_amdgcn_s_barrier()
; #define PG8_SCHED __builtin_amdgcn_sched_barrier(0)
; template <class Epi, class Sched, bool ALIGN_EPI = false, bool SP2 = false>
; __device__ __forceinline__ void gemm_phase(PG8_LAS unsigned char* lds, const Gemm g, const Sched& S, const Epi& E, const int tid) {
;     ...
;         for (int t = 0; t < nt; t += 2) {
;             const bool last = (t == nt - 2);
;             const char* a1 = cA + (size_t)(t + 1) * kstep;
;             const char* a2 = last ? nA : cA + (size_t)(t + 2) * kstep; const char* b2 = last ? nB : cB + (size_t)(t + 2) * kstep;
;             const char* a3 = a2 + kstep; const char* b3 = b2 + kstep;
;     ...
;             PG8_LDA(At, 1, 1); PG8_STAGE(PG8_SB(1, 0), b3, voffB); PG8_STAGE(PG8_SB(1, 1), b3, voffB1); PG8_STAGE(PG8_SA(1, 0), a3, voffA);
;             PG8_WAIT_V(8); PG8_WAIT_L(0); PG8_BAR; PG8_MMA(1, 0, At, B0); PG8_MMA(1, 1, At, B1); PG8_BAR; PG8_SCHED;
	s_add_i32 s36, s52, s41
	v_lshl_add_u64 v[204:205], v[204:205], 0, s[66:67]
	s_mov_b32 m0, s36
	ds_read_b128 v[164:167], v225 offset:49152
	ds_read_b128 v[168:171], v225 offset:50176
	ds_read_b128 v[172:175], v225 offset:51200
	ds_read_b128 v[188:191], v225 offset:52224
	ds_read_b128 v[192:195], v225 offset:53248
	ds_read_b128 v[196:199], v225 offset:54272
	ds_read_b128 v[200:203], v225 offset:55296
	ds_read_b128 v[208:211], v225 offset:56320
	global_load_lds_dwordx4 v[204:205], off
	v_lshl_add_u64 v[204:205], v[212:213], 0, s[66:67]
	s_add_i32 m0, s36, 0x2000
	s_add_i32 s36, s53, s41
	global_load_lds_dwordx4 v[204:205], off
	v_lshl_add_u64 v[204:205], v[214:215], 0, s[66:67]
	s_mov_b32 m0, s36
	s_nop 0
	global_load_lds_dwordx4 v[204:205], off
	v_lshl_add_u64 v[204:205], v[226:227], 0, s[66:67]
	s_add_i32 m0, s36, 0x2000
	s_nop 0
	global_load_lds_dwordx4 v[204:205], off
	v_lshl_add_u64 v[204:205], v[228:229], 0, s[66:67]
	s_mov_b32 m0, s76
	s_nop 0
	global_load_lds_dwordx4 v[204:205], off
	v_lshl_add_u64 v[204:205], v[230:231], 0, s[66:67]
	s_mov_b32 m0, s77
	s_nop 0
	global_load_lds_dwordx4 v[204:205], off
	s_waitcnt vmcnt(8)
	s_waitcnt lgkmcnt(0)
	s_barrier
	s_setprio 1
	s_waitcnt lgkmcnt(0)
	v_mfma_f32_16x16x32_bf16 v[64:67], v[108:111], v[164:167], v[64:67]
	v_mfma_f32_16x16x32_bf16 v[56:59], v[124:127], v[164:167], v[56:59]
	v_mfma_f32_16x16x32_bf16 v[48:51], v[108:111], v[172:175], v[48:51]
	v_mfma_f32_16x16x32_bf16 v[40:43], v[124:127], v[172:175], v[40:43]
	v_mfma_f32_16x16x32_bf16 v[32:35], v[108:111], v[192:195], v[32:35]
	v_mfma_f32_16x16x32_bf16 v[24:27], v[124:127], v[192:195], v[24:27]
	v_mfma_f32_16x16x32_bf16 v[16:19], v[108:111], v[200:203], v[16:19]
	v_mfma_f32_16x16x32_bf16 v[8:11], v[124:127], v[200:203], v[8:11]
	v_mfma_f32_16x16x32_bf16 v[64:67], v[112:115], v[168:171], v[64:67]
	s_add_i32 s51, s51, 2
	v_mfma_f32_16x16x32_bf16 v[56:59], v[136:139], v[168:171], v[56:59]
	s_add_u32 s46, s46, 0x100
	v_mfma_f32_16x16x32_bf16 v[48:51], v[112:115], v[188:191], v[48:51]
	s_addc_u32 s47, s47, 0
	v_mfma_f32_16x16x32_bf16 v[40:43], v[136:139], v[188:191], v[40:43]
	s_add_u32 s49, s49, 0x100
	v_mfma_f32_16x16x32_bf16 v[32:35], v[112:115], v[196:199], v[32:35]
	s_addc_u32 s50, s50, 0
	v_mfma_f32_16x16x32_bf16 v[24:27], v[136:139], v[196:199], v[24:27]
	s_add_u32 s36, s46, 0xfffc0080
	v_mfma_f32_16x16x32_bf16 v[16:19], v[112:115], v[208:211], v[16:19]
	s_addc_u32 s37, s47, -1
	v_mfma_f32_16x16x32_bf16 v[8:11], v[136:139], v[208:211], v[8:11]
	s_add_i32 s58, 0, 0x10000
	s_setprio 0
	s_setprio 1
	v_mfma_f32_16x16x32_bf16 v[60:63], v[140:143], v[164:167], v[60:63]
	s_cmp_eq_u32 s51, 12
	v_mfma_f32_16x16x32_bf16 v[52:55], v[156:159], v[164:167], v[52:55]
	s_cselect_b32 s37, s11, s37
	v_mfma_f32_16x16x32_bf16 v[44:47], v[140:143], v[172:175], v[44:47]
	s_cselect_b32 s36, s40, s36
	v_mfma_f32_16x16x32_bf16 v[36:39], v[156:159], v[172:175], v[36:39]
	s_cselect_b32 s53, s9, s50
	v_mfma_f32_16x16x32_bf16 v[28:31], v[140:143], v[192:195], v[28:31]
	s_cselect_b32 s52, s45, s49
	v_mfma_f32_16x16x32_bf16 v[20:23], v[156:159], v[192:195], v[20:23]
	s_add_i32 s59, 0, 0x14000
	v_mfma_f32_16x16x32_bf16 v[12:15], v[140:143], v[200:203], v[12:15]
	s_cmp_gt_u32 s51, 13
	v_mfma_f32_16x16x32_bf16 v[4:7], v[156:159], v[200:203], v[4:7]
	v_mfma_f32_16x16x32_bf16 v[60:63], v[152:155], v[168:171], v[60:63]
	v_mfma_f32_16x16x32_bf16 v[52:55], v[160:163], v[168:171], v[52:55]
	v_mfma_f32_16x16x32_bf16 v[44:47], v[152:155], v[188:191], v[44:47]
	v_mfma_f32_16x16x32_bf16 v[36:39], v[160:163], v[188:191], v[36:39]
	v_mfma_f32_16x16x32_bf16 v[28:31], v[152:155], v[196:199], v[28:31]
	v_mfma_f32_16x16x32_bf16 v[20:23], v[160:163], v[196:199], v[20:23]
	v_mfma_f32_16x16x32_bf16 v[12:15], v[152:155], v[208:211], v[12:15]
	v_mfma_f32_16x16x32_bf16 v[4:7], v[160:163], v[208:211], v[4:7]
	s_setprio 0
	s_barrier
	s_cbranch_scc0 .LBB0_343
	s_and_b64 vcc, exec, s[6:7]
	s_cbranch_vccz .LBB0_346
	s_barrier

; #define PG8_STAGE(bufoff, gbase, voff) do { _Pragma("unroll") for (int _i = 0; _i < 2; ++_i) \
;         __builtin_amdgcn_global_load_lds((const unsigned*)((const char*)(gbase) + (voff)[_i]), (PG8_LAS unsigned*)(lds + (bufoff) + ldsw + _i * 8192), 16, 0, 0); } while (0)
; #define PG8_LDA(dst, b, h) do { _Pragma("unroll") for (int m = 0; m < 4; ++m) _Pragma("unroll") for (int k = 0; k < 2; ++k) dst[m][k] = *(const PG8_LAS bf16x8*)(lds + PG8_SA(b, h) + aoff + m * 2048 + k * 1024); } while (0)
; #define PG8_LDB(dst, b, h) do { _Pragma("unroll") for (int n = 0; n < 2; ++n) _Pragma("unroll") for (int k = 0; k < 2; ++k) dst[n][k] = *(const PG8_LAS bf16x8*)(lds + PG8_SB(b, h) + boff + n * 2048 + k * 1024); } while (0)
; #define PG8_WAIT_V(n) asm volatile("s_waitcnt vmcnt(" #n ")" ::: "memory")
; #define PG8_WAIT_L(n) asm volatile("s_waitcnt lgkmcnt(" #n ")" ::: "memory")
; #define PG8_BAR __builtin_amdgcn_s_barrier()
; template <class Epi, class Sched, bool ALIGN_EPI = false, bool SP2 = false>
; __device__ __forceinline__ void gemm_phase(PG8_LAS unsigned char* lds, const Gemm g, const Sched& S, const Epi& E, const int tid) {
;     ...
;         const bool has_next = S.next(ui + 1, nxt);
;         const char* nA = has_next ? (const char*)g.A + (size_t)nxt.pm * tstep : cA; const char* nB = has_next ? (const char*)g.Bt + (size_t)nxt.pn * tstep : cB;
;         for (int t = 0; t < nt; t += 2) {
;             const bool last = (t == nt - 2);
;             const char* a1 = cA + (size_t)(t + 1) * kstep;
;             const char* a2 = last ? nA : cA + (size_t)(t + 2) * kstep; const char* b2 = last ? nB : cB + (size_t)(t + 2) * kstep;
;             const char* a3 = a2 + kstep; const char* b3 = b2 + kstep;
;             if (last && has_next) S.a_ready(nxt);
;             if constexpr (SP2) {
;             PG8_LDB(B0, 0, 0); PG8_LDB(B1, 0, 1); PG8_SCHED; PG8_LDA(At, 0, 0); PG8_STAGE(PG8_SA(1, 1), a1 + hstep, voffA);
;             PG8_WAIT_V(8); PG8_WAIT_L(0); PG8_BAR; PG8_MMA(0, 0, At, B0); PG8_MMA(0, 1, At, B1); PG8_BAR; PG8_SCHED;
;     ...
; #pragma unroll
;         for (int a = 0; a < 2; ++a)
; #pragma unroll
;             for (int b = 0; b < 2; ++b)
; #pragma unroll
;                 for (int m = 0; m < 4; ++m)
; #pragma unroll
;                     for (int n = 0; n < 2; ++n) acc[a][b][m][n] = (f32x4){0.f, 0.f, 0.f, 0.f};
;         cur = nxt; cA = nA; cB = nB; ++ui;
.LBB0_577:
	s_add_u32 s0, s0, 0x80
	s_addc_u32 s1, s1, 0
	s_add_u32 s36, s8, 0x100
	v_mov_b32_e32 v4, 0
	s_addc_u32 s37, s9, 0
	s_mov_b32 s8, 0
	s_waitcnt lgkmcnt(0)
	v_mov_b32_e32 v5, v4
	v_mov_b32_e32 v6, v4
	v_mov_b32_e32 v7, v4
	v_mov_b32_e32 v8, v4
	v_mov_b32_e32 v9, v4
	v_mov_b32_e32 v10, v4
	v_mov_b32_e32 v11, v4
	v_mov_b32_e32 v20, v4
	v_mov_b32_e32 v21, v4
	v_mov_b32_e32 v22, v4
	v_mov_b32_e32 v23, v4
	v_mov_b32_e32 v24, v4
	v_mov_b32_e32 v25, v4
	v_mov_b32_e32 v26, v4
	v_mov_b32_e32 v27, v4
	v_mov_b32_e32 v36, v4
	v_mov_b32_e32 v37, v4
	v_mov_b32_e32 v38, v4
	v_mov_b32_e32 v39, v4
	v_mov_b32_e32 v40, v4
	v_mov_b32_e32 v41, v4
	v_mov_b32_e32 v42, v4
	v_mov_b32_e32 v43, v4
	v_mov_b32_e32 v52, v4
	v_mov_b32_e32 v53, v4
	v_mov_b32_e32 v54, v4
	v_mov_b32_e32 v55, v4
	v_mov_b32_e32 v56, v4
	v_mov_b32_e32 v57, v4
	v_mov_b32_e32 v58, v4
	v_mov_b32_e32 v59, v4
	v_mov_b32_e32 v12, v4
	v_mov_b32_e32 v13, v4
	v_mov_b32_e32 v14, v4
	v_mov_b32_e32 v15, v4
	v_mov_b32_e32 v16, v4
	v_mov_b32_e32 v17, v4
	v_mov_b32_e32 v18, v4
	v_mov_b32_e32 v19, v4
	v_mov_b32_e32 v28, v4
	v_mov_b32_e32 v29, v4
	v_mov_b32_e32 v30, v4
	v_mov_b32_e32 v31, v4
	v_mov_b32_e32 v32, v4
	v_mov_b32_e32 v33, v4
	v_mov_b32_e32 v34, v4
	v_mov_b32_e32 v35, v4
	v_mov_b32_e32 v44, v4
	v_mov_b32_e32 v45, v4
	v_mov_b32_e32 v46, v4
	v_mov_b32_e32 v47, v4
	v_mov_b32_e32 v48, v4
	v_mov_b32_e32 v49, v4
	v_mov_b32_e32 v50, v4
	v_mov_b32_e32 v51, v4
	v_mov_b32_e32 v64, v4
	v_mov_b32_e32 v65, v4
	v_mov_b32_e32 v66, v4
	v_mov_b32_e32 v67, v4
	v_mov_b32_e32 v72, v4
	v_mov_b32_e32 v73, v4
	v_mov_b32_e32 v74, v4
	v_mov_b32_e32 v75, v4
	s_waitcnt vmcnt(0)
	v_mov_b32_e32 v84, v4
	v_mov_b32_e32 v85, v4
	v_mov_b32_e32 v86, v4
	v_mov_b32_e32 v87, v4
	v_mov_b32_e32 v88, v4
	v_mov_b32_e32 v89, v4
	v_mov_b32_e32 v90, v4
	v_mov_b32_e32 v91, v4
	v_mov_b32_e32 v100, v4
	v_mov_b32_e32 v101, v4
	v_mov_b32_e32 v102, v4
	v_mov_b32_e32 v103, v4
	v_mov_b32_e32 v104, v4
	v_mov_b32_e32 v105, v4
	v_mov_b32_e32 v106, v4
	v_mov_b32_e32 v107, v4
	v_mov_b32_e32 v116, v4
	v_mov_b32_e32 v117, v4
	v_mov_b32_e32 v118, v4
	v_mov_b32_e32 v119, v4
	v_mov_b32_e32 v120, v4
	v_mov_b32_e32 v121, v4
	v_mov_b32_e32 v122, v4
	v_mov_b32_e32 v123, v4
	v_mov_b32_e32 v132, v4
	v_mov_b32_e32 v133, v4
	v_mov_b32_e32 v134, v4
	v_mov_b32_e32 v135, v4
	v_mov_b32_e32 v136, v4
	v_mov_b32_e32 v137, v4
	v_mov_b32_e32 v138, v4
	v_mov_b32_e32 v139, v4
	v_mov_b32_e32 v92, v4
	v_mov_b32_e32 v93, v4
	v_mov_b32_e32 v94, v4
	v_mov_b32_e32 v95, v4
	v_mov_b32_e32 v96, v4
	v_mov_b32_e32 v97, v4
	v_mov_b32_e32 v98, v4
	v_mov_b32_e32 v99, v4
	v_mov_b32_e32 v108, v4
	v_mov_b32_e32 v109, v4
	v_mov_b32_e32 v110, v4
	v_mov_b32_e32 v111, v4
	v_mov_b32_e32 v112, v4
	v_mov_b32_e32 v113, v4
	v_mov_b32_e32 v114, v4
	v_mov_b32_e32 v115, v4
	v_mov_b32_e32 v124, v4
	v_mov_b32_e32 v125, v4
	v_mov_b32_e32 v126, v4
	v_mov_b32_e32 v127, v4
	v_mov_b32_e32 v128, v4
	v_mov_b32_e32 v129, v4
	v_mov_b32_e32 v130, v4
	v_mov_b32_e32 v131, v4
	v_mov_b32_e32 v140, v4
	v_mov_b32_e32 v141, v4
	v_mov_b32_e32 v142, v4
	v_mov_b32_e32 v143, v4
	v_mov_b32_e32 v144, v4
	v_mov_b32_e32 v145, v4
	v_mov_b32_e32 v146, v4
	v_mov_b32_e32 v147, v4
	s_add_i32 s38, s8, 2
	s_add_u32 s39, s0, 0x80
	s_addc_u32 s9, s1, 0
	s_add_i32 s42, 0, 0x10000
	s_cmp_eq_u32 s85, s8
	s_cselect_b32 s9, s57, s9
	s_cselect_b32 s8, s56, s39
	s_cselect_b32 s41, s45, s37
	s_cselect_b32 s40, s44, s36
	s_add_i32 s39, 0, 0x14000
.LBB0_578:
	v_add_u32_e32 v80, s42, v230
	v_add_u32_e32 v160, s39, v230
	ds_read_b128 v[60:63], v80
	ds_read_b128 v[68:71], v80 offset:1024
	ds_read_b128 v[76:79], v80 offset:2048
	ds_read_b128 v[80:83], v80 offset:3072
	ds_read_b128 v[148:151], v160
	ds_read_b128 v[152:155], v160 offset:1024
	ds_read_b128 v[156:159], v160 offset:2048
	ds_read_b128 v[160:163], v160 offset:3072
	v_lshl_add_u64 v[200:201], s[0:1], 0, v[188:189]
	s_add_i32 m0, s68, 0xc000
	ds_read_b128 v[164:167], v245
	ds_read_b128 v[168:171], v245 offset:1024
	ds_read_b128 v[172:175], v245 offset:2048
	ds_read_b128 v[176:179], v245 offset:3072
	ds_read_b128 v[192:195], v245 offset:4096
	ds_read_b128 v[196:199], v245 offset:5120
	ds_read_b128 v[212:215], v245 offset:6144
	ds_read_b128 v[216:219], v245 offset:7168
	global_load_lds_dwordx4 v[200:201], off
	v_lshl_add_u64 v[200:201], s[0:1], 0, v[190:191]
	s_add_i32 m0, s68, 0xe000
	s_nop 0
	global_load_lds_dwordx4 v[200:201], off
	s_waitcnt vmcnt(8)
	s_waitcnt lgkmcnt(0)
	s_barrier
	s_setprio 1
	s_waitcnt lgkmcnt(0)
	v_mfma_f32_16x16x32_bf16 v[144:147], v[60:63], v[164:167], v[144:147]
	v_mfma_f32_16x16x32_bf16 v[140:143], v[76:79], v[164:167], v[140:143]
	v_mfma_f32_16x16x32_bf16 v[128:131], v[60:63], v[172:175], v[128:131]
	v_mfma_f32_16x16x32_bf16 v[124:127], v[76:79], v[172:175], v[124:127]
	v_mfma_f32_16x16x32_bf16 v[112:115], v[60:63], v[192:195], v[112:115]
	v_mfma_f32_16x16x32_bf16 v[108:111], v[76:79], v[192:195], v[108:111]
	v_mfma_f32_16x16x32_bf16 v[96:99], v[60:63], v[212:215], v[96:99]
	v_mfma_f32_16x16x32_bf16 v[92:95], v[76:79], v[212:215], v[92:95]
	v_mfma_f32_16x16x32_bf16 v[144:147], v[68:71], v[168:171], v[144:147]
	v_mfma_f32_16x16x32_bf16 v[140:143], v[80:83], v[168:171], v[140:143]
	v_mfma_f32_16x16x32_bf16 v[128:131], v[68:71], v[176:179], v[128:131]
	v_mfma_f32_16x16x32_bf16 v[124:127], v[80:83], v[176:179], v[124:127]
	v_mfma_f32_16x16x32_bf16 v[112:115], v[68:71], v[196:199], v[112:115]
	v_mfma_f32_16x16x32_bf16 v[108:111], v[80:83], v[196:199], v[108:111]
	v_mfma_f32_16x16x32_bf16 v[96:99], v[68:71], v[216:219], v[96:99]
	v_mfma_f32_16x16x32_bf16 v[92:95], v[80:83], v[216:219], v[92:95]
	s_setprio 0
	s_setprio 1
	v_mfma_f32_16x16x32_bf16 v[136:139], v[148:151], v[164:167], v[136:139]
	v_mfma_f32_16x16x32_bf16 v[132:135], v[156:159], v[164:167], v[132:135]
	v_mfma_f32_16x16x32_bf16 v[120:123], v[148:151], v[172:175], v[120:123]
	v_mfma_f32_16x16x32_bf16 v[116:119], v[156:159], v[172:175], v[116:119]
	v_mfma_f32_16x16x32_bf16 v[104:107], v[148:151], v[192:195], v[104:107]
	v_mfma_f32_16x16x32_bf16 v[100:103], v[156:159], v[192:195], v[100:103]
	v_mfma_f32_16x16x32_bf16 v[88:91], v[148:151], v[212:215], v[88:91]
	v_mfma_f32_16x16x32_bf16 v[84:87], v[156:159], v[212:215], v[84:87]
	v_mfma_f32_16x16x32_bf16 v[136:139], v[152:155], v[168:171], v[136:139]
	v_mfma_f32_16x16x32_bf16 v[132:135], v[160:163], v[168:171], v[132:135]
	v_mfma_f32_16x16x32_bf16 v[120:123], v[152:155], v[176:179], v[120:123]
	v_mfma_f32_16x16x32_bf16 v[116:119], v[160:163], v[176:179], v[116:119]
	v_mfma_f32_16x16x32_bf16 v[104:107], v[152:155], v[196:199], v[104:107]
	v_mfma_f32_16x16x32_bf16 v[100:103], v[160:163], v[196:199], v[100:103]
	v_mfma_f32_16x16x32_bf16 v[88:91], v[152:155], v[216:219], v[88:91]
	v_mfma_f32_16x16x32_bf16 v[84:87], v[160:163], v[216:219], v[84:87]
	s_setprio 0
	s_barrier
; #define PG8_STAGE(bufoff, gbase, voff) do { _Pragma("unroll") for (int _i = 0; _i < 2; ++_i) \
;         __builtin_amdgcn_global_load_lds((const unsigned*)((const char*)(gbase) + (voff)[_i]), (PG8_LAS unsigned*)(lds + (bufoff) + ldsw + _i * 8192), 16, 0, 0); } while (0)
; #define PG8_LDA(dst, b, h) do { _Pragma("unroll") for (int m = 0; m < 4; ++m) _Pragma("unroll") for (int k = 0; k < 2; ++k) dst[m][k] = *(const PG8_LAS bf16x8*)(lds + PG8_SA(b, h) + aoff + m * 2048 + k * 1024); } while (0)
; #define PG8_LDB(dst, b, h) do { _Pragma("unroll") for (int n = 0; n < 2; ++n) _Pragma("unroll") for (int k = 0; k < 2; ++k) dst[n][k] = *(const PG8_LAS bf16x8*)(lds + PG8_SB(b, h) + boff + n * 2048 + k * 1024); } while (0)
; #define PG8_MMA(ai, bj, At, Bt) do { __builtin_amdgcn_s_setprio(1); _Pragma("unroll") for (int m = 0; m < 4; ++m) _Pragma("unroll") for (int n = 0; n < 2; ++n) _Pragma("unroll") for (int k = 0; k < 2; ++k) \
;         acc[ai][bj][m][n] = __builtin_amdgcn_mfma_f32_16x16x32_bf16(Bt[n][k], At[m][k], acc[ai][bj][m][n], 0, 0, 0); __builtin_amdgcn_s_setprio(0); } while (0)
; #define PG8_WAIT_V(n) asm volatile("s_waitcnt vmcnt(" #n ")" ::: "memory")
; #define PG8_WAIT_L(n) asm volatile("s_waitcnt lgkmcnt(" #n ")" ::: "memory")
; #define PG8_BAR __builtin_amdgcn_s_barrier()
; #define PG8_SCHED __builtin_amdgcn_sched_barrier(0)
; template <class Epi, class Sched, bool ALIGN_EPI = false, bool SP2 = false>
; __device__ __forceinline__ void gemm_phase(PG8_LAS unsigned char* lds, const Gemm g, const Sched& S, const Epi& E, const int tid) {
;     ...
;             PG8_LDA(At, 0, 1); PG8_STAGE(PG8_SB(0, 0), b2, voffB); PG8_STAGE(PG8_SB(0, 1), b2, voffB1); PG8_STAGE(PG8_SA(0, 0), a2, voffA);
;             PG8_WAIT_V(8); PG8_WAIT_L(0); PG8_BAR; PG8_MMA(1, 0, At, B0); PG8_MMA(1, 1, At, B1); PG8_BAR; PG8_SCHED;
;             PG8_LDB(B0, 1, 0); PG8_LDB(B1, 1, 1); PG8_SCHED; PG8_LDA(At, 1, 0); PG8_STAGE(PG8_SA(0, 1), a2 + hstep, voffA);
;             PG8_WAIT_V(8); PG8_WAIT_L(0); PG8_BAR; PG8_MMA(0, 0, At, B0); PG8_MMA(0, 1, At, B1); PG8_BAR; PG8_SCHED;
	s_add_i32 s42, s42, s73
	v_lshl_add_u64 v[200:201], s[40:41], 0, v[2:3]
	s_mov_b32 m0, s42
	ds_read_b128 v[164:167], v245 offset:16384
	ds_read_b128 v[168:171], v245 offset:17408
	ds_read_b128 v[172:175], v245 offset:18432
	ds_read_b128 v[176:179], v245 offset:19456
	ds_read_b128 v[192:195], v245 offset:20480
	ds_read_b128 v[196:199], v245 offset:21504
	ds_read_b128 v[212:215], v245 offset:22528
	ds_read_b128 v[216:219], v245 offset:23552
	global_load_lds_dwordx4 v[200:201], off
	v_lshl_add_u64 v[202:203], s[40:41], 0, v[184:185]
	s_add_i32 m0, s42, 0x2000
	s_add_i32 s39, s39, s73
	global_load_lds_dwordx4 v[202:203], off
	v_lshl_add_u64 v[204:205], s[40:41], 0, v[180:181]
	s_mov_b32 m0, s39
	v_lshl_add_u64 v[208:209], s[40:41], 0, v[186:187]
	global_load_lds_dwordx4 v[204:205], off
	s_add_i32 m0, s39, 0x2000
	v_lshl_add_u64 v[210:211], s[8:9], 0, v[0:1]
	global_load_lds_dwordx4 v[208:209], off
	s_mov_b32 m0, s68
	v_lshl_add_u64 v[220:221], s[8:9], 0, v[182:183]
	global_load_lds_dwordx4 v[210:211], off
	s_mov_b32 m0, s33
	s_nop 0
	global_load_lds_dwordx4 v[220:221], off
	s_waitcnt vmcnt(8)
	s_waitcnt lgkmcnt(0)
	s_barrier
	s_setprio 1
	s_waitcnt lgkmcnt(0)
	v_mfma_f32_16x16x32_bf16 v[72:75], v[60:63], v[164:167], v[72:75]
	v_mfma_f32_16x16x32_bf16 v[64:67], v[76:79], v[164:167], v[64:67]
	v_mfma_f32_16x16x32_bf16 v[48:51], v[60:63], v[172:175], v[48:51]
	v_mfma_f32_16x16x32_bf16 v[44:47], v[76:79], v[172:175], v[44:47]
	v_mfma_f32_16x16x32_bf16 v[32:35], v[60:63], v[192:195], v[32:35]
	v_mfma_f32_16x16x32_bf16 v[28:31], v[76:79], v[192:195], v[28:31]
	v_mfma_f32_16x16x32_bf16 v[16:19], v[60:63], v[212:215], v[16:19]
	v_mfma_f32_16x16x32_bf16 v[12:15], v[76:79], v[212:215], v[12:15]
	v_mfma_f32_16x16x32_bf16 v[72:75], v[68:71], v[168:171], v[72:75]
	v_mfma_f32_16x16x32_bf16 v[64:67], v[80:83], v[168:171], v[64:67]
	v_mfma_f32_16x16x32_bf16 v[48:51], v[68:71], v[176:179], v[48:51]
	v_mfma_f32_16x16x32_bf16 v[44:47], v[80:83], v[176:179], v[44:47]
	v_mfma_f32_16x16x32_bf16 v[32:35], v[68:71], v[196:199], v[32:35]
	v_mfma_f32_16x16x32_bf16 v[28:31], v[80:83], v[196:199], v[28:31]
	v_mfma_f32_16x16x32_bf16 v[16:19], v[68:71], v[216:219], v[16:19]
	v_mfma_f32_16x16x32_bf16 v[12:15], v[80:83], v[216:219], v[12:15]
	s_setprio 0
	s_setprio 1
	v_mfma_f32_16x16x32_bf16 v[56:59], v[148:151], v[164:167], v[56:59]
	v_mfma_f32_16x16x32_bf16 v[52:55], v[156:159], v[164:167], v[52:55]
	v_mfma_f32_16x16x32_bf16 v[40:43], v[148:151], v[172:175], v[40:43]
	v_mfma_f32_16x16x32_bf16 v[36:39], v[156:159], v[172:175], v[36:39]
	v_mfma_f32_16x16x32_bf16 v[24:27], v[148:151], v[192:195], v[24:27]
	v_mfma_f32_16x16x32_bf16 v[20:23], v[156:159], v[192:195], v[20:23]
	v_mfma_f32_16x16x32_bf16 v[8:11], v[148:151], v[212:215], v[8:11]
	v_mfma_f32_16x16x32_bf16 v[4:7], v[156:159], v[212:215], v[4:7]
	v_mfma_f32_16x16x32_bf16 v[56:59], v[152:155], v[168:171], v[56:59]
	v_mfma_f32_16x16x32_bf16 v[52:55], v[160:163], v[168:171], v[52:55]
	v_mfma_f32_16x16x32_bf16 v[40:43], v[152:155], v[176:179], v[40:43]
	v_mfma_f32_16x16x32_bf16 v[36:39], v[160:163], v[176:179], v[36:39]
	v_mfma_f32_16x16x32_bf16 v[24:27], v[152:155], v[196:199], v[24:27]
	v_mfma_f32_16x16x32_bf16 v[20:23], v[160:163], v[196:199], v[20:23]
	v_mfma_f32_16x16x32_bf16 v[8:11], v[152:155], v[216:219], v[8:11]
	v_mfma_f32_16x16x32_bf16 v[4:7], v[160:163], v[216:219], v[4:7]
	s_setprio 0
	s_barrier
	s_add_i32 s39, 0, 0x18000
	s_add_i32 s40, 0, 0x1c000
	v_add_u32_e32 v80, s39, v230
	v_add_u32_e32 v160, s40, v230
	ds_read_b128 v[60:63], v80
	ds_read_b128 v[68:71], v80 offset:1024
	ds_read_b128 v[76:79], v80 offset:2048
	ds_read_b128 v[80:83], v80 offset:3072
	ds_read_b128 v[148:151], v160
	ds_read_b128 v[152:155], v160 offset:1024
	ds_read_b128 v[156:159], v160 offset:2048
	ds_read_b128 v[160:163], v160 offset:3072
	s_add_u32 s8, s8, s60
	s_addc_u32 s9, s9, 0
	s_mov_b32 m0, s62
	v_lshl_add_u64 v[222:223], s[8:9], 0, v[0:1]
	ds_read_b128 v[164:167], v245 offset:32768
	ds_read_b128 v[168:171], v245 offset:33792
	ds_read_b128 v[172:175], v245 offset:34816
	ds_read_b128 v[176:179], v245 offset:35840
	ds_read_b128 v[192:195], v245 offset:36864
	ds_read_b128 v[196:199], v245 offset:37888
	ds_read_b128 v[212:215], v245 offset:38912
	ds_read_b128 v[216:219], v245 offset:39936
	global_load_lds_dwordx4 v[222:223], off
	v_lshl_add_u64 v[222:223], s[8:9], 0, v[182:183]
	s_mov_b32 m0, s63
	s_nop 0
	global_load_lds_dwordx4 v[222:223], off
	s_waitcnt vmcnt(8)
	s_waitcnt lgkmcnt(0)
	s_barrier
; #define PG8_STAGE(bufoff, gbase, voff) do { _Pragma("unroll") for (int _i = 0; _i < 2; ++_i) \
;         __builtin_amdgcn_global_load_lds((const unsigned*)((const char*)(gbase) + (voff)[_i]), (PG8_LAS unsigned*)(lds + (bufoff) + ldsw + _i * 8192), 16, 0, 0); } while (0)
; #define PG8_LDA(dst, b, h) do { _Pragma("unroll") for (int m = 0; m < 4; ++m) _Pragma("unroll") for (int k = 0; k < 2; ++k) dst[m][k] = *(const PG8_LAS bf16x8*)(lds + PG8_SA(b, h) + aoff + m * 2048 + k * 1024); } while (0)
; #define PG8_LDB(dst, b, h) do { _Pragma("unroll") for (int n = 0; n < 2; ++n) _Pragma("unroll") for (int k = 0; k < 2; ++k) dst[n][k] = *(const PG8_LAS bf16x8*)(lds + PG8_SB(b, h) + boff + n * 2048 + k * 1024); } while (0)
; #define PG8_MMA(ai, bj, At, Bt) do { __builtin_amdgcn_s_setprio(1); _Pragma("unroll") for (int m = 0; m < 4; ++m) _Pragma("unroll") for (int n = 0; n < 2; ++n) _Pragma("unroll") for (int k = 0; k < 2; ++k) \
;         acc[ai][bj][m][n] = __builtin_amdgcn_mfma_f32_16x16x32_bf16(Bt[n][k], At[m][k], acc[ai][bj][m][n], 0, 0, 0); __builtin_amdgcn_s_setprio(0); } while (0)
; #define PG8_WAIT_V(n) asm volatile("s_waitcnt vmcnt(" #n ")" ::: "memory")
; #define PG8_WAIT_L(n) asm volatile("s_waitcnt lgkmcnt(" #n ")" ::: "memory")
; #define PG8_BAR __builtin_amdgcn_s_barrier()
; template <class Epi, class Sched, bool ALIGN_EPI = false, bool SP2 = false>
; __device__ __forceinline__ void gemm_phase(PG8_LAS unsigned char* lds, const Gemm g, const Sched& S, const Epi& E, const int tid) {
;     ...
;         for (int t = 0; t < nt; t += 2) {
;             const bool last = (t == nt - 2);
;             const char* a1 = cA + (size_t)(t + 1) * kstep;
;             const char* a2 = last ? nA : cA + (size_t)(t + 2) * kstep; const char* b2 = last ? nB : cB + (size_t)(t + 2) * kstep;
;             const char* a3 = a2 + kstep; const char* b3 = b2 + kstep;
;     ...
;             PG8_LDB(B0, 1, 0); PG8_LDB(B1, 1, 1); PG8_SCHED; PG8_LDA(At, 1, 0); PG8_STAGE(PG8_SA(0, 1), a2 + hstep, voffA);
;             PG8_WAIT_V(8); PG8_WAIT_L(0); PG8_BAR; PG8_MMA(0, 0, At, B0); PG8_MMA(0, 1, At, B1); PG8_BAR; PG8_SCHED;
;             PG8_LDA(At, 1, 1); PG8_STAGE(PG8_SB(1, 0), b3, voffB); PG8_STAGE(PG8_SB(1, 1), b3, voffB1); PG8_STAGE(PG8_SA(1, 0), a3, voffA);
;             PG8_WAIT_V(8); PG8_WAIT_L(0); PG8_BAR; PG8_MMA(1, 0, At, B0); PG8_MMA(1, 1, At, B1); PG8_BAR; PG8_SCHED;
	s_setprio 1
	s_waitcnt lgkmcnt(0)
	v_mfma_f32_16x16x32_bf16 v[144:147], v[60:63], v[164:167], v[144:147]
	v_mfma_f32_16x16x32_bf16 v[140:143], v[76:79], v[164:167], v[140:143]
	v_mfma_f32_16x16x32_bf16 v[128:131], v[60:63], v[172:175], v[128:131]
	v_mfma_f32_16x16x32_bf16 v[124:127], v[76:79], v[172:175], v[124:127]
	v_mfma_f32_16x16x32_bf16 v[112:115], v[60:63], v[192:195], v[112:115]
	v_mfma_f32_16x16x32_bf16 v[108:111], v[76:79], v[192:195], v[108:111]
	v_mfma_f32_16x16x32_bf16 v[96:99], v[60:63], v[212:215], v[96:99]
	v_mfma_f32_16x16x32_bf16 v[92:95], v[76:79], v[212:215], v[92:95]
	v_mfma_f32_16x16x32_bf16 v[144:147], v[68:71], v[168:171], v[144:147]
	v_mfma_f32_16x16x32_bf16 v[140:143], v[80:83], v[168:171], v[140:143]
	v_mfma_f32_16x16x32_bf16 v[128:131], v[68:71], v[176:179], v[128:131]
	v_mfma_f32_16x16x32_bf16 v[124:127], v[80:83], v[176:179], v[124:127]
	v_mfma_f32_16x16x32_bf16 v[112:115], v[68:71], v[196:199], v[112:115]
	v_mfma_f32_16x16x32_bf16 v[108:111], v[80:83], v[196:199], v[108:111]
	v_mfma_f32_16x16x32_bf16 v[96:99], v[68:71], v[216:219], v[96:99]
	v_mfma_f32_16x16x32_bf16 v[92:95], v[80:83], v[216:219], v[92:95]
	s_setprio 0
	s_setprio 1
	v_mfma_f32_16x16x32_bf16 v[136:139], v[148:151], v[164:167], v[136:139]
	v_mfma_f32_16x16x32_bf16 v[132:135], v[156:159], v[164:167], v[132:135]
	v_mfma_f32_16x16x32_bf16 v[120:123], v[148:151], v[172:175], v[120:123]
	v_mfma_f32_16x16x32_bf16 v[116:119], v[156:159], v[172:175], v[116:119]
	v_mfma_f32_16x16x32_bf16 v[104:107], v[148:151], v[192:195], v[104:107]
	v_mfma_f32_16x16x32_bf16 v[100:103], v[156:159], v[192:195], v[100:103]
	v_mfma_f32_16x16x32_bf16 v[88:91], v[148:151], v[212:215], v[88:91]
	v_mfma_f32_16x16x32_bf16 v[84:87], v[156:159], v[212:215], v[84:87]
	v_mfma_f32_16x16x32_bf16 v[136:139], v[152:155], v[168:171], v[136:139]
	v_mfma_f32_16x16x32_bf16 v[132:135], v[160:163], v[168:171], v[132:135]
	v_mfma_f32_16x16x32_bf16 v[120:123], v[152:155], v[176:179], v[120:123]
	v_mfma_f32_16x16x32_bf16 v[116:119], v[160:163], v[176:179], v[116:119]
	v_mfma_f32_16x16x32_bf16 v[104:107], v[152:155], v[196:199], v[104:107]
	v_mfma_f32_16x16x32_bf16 v[100:103], v[160:163], v[196:199], v[100:103]
	v_mfma_f32_16x16x32_bf16 v[88:91], v[152:155], v[216:219], v[88:91]
	v_mfma_f32_16x16x32_bf16 v[84:87], v[160:163], v[216:219], v[84:87]
	s_setprio 0
	s_barrier
	s_add_i32 s8, s39, s73
	v_lshl_add_u64 v[200:201], v[200:201], 0, s[66:67]
	s_mov_b32 m0, s8
	ds_read_b128 v[164:167], v245 offset:49152
	ds_read_b128 v[168:171], v245 offset:50176
	ds_read_b128 v[172:175], v245 offset:51200
	ds_read_b128 v[176:179], v245 offset:52224
	ds_read_b128 v[192:195], v245 offset:53248
	ds_read_b128 v[196:199], v245 offset:54272
	ds_read_b128 v[212:215], v245 offset:55296
	ds_read_b128 v[216:219], v245 offset:56320
	global_load_lds_dwordx4 v[200:201], off
	v_lshl_add_u64 v[200:201], v[202:203], 0, s[66:67]
	s_add_i32 m0, s8, 0x2000
	s_add_i32 s8, s40, s73
	global_load_lds_dwordx4 v[200:201], off
	v_lshl_add_u64 v[200:201], v[204:205], 0, s[66:67]
	s_mov_b32 m0, s8
	s_nop 0
	global_load_lds_dwordx4 v[200:201], off
	v_lshl_add_u64 v[200:201], v[208:209], 0, s[66:67]
	s_add_i32 m0, s8, 0x2000
	s_nop 0
	global_load_lds_dwordx4 v[200:201], off
	v_lshl_add_u64 v[200:201], v[210:211], 0, s[66:67]
	s_mov_b32 m0, s96
	s_nop 0
	global_load_lds_dwordx4 v[200:201], off
	v_lshl_add_u64 v[200:201], v[220:221], 0, s[66:67]
	s_mov_b32 m0, s97
	s_nop 0
	global_load_lds_dwordx4 v[200:201], off
	s_waitcnt vmcnt(8)
	s_waitcnt lgkmcnt(0)
	s_barrier
	s_setprio 1
	s_waitcnt lgkmcnt(0)
	v_mfma_f32_16x16x32_bf16 v[72:75], v[60:63], v[164:167], v[72:75]
	v_mfma_f32_16x16x32_bf16 v[64:67], v[76:79], v[164:167], v[64:67]
	v_mfma_f32_16x16x32_bf16 v[48:51], v[60:63], v[172:175], v[48:51]
	v_mfma_f32_16x16x32_bf16 v[44:47], v[76:79], v[172:175], v[44:47]
	v_mfma_f32_16x16x32_bf16 v[32:35], v[60:63], v[192:195], v[32:35]
	v_mfma_f32_16x16x32_bf16 v[28:31], v[76:79], v[192:195], v[28:31]
	v_mfma_f32_16x16x32_bf16 v[16:19], v[60:63], v[212:215], v[16:19]
	v_mfma_f32_16x16x32_bf16 v[12:15], v[76:79], v[212:215], v[12:15]
	v_mfma_f32_16x16x32_bf16 v[72:75], v[68:71], v[168:171], v[72:75]
	s_add_u32 s0, s0, 0x100
	v_mfma_f32_16x16x32_bf16 v[64:67], v[80:83], v[168:171], v[64:67]
	s_addc_u32 s1, s1, 0
	v_mfma_f32_16x16x32_bf16 v[48:51], v[68:71], v[176:179], v[48:51]
	s_add_u32 s36, s36, 0x100
	v_mfma_f32_16x16x32_bf16 v[44:47], v[80:83], v[176:179], v[44:47]
	s_addc_u32 s37, s37, 0
	v_mfma_f32_16x16x32_bf16 v[32:35], v[68:71], v[196:199], v[32:35]
	s_cmp_ge_u32 s38, s49
	v_mfma_f32_16x16x32_bf16 v[28:31], v[80:83], v[196:199], v[28:31]
	s_cselect_b32 s32, 1, 0
	v_mfma_f32_16x16x32_bf16 v[16:19], v[68:71], v[216:219], v[16:19]
	s_mov_b32 s8, s38
	v_mfma_f32_16x16x32_bf16 v[12:15], v[80:83], v[216:219], v[12:15]
	s_add_i32 s38, s8, 2
	s_setprio 0
	s_setprio 1
	v_mfma_f32_16x16x32_bf16 v[56:59], v[148:151], v[164:167], v[56:59]
	s_add_u32 s39, s0, 0x80
	v_mfma_f32_16x16x32_bf16 v[52:55], v[156:159], v[164:167], v[52:55]
	s_addc_u32 s9, s1, 0
	v_mfma_f32_16x16x32_bf16 v[40:43], v[148:151], v[172:175], v[40:43]
	s_add_i32 s42, 0, 0x10000
	v_mfma_f32_16x16x32_bf16 v[36:39], v[156:159], v[172:175], v[36:39]
	s_cmp_eq_u32 s85, s8
	v_mfma_f32_16x16x32_bf16 v[24:27], v[148:151], v[192:195], v[24:27]
	s_cselect_b32 s9, s57, s9
	v_mfma_f32_16x16x32_bf16 v[20:23], v[156:159], v[192:195], v[20:23]
	s_cselect_b32 s8, s56, s39
	v_mfma_f32_16x16x32_bf16 v[8:11], v[148:151], v[212:215], v[8:11]
	s_cselect_b32 s41, s45, s37
	v_mfma_f32_16x16x32_bf16 v[4:7], v[156:159], v[212:215], v[4:7]
	s_cselect_b32 s40, s44, s36
	v_mfma_f32_16x16x32_bf16 v[56:59], v[152:155], v[168:171], v[56:59]
	s_add_i32 s39, 0, 0x14000
	v_mfma_f32_16x16x32_bf16 v[52:55], v[160:163], v[168:171], v[52:55]
	s_cmp_lg_u32 s32, 0
	v_mfma_f32_16x16x32_bf16 v[40:43], v[152:155], v[176:179], v[40:43]
	v_mfma_f32_16x16x32_bf16 v[36:39], v[160:163], v[176:179], v[36:39]
	v_mfma_f32_16x16x32_bf16 v[24:27], v[152:155], v[196:199], v[24:27]
	v_mfma_f32_16x16x32_bf16 v[20:23], v[160:163], v[196:199], v[20:23]
	v_mfma_f32_16x16x32_bf16 v[8:11], v[152:155], v[216:219], v[8:11]
	v_mfma_f32_16x16x32_bf16 v[4:7], v[160:163], v[216:219], v[4:7]
	s_setprio 0
	s_barrier
	s_cbranch_scc0 .LBB0_578
	s_and_b64 vcc, exec, s[80:81]
	s_cbranch_vccz .LBB0_581
	s_barrier

; #define PG8_STAGE(bufoff, gbase, voff) do { _Pragma("unroll") for (int _i = 0; _i < 2; ++_i) \
;         __builtin_amdgcn_global_load_lds((const unsigned*)((const char*)(gbase) + (voff)[_i]), (PG8_LAS unsigned*)(lds + (bufoff) + ldsw + _i * 8192), 16, 0, 0); } while (0)
; #define PG8_LDA(dst, b, h) do { _Pragma("unroll") for (int m = 0; m < 4; ++m) _Pragma("unroll") for (int k = 0; k < 2; ++k) dst[m][k] = *(const PG8_LAS bf16x8*)(lds + PG8_SA(b, h) + aoff + m * 2048 + k * 1024); } while (0)
; #define PG8_LDB(dst, b, h) do { _Pragma("unroll") for (int n = 0; n < 2; ++n) _Pragma("unroll") for (int k = 0; k < 2; ++k) dst[n][k] = *(const PG8_LAS bf16x8*)(lds + PG8_SB(b, h) + boff + n * 2048 + k * 1024); } while (0)
; #define PG8_MMA(ai, bj, At, Bt) do { __builtin_amdgcn_s_setprio(1); _Pragma("unroll") for (int m = 0; m < 4; ++m) _Pragma("unroll") for (int n = 0; n < 2; ++n) _Pragma("unroll") for (int k = 0; k < 2; ++k) \
;         acc[ai][bj][m][n] = __builtin_amdgcn_mfma_f32_16x16x32_bf16(Bt[n][k], At[m][k], acc[ai][bj][m][n], 0, 0, 0); __builtin_amdgcn_s_setprio(0); } while (0)
; #define PG8_WAIT_V(n) asm volatile("s_waitcnt vmcnt(" #n ")" ::: "memory")
; #define PG8_BAR __builtin_amdgcn_s_barrier()
; template <class Epi, class Sched, bool ALIGN_EPI = false, bool SP2 = false>
; __device__ __forceinline__ void gemm_phase(PG8_LAS unsigned char* lds, const Gemm g, const Sched& S, const Epi& E, const int tid) {
;     ...
;         for (int t = 0; t < nt; t += 2) {
;             const bool last = (t == nt - 2);
;             const char* a1 = cA + (size_t)(t + 1) * kstep;
;             const char* a2 = last ? nA : cA + (size_t)(t + 2) * kstep; const char* b2 = last ? nB : cB + (size_t)(t + 2) * kstep;
;             const char* a3 = a2 + kstep; const char* b3 = b2 + kstep;
;             if (last && has_next) S.a_ready(nxt);
;             if constexpr (SP2) {
;             PG8_LDB(B0, 0, 0); PG8_LDB(B1, 0, 1); PG8_SCHED; PG8_LDA(At, 0, 0); PG8_STAGE(PG8_SA(1, 1), a1 + hstep, voffA);
;             PG8_WAIT_V(8); PG8_WAIT_L(0); PG8_BAR; PG8_MMA(0, 0, At, B0); PG8_MMA(0, 1, At, B1); PG8_BAR; PG8_SCHED;
;             PG8_LDA(At, 0, 1); PG8_STAGE(PG8_SB(0, 0), b2, voffB); PG8_STAGE(PG8_SB(0, 1), b2, voffB1); PG8_STAGE(PG8_SA(0, 0), a2, voffA);
;             PG8_WAIT_V(8); PG8_WAIT_L(0); PG8_BAR; PG8_MMA(1, 0, At, B0); PG8_MMA(1, 1, At, B1); PG8_BAR; PG8_SCHED;
.LBB0_724:
.LBB0_726:
	s_add_u32 s46, s46, 0x40080
	s_addc_u32 s47, s47, 0
	s_add_u32 s52, s52, 0x100
	s_addc_u32 s53, s53, 0
	s_mov_b32 s62, -2
	s_add_u32 s36, s46, 0xfffc0080
	s_addc_u32 s37, s47, -1
	s_add_i32 s63, 0, 0x10000
	s_cmp_eq_u32 s62, 12
	s_cselect_b32 s37, s11, s37
	s_cselect_b32 s36, s59, s36
	v_add_u32_e32 v148, s63, v151
	s_cselect_b32 s73, s9, s53
	s_cselect_b32 s72, s60, s52
	s_add_i32 s68, 0, 0x14000
	ds_read_b128 v[144:147], v148
	ds_read_b128 v[156:159], v148 offset:1024
	ds_read_b128 v[160:163], v148 offset:2048
	ds_read_b128 v[164:167], v148 offset:3072
	v_add_u32_e32 v148, s68, v151
	ds_read_b128 v[168:171], v148
	ds_read_b128 v[172:175], v148 offset:1024
	ds_read_b128 v[176:179], v148 offset:2048
	ds_read_b128 v[180:183], v148 offset:3072
	v_lshl_add_u64 v[148:149], s[46:47], 0, v[140:141]
	s_add_i32 m0, s43, 0xc000
	ds_read_b128 v[184:187], v154
	ds_read_b128 v[188:191], v154 offset:1024
	ds_read_b128 v[192:195], v154 offset:2048
	ds_read_b128 v[196:199], v154 offset:3072
	ds_read_b128 v[212:215], v154 offset:4096
	ds_read_b128 v[216:219], v154 offset:5120
	ds_read_b128 v[220:223], v154 offset:6144
	ds_read_b128 v[224:227], v154 offset:7168
	global_load_lds_dwordx4 v[148:149], off
	v_lshl_add_u64 v[148:149], s[46:47], 0, v[142:143]
	s_add_i32 m0, s43, 0xe000
	s_nop 0
	global_load_lds_dwordx4 v[148:149], off
	s_waitcnt vmcnt(8)
	s_waitcnt lgkmcnt(0)
	s_barrier
	s_setprio 1
	s_waitcnt lgkmcnt(0)
	v_mfma_f32_16x16x32_bf16 v[128:131], v[144:147], v[184:187], 0
	v_mfma_f32_16x16x32_bf16 v[120:123], v[160:163], v[184:187], 0
	v_mfma_f32_16x16x32_bf16 v[112:115], v[144:147], v[192:195], 0
	v_mfma_f32_16x16x32_bf16 v[104:107], v[160:163], v[192:195], 0
	v_mfma_f32_16x16x32_bf16 v[96:99], v[144:147], v[212:215], 0
	v_mfma_f32_16x16x32_bf16 v[88:91], v[160:163], v[212:215], 0
	v_mfma_f32_16x16x32_bf16 v[80:83], v[144:147], v[220:223], 0
	v_mfma_f32_16x16x32_bf16 v[72:75], v[160:163], v[220:223], 0
	v_mfma_f32_16x16x32_bf16 v[128:131], v[156:159], v[188:191], v[128:131]
	v_mfma_f32_16x16x32_bf16 v[120:123], v[164:167], v[188:191], v[120:123]
	v_mfma_f32_16x16x32_bf16 v[112:115], v[156:159], v[196:199], v[112:115]
	v_mfma_f32_16x16x32_bf16 v[104:107], v[164:167], v[196:199], v[104:107]
	v_mfma_f32_16x16x32_bf16 v[96:99], v[156:159], v[216:219], v[96:99]
	v_mfma_f32_16x16x32_bf16 v[88:91], v[164:167], v[216:219], v[88:91]
	v_mfma_f32_16x16x32_bf16 v[80:83], v[156:159], v[224:227], v[80:83]
	v_mfma_f32_16x16x32_bf16 v[72:75], v[164:167], v[224:227], v[72:75]
	s_setprio 0
	s_setprio 1
	v_mfma_f32_16x16x32_bf16 v[124:127], v[168:171], v[184:187], 0
	v_mfma_f32_16x16x32_bf16 v[116:119], v[176:179], v[184:187], 0
	v_mfma_f32_16x16x32_bf16 v[108:111], v[168:171], v[192:195], 0
	v_mfma_f32_16x16x32_bf16 v[100:103], v[176:179], v[192:195], 0
	v_mfma_f32_16x16x32_bf16 v[92:95], v[168:171], v[212:215], 0
	v_mfma_f32_16x16x32_bf16 v[84:87], v[176:179], v[212:215], 0
	v_mfma_f32_16x16x32_bf16 v[76:79], v[168:171], v[220:223], 0
	v_mfma_f32_16x16x32_bf16 v[68:71], v[176:179], v[220:223], 0
	v_mfma_f32_16x16x32_bf16 v[124:127], v[172:175], v[188:191], v[124:127]
	v_mfma_f32_16x16x32_bf16 v[116:119], v[180:183], v[188:191], v[116:119]
	v_mfma_f32_16x16x32_bf16 v[108:111], v[172:175], v[196:199], v[108:111]
	v_mfma_f32_16x16x32_bf16 v[100:103], v[180:183], v[196:199], v[100:103]
	v_mfma_f32_16x16x32_bf16 v[92:95], v[172:175], v[216:219], v[92:95]
	v_mfma_f32_16x16x32_bf16 v[84:87], v[180:183], v[216:219], v[84:87]
	v_mfma_f32_16x16x32_bf16 v[76:79], v[172:175], v[224:227], v[76:79]
	v_mfma_f32_16x16x32_bf16 v[68:71], v[180:183], v[224:227], v[68:71]
	s_setprio 0
	s_barrier
	s_add_i32 s63, s63, s33
	v_lshl_add_u64 v[148:149], s[72:73], 0, v[2:3]
	s_mov_b32 m0, s63
	ds_read_b128 v[184:187], v154 offset:16384
	ds_read_b128 v[188:191], v154 offset:17408
	ds_read_b128 v[192:195], v154 offset:18432
	ds_read_b128 v[196:199], v154 offset:19456
	ds_read_b128 v[212:215], v154 offset:20480
	ds_read_b128 v[216:219], v154 offset:21504
	ds_read_b128 v[220:223], v154 offset:22528
	ds_read_b128 v[224:227], v154 offset:23552
	global_load_lds_dwordx4 v[148:149], off
	v_lshl_add_u64 v[200:201], s[72:73], 0, v[132:133]
	s_add_i32 m0, s63, 0x2000
	s_add_i32 s63, s68, s33
	global_load_lds_dwordx4 v[200:201], off
	v_lshl_add_u64 v[202:203], s[72:73], 0, v[136:137]
	s_mov_b32 m0, s63
	v_lshl_add_u64 v[204:205], s[72:73], 0, v[0:1]
	global_load_lds_dwordx4 v[202:203], off
	s_add_i32 m0, s63, 0x2000
	v_lshl_add_u64 v[208:209], s[36:37], 0, v[138:139]
	global_load_lds_dwordx4 v[204:205], off
	s_mov_b32 m0, s43
	v_lshl_add_u64 v[210:211], s[36:37], 0, v[134:135]
	global_load_lds_dwordx4 v[208:209], off
	s_mov_b32 m0, s45
	s_nop 0
	global_load_lds_dwordx4 v[210:211], off
	s_waitcnt vmcnt(8)
	s_waitcnt lgkmcnt(0)
	s_barrier
; #define PG8_STAGE(bufoff, gbase, voff) do { _Pragma("unroll") for (int _i = 0; _i < 2; ++_i) \
;         __builtin_amdgcn_global_load_lds((const unsigned*)((const char*)(gbase) + (voff)[_i]), (PG8_LAS unsigned*)(lds + (bufoff) + ldsw + _i * 8192), 16, 0, 0); } while (0)
; #define PG8_LDA(dst, b, h) do { _Pragma("unroll") for (int m = 0; m < 4; ++m) _Pragma("unroll") for (int k = 0; k < 2; ++k) dst[m][k] = *(const PG8_LAS bf16x8*)(lds + PG8_SA(b, h) + aoff + m * 2048 + k * 1024); } while (0)
; #define PG8_LDB(dst, b, h) do { _Pragma("unroll") for (int n = 0; n < 2; ++n) _Pragma("unroll") for (int k = 0; k < 2; ++k) dst[n][k] = *(const PG8_LAS bf16x8*)(lds + PG8_SB(b, h) + boff + n * 2048 + k * 1024); } while (0)
; #define PG8_MMA(ai, bj, At, Bt) do { __builtin_amdgcn_s_setprio(1); _Pragma("unroll") for (int m = 0; m < 4; ++m) _Pragma("unroll") for (int n = 0; n < 2; ++n) _Pragma("unroll") for (int k = 0; k < 2; ++k) \
;         acc[ai][bj][m][n] = __builtin_amdgcn_mfma_f32_16x16x32_bf16(Bt[n][k], At[m][k], acc[ai][bj][m][n], 0, 0, 0); __builtin_amdgcn_s_setprio(0); } while (0)
; #define PG8_WAIT_V(n) asm volatile("s_waitcnt vmcnt(" #n ")" ::: "memory")
; #define PG8_WAIT_L(n) asm volatile("s_waitcnt lgkmcnt(" #n ")" ::: "memory")
; #define PG8_BAR __builtin_amdgcn_s_barrier()
; #define PG8_SCHED __builtin_amdgcn_sched_barrier(0)
; template <class Epi, class Sched, bool ALIGN_EPI = false, bool SP2 = false>
; __device__ __forceinline__ void gemm_phase(PG8_LAS unsigned char* lds, const Gemm g, const Sched& S, const Epi& E, const int tid) {
;     ...
;             PG8_WAIT_V(8); PG8_WAIT_L(0); PG8_BAR; PG8_MMA(1, 0, At, B0); PG8_MMA(1, 1, At, B1); PG8_BAR; PG8_SCHED;
;             PG8_LDB(B0, 1, 0); PG8_LDB(B1, 1, 1); PG8_SCHED; PG8_LDA(At, 1, 0); PG8_STAGE(PG8_SA(0, 1), a2 + hstep, voffA);
;             PG8_WAIT_V(8); PG8_WAIT_L(0); PG8_BAR; PG8_MMA(0, 0, At, B0); PG8_MMA(0, 1, At, B1); PG8_BAR; PG8_SCHED;
	s_setprio 1
	s_waitcnt lgkmcnt(0)
	v_mfma_f32_16x16x32_bf16 v[64:67], v[144:147], v[184:187], 0
	v_mfma_f32_16x16x32_bf16 v[56:59], v[160:163], v[184:187], 0
	v_mfma_f32_16x16x32_bf16 v[48:51], v[144:147], v[192:195], 0
	v_mfma_f32_16x16x32_bf16 v[40:43], v[160:163], v[192:195], 0
	v_mfma_f32_16x16x32_bf16 v[32:35], v[144:147], v[212:215], 0
	v_mfma_f32_16x16x32_bf16 v[24:27], v[160:163], v[212:215], 0
	v_mfma_f32_16x16x32_bf16 v[16:19], v[144:147], v[220:223], 0
	v_mfma_f32_16x16x32_bf16 v[8:11], v[160:163], v[220:223], 0
	v_mfma_f32_16x16x32_bf16 v[64:67], v[156:159], v[188:191], v[64:67]
	v_mfma_f32_16x16x32_bf16 v[56:59], v[164:167], v[188:191], v[56:59]
	v_mfma_f32_16x16x32_bf16 v[48:51], v[156:159], v[196:199], v[48:51]
	v_mfma_f32_16x16x32_bf16 v[40:43], v[164:167], v[196:199], v[40:43]
	v_mfma_f32_16x16x32_bf16 v[32:35], v[156:159], v[216:219], v[32:35]
	v_mfma_f32_16x16x32_bf16 v[24:27], v[164:167], v[216:219], v[24:27]
	v_mfma_f32_16x16x32_bf16 v[16:19], v[156:159], v[224:227], v[16:19]
	v_mfma_f32_16x16x32_bf16 v[8:11], v[164:167], v[224:227], v[8:11]
	s_setprio 0
	s_setprio 1
	v_mfma_f32_16x16x32_bf16 v[60:63], v[168:171], v[184:187], 0
	v_mfma_f32_16x16x32_bf16 v[52:55], v[176:179], v[184:187], 0
	v_mfma_f32_16x16x32_bf16 v[44:47], v[168:171], v[192:195], 0
	v_mfma_f32_16x16x32_bf16 v[36:39], v[176:179], v[192:195], 0
	v_mfma_f32_16x16x32_bf16 v[28:31], v[168:171], v[212:215], 0
	v_mfma_f32_16x16x32_bf16 v[20:23], v[176:179], v[212:215], 0
	v_mfma_f32_16x16x32_bf16 v[12:15], v[168:171], v[220:223], 0
	v_mfma_f32_16x16x32_bf16 v[4:7], v[176:179], v[220:223], 0
	v_mfma_f32_16x16x32_bf16 v[60:63], v[172:175], v[188:191], v[60:63]
	v_mfma_f32_16x16x32_bf16 v[52:55], v[180:183], v[188:191], v[52:55]
	v_mfma_f32_16x16x32_bf16 v[44:47], v[172:175], v[196:199], v[44:47]
	v_mfma_f32_16x16x32_bf16 v[36:39], v[180:183], v[196:199], v[36:39]
	v_mfma_f32_16x16x32_bf16 v[28:31], v[172:175], v[216:219], v[28:31]
	v_mfma_f32_16x16x32_bf16 v[20:23], v[180:183], v[216:219], v[20:23]
	v_mfma_f32_16x16x32_bf16 v[12:15], v[172:175], v[224:227], v[12:15]
	v_mfma_f32_16x16x32_bf16 v[4:7], v[180:183], v[224:227], v[4:7]
	s_setprio 0
	s_barrier
	s_add_i32 s63, 0, 0x18000
	v_add_u32_e32 v155, s63, v151
	s_add_i32 s68, 0, 0x1c000
	ds_read_b128 v[144:147], v155
	ds_read_b128 v[156:159], v155 offset:1024
	ds_read_b128 v[160:163], v155 offset:2048
	ds_read_b128 v[164:167], v155 offset:3072
	v_add_u32_e32 v155, s68, v151
	ds_read_b128 v[168:171], v155
	ds_read_b128 v[172:175], v155 offset:1024
	ds_read_b128 v[176:179], v155 offset:2048
	ds_read_b128 v[180:183], v155 offset:3072
	s_add_u32 s36, s36, 0x40000
	s_addc_u32 s37, s37, 0
	s_mov_b32 m0, s48
	v_lshl_add_u64 v[228:229], s[36:37], 0, v[138:139]
	ds_read_b128 v[184:187], v154 offset:32768
	ds_read_b128 v[188:191], v154 offset:33792
	ds_read_b128 v[192:195], v154 offset:34816
	ds_read_b128 v[196:199], v154 offset:35840
	ds_read_b128 v[212:215], v154 offset:36864
	ds_read_b128 v[216:219], v154 offset:37888
	ds_read_b128 v[220:223], v154 offset:38912
	ds_read_b128 v[224:227], v154 offset:39936
	global_load_lds_dwordx4 v[228:229], off
	v_lshl_add_u64 v[228:229], s[36:37], 0, v[134:135]
	s_mov_b32 m0, s49
	s_nop 0
	global_load_lds_dwordx4 v[228:229], off
	s_waitcnt vmcnt(8)
	s_waitcnt lgkmcnt(0)
	s_barrier
	s_setprio 1
	s_waitcnt lgkmcnt(0)
	v_mfma_f32_16x16x32_bf16 v[128:131], v[144:147], v[184:187], v[128:131]
	v_mfma_f32_16x16x32_bf16 v[120:123], v[160:163], v[184:187], v[120:123]
	v_mfma_f32_16x16x32_bf16 v[112:115], v[144:147], v[192:195], v[112:115]
	v_mfma_f32_16x16x32_bf16 v[104:107], v[160:163], v[192:195], v[104:107]
	v_mfma_f32_16x16x32_bf16 v[96:99], v[144:147], v[212:215], v[96:99]
	v_mfma_f32_16x16x32_bf16 v[88:91], v[160:163], v[212:215], v[88:91]
	v_mfma_f32_16x16x32_bf16 v[80:83], v[144:147], v[220:223], v[80:83]
	v_mfma_f32_16x16x32_bf16 v[72:75], v[160:163], v[220:223], v[72:75]
	v_mfma_f32_16x16x32_bf16 v[128:131], v[156:159], v[188:191], v[128:131]
	v_mfma_f32_16x16x32_bf16 v[120:123], v[164:167], v[188:191], v[120:123]
	v_mfma_f32_16x16x32_bf16 v[112:115], v[156:159], v[196:199], v[112:115]
	v_mfma_f32_16x16x32_bf16 v[104:107], v[164:167], v[196:199], v[104:107]
	v_mfma_f32_16x16x32_bf16 v[96:99], v[156:159], v[216:219], v[96:99]
	v_mfma_f32_16x16x32_bf16 v[88:91], v[164:167], v[216:219], v[88:91]
	v_mfma_f32_16x16x32_bf16 v[80:83], v[156:159], v[224:227], v[80:83]
	v_mfma_f32_16x16x32_bf16 v[72:75], v[164:167], v[224:227], v[72:75]
	s_setprio 0
	s_setprio 1
	v_mfma_f32_16x16x32_bf16 v[124:127], v[168:171], v[184:187], v[124:127]
	v_mfma_f32_16x16x32_bf16 v[116:119], v[176:179], v[184:187], v[116:119]
	v_mfma_f32_16x16x32_bf16 v[108:111], v[168:171], v[192:195], v[108:111]
	v_mfma_f32_16x16x32_bf16 v[100:103], v[176:179], v[192:195], v[100:103]
	v_mfma_f32_16x16x32_bf16 v[92:95], v[168:171], v[212:215], v[92:95]
	v_mfma_f32_16x16x32_bf16 v[84:87], v[176:179], v[212:215], v[84:87]
	v_mfma_f32_16x16x32_bf16 v[76:79], v[168:171], v[220:223], v[76:79]
	v_mfma_f32_16x16x32_bf16 v[68:71], v[176:179], v[220:223], v[68:71]
	v_mfma_f32_16x16x32_bf16 v[124:127], v[172:175], v[188:191], v[124:127]
	v_mfma_f32_16x16x32_bf16 v[116:119], v[180:183], v[188:191], v[116:119]
	v_mfma_f32_16x16x32_bf16 v[108:111], v[172:175], v[196:199], v[108:111]
	v_mfma_f32_16x16x32_bf16 v[100:103], v[180:183], v[196:199], v[100:103]
	v_mfma_f32_16x16x32_bf16 v[92:95], v[172:175], v[216:219], v[92:95]
	v_mfma_f32_16x16x32_bf16 v[84:87], v[180:183], v[216:219], v[84:87]
	v_mfma_f32_16x16x32_bf16 v[76:79], v[172:175], v[224:227], v[76:79]
	v_mfma_f32_16x16x32_bf16 v[68:71], v[180:183], v[224:227], v[68:71]
	s_setprio 0
	s_barrier
; #define PG8_WAIT_V(n) asm volatile("s_waitcnt vmcnt(" #n ")" ::: "memory")
;     __host__ __device__ bool next(int i, Unit& u) const {
;         const long L = (long)i * G + c; if (L >= nwg) return false;
;         int wgid = (int)L; { const int q = nwg / NXCD, r = nwg % NXCD, xcd = wgid % NXCD, off = wgid / NXCD; wgid = (xcd < r ? xcd * (q + 1) : r * (q + 1) + (xcd - r) * q) + off; }
;         const int nig = WGM * nN, gid = wgid / nig, fm = gid * WGM, gsz = (nM - fm) < WGM ? (nM - fm) : WGM;
;         u.pm = fm + ((wgid % nig) % gsz); u.pn = (wgid % nig) / gsz; u.idx = i; return true;
; template <class Epi, class Sched, bool ALIGN_EPI = false, bool SP2 = false>
; __device__ __forceinline__ void gemm_phase(PG8_LAS unsigned char* lds, const Gemm g, const Sched& S, const Epi& E, const int tid) {
;     ...
;         const bool has_next = S.next(ui + 1, nxt);
;         const char* nA = has_next ? (const char*)g.A + (size_t)nxt.pm * tstep : cA; const char* nB = has_next ? (const char*)g.Bt + (size_t)nxt.pn * tstep : cB;
;         for (int t = 0; t < nt; t += 2) {
;             const bool last = (t == nt - 2);
;             const char* a1 = cA + (size_t)(t + 1) * kstep;
;             const char* a2 = last ? nA : cA + (size_t)(t + 2) * kstep; const char* b2 = last ? nB : cB + (size_t)(t + 2) * kstep;
;             const char* a3 = a2 + kstep; const char* b3 = b2 + kstep;
;             if (last && has_next) S.a_ready(nxt);
;             if constexpr (SP2) {
;             PG8_LDB(B0, 0, 0); PG8_LDB(B1, 0, 1); PG8_SCHED; PG8_LDA(At, 0, 0); PG8_STAGE(PG8_SA(1, 1), a1 + hstep, voffA);
;             PG8_WAIT_V(8); PG8_WAIT_L(0); PG8_BAR; PG8_MMA(0, 0, At, B0); PG8_MMA(0, 1, At, B1); PG8_BAR; PG8_SCHED;
;             PG8_LDA(At, 0, 1); PG8_STAGE(PG8_SB(0, 0), b2, voffB); PG8_STAGE(PG8_SB(0, 1), b2, voffB1); PG8_STAGE(PG8_SA(0, 0), a2, voffA);
;             PG8_WAIT_V(8); PG8_WAIT_L(0); PG8_BAR; PG8_MMA(1, 0, At, B0); PG8_MMA(1, 1, At, B1); PG8_BAR; PG8_SCHED;
;             PG8_LDB(B0, 1, 0); PG8_LDB(B1, 1, 1); PG8_SCHED; PG8_LDA(At, 1, 0); PG8_STAGE(PG8_SA(0, 1), a2 + hstep, voffA);
;             PG8_WAIT_V(8); PG8_WAIT_L(0); PG8_BAR; PG8_MMA(0, 0, At, B0); PG8_MMA(0, 1, At, B1); PG8_BAR; PG8_SCHED;
;             PG8_LDA(At, 1, 1); PG8_STAGE(PG8_SB(1, 0), b3, voffB); PG8_STAGE(PG8_SB(1, 1), b3, voffB1); PG8_STAGE(PG8_SA(1, 0), a3, voffA);
	s_add_i32 s36, s63, s33
	v_lshl_add_u64 v[148:149], v[148:149], 0, s[66:67]
	s_mov_b32 m0, s36
	ds_read_b128 v[184:187], v154 offset:49152
	ds_read_b128 v[188:191], v154 offset:50176
	ds_read_b128 v[192:195], v154 offset:51200
	ds_read_b128 v[196:199], v154 offset:52224
	ds_read_b128 v[212:215], v154 offset:53248
	ds_read_b128 v[216:219], v154 offset:54272
	ds_read_b128 v[220:223], v154 offset:55296
	ds_read_b128 v[224:227], v154 offset:56320
	global_load_lds_dwordx4 v[148:149], off
	v_lshl_add_u64 v[148:149], v[200:201], 0, s[66:67]
	s_add_i32 m0, s36, 0x2000
	s_add_i32 s36, s68, s33
	global_load_lds_dwordx4 v[148:149], off
	v_lshl_add_u64 v[148:149], v[202:203], 0, s[66:67]
	s_mov_b32 m0, s36
	s_nop 0
	global_load_lds_dwordx4 v[148:149], off
	v_lshl_add_u64 v[148:149], v[204:205], 0, s[66:67]
	s_add_i32 m0, s36, 0x2000
	s_nop 0
	global_load_lds_dwordx4 v[148:149], off
	v_lshl_add_u64 v[148:149], v[208:209], 0, s[66:67]
	s_mov_b32 m0, s50
	s_nop 0
	global_load_lds_dwordx4 v[148:149], off
	v_lshl_add_u64 v[148:149], v[210:211], 0, s[66:67]
	s_mov_b32 m0, s51
	s_nop 0
	global_load_lds_dwordx4 v[148:149], off
	s_waitcnt vmcnt(8)
	s_waitcnt lgkmcnt(0)
	s_barrier
	s_setprio 1
	s_waitcnt lgkmcnt(0)
	v_mfma_f32_16x16x32_bf16 v[64:67], v[144:147], v[184:187], v[64:67]
	s_add_i32 s55, s55, 1
	s_mul_i32 s2, s55, s54
	s_mul_hi_u32 s3, s55, s88
	v_mfma_f32_16x16x32_bf16 v[56:59], v[160:163], v[184:187], v[56:59]
	s_add_i32 s3, s3, s2
	s_mul_i32 s2, s55, s88
	s_add_u32 s12, s2, s90
	v_mfma_f32_16x16x32_bf16 v[48:51], v[144:147], v[192:195], v[48:51]
	s_addc_u32 s13, s3, s42
	v_mov_b64_e32 v[242:243], 0xb00
	v_cmp_lt_i64_e64 s[2:3], s[12:13], v[242:243]
	v_mfma_f32_16x16x32_bf16 v[40:43], v[160:163], v[192:195], v[40:43]
	s_ashr_i32 s8, s12, 31
	s_lshr_b32 s8, s8, 29
	s_add_i32 s8, s12, s8
	v_mfma_f32_16x16x32_bf16 v[32:35], v[144:147], v[212:215], v[32:35]
	s_ashr_i32 s9, s8, 3
	s_and_b32 s8, s8, -8
	s_sub_i32 s8, s12, s8
	v_mfma_f32_16x16x32_bf16 v[24:27], v[160:163], v[212:215], v[24:27]
	s_cmp_lt_i32 s8, 0
	s_movk_i32 s10, 0x161
	s_cselect_b32 s10, s10, 0x160
	v_mfma_f32_16x16x32_bf16 v[16:19], v[144:147], v[220:223], v[16:19]
	s_mul_i32 s8, s8, s10
	s_add_i32 s8, s8, s9
	s_mul_hi_i32 s9, s8, 0x2e8ba2e9
	v_mfma_f32_16x16x32_bf16 v[8:11], v[160:163], v[220:223], v[8:11]
	s_lshr_b32 s10, s9, 31
	s_ashr_i32 s9, s9, 5
	s_add_i32 s9, s9, s10
	v_mfma_f32_16x16x32_bf16 v[64:67], v[156:159], v[188:191], v[64:67]
	s_lshl_b32 s10, s9, 3
	s_sub_i32 s11, 0x80, s10
	s_min_i32 s11, s11, 8
	v_mfma_f32_16x16x32_bf16 v[56:59], v[164:167], v[188:191], v[56:59]
	s_abs_i32 s12, s11
	v_cvt_f32_u32_e32 v241, s12
	s_sub_i32 s14, 0, s12
	v_mfma_f32_16x16x32_bf16 v[48:51], v[156:159], v[196:199], v[48:51]
	s_mulk_i32 s9, 0xb0
	s_sub_i32 s9, s8, s9
	v_rcp_iflag_f32_e32 v241, v241
	v_mfma_f32_16x16x32_bf16 v[40:43], v[164:167], v[196:199], v[40:43]
	s_abs_i32 s8, s9
	s_xor_b32 s13, s9, s11
	s_ashr_i32 s13, s13, 31
	v_mfma_f32_16x16x32_bf16 v[32:35], v[156:159], v[216:219], v[32:35]
	v_mul_f32_e32 v241, 0x4f7ffffe, v241
	v_cvt_u32_f32_e32 v241, v241
	s_mov_b32 s56, s55
	v_mfma_f32_16x16x32_bf16 v[24:27], v[164:167], v[216:219], v[24:27]
	v_readfirstlane_b32 s15, v241
	s_mul_i32 s14, s14, s15
	s_mul_hi_u32 s14, s15, s14
	v_mfma_f32_16x16x32_bf16 v[16:19], v[156:159], v[224:227], v[16:19]
	s_add_i32 s15, s15, s14
	s_mul_hi_u32 s14, s8, s15
	s_mul_i32 s15, s14, s12
	v_mfma_f32_16x16x32_bf16 v[8:11], v[164:167], v[224:227], v[8:11]
	s_sub_i32 s8, s8, s15
	s_add_i32 s36, s14, 1
	s_sub_i32 s15, s8, s12
	s_setprio 0
	s_setprio 1
	v_mfma_f32_16x16x32_bf16 v[60:63], v[168:171], v[184:187], v[60:63]
	s_cmp_ge_u32 s8, s12
	s_cselect_b32 s14, s36, s14
	s_cselect_b32 s8, s15, s8
	v_mfma_f32_16x16x32_bf16 v[52:55], v[176:179], v[184:187], v[52:55]
	s_add_i32 s15, s14, 1
	s_cmp_ge_u32 s8, s12
	s_cselect_b32 s8, s15, s14
	v_mfma_f32_16x16x32_bf16 v[44:47], v[168:171], v[192:195], v[44:47]
	s_xor_b32 s8, s8, s13
	s_sub_i32 s8, s8, s13
	s_mul_i32 s11, s8, s11
	v_mfma_f32_16x16x32_bf16 v[36:39], v[176:179], v[192:195], v[36:39]
	s_sub_i32 s9, s9, s11
	s_add_i32 s10, s10, s9
	s_ashr_i32 s11, s10, 31
	v_mfma_f32_16x16x32_bf16 v[28:31], v[168:171], v[212:215], v[28:31]
	s_lshl_b64 s[12:13], s[10:11], 19
	s_add_u32 s12, s38, s12
	s_addc_u32 s13, s39, s13
	v_mfma_f32_16x16x32_bf16 v[20:23], v[176:179], v[212:215], v[20:23]
	s_and_b64 s[14:15], s[2:3], exec
	s_cselect_b32 s11, s13, s47
	s_cselect_b32 s59, s12, s46
	v_mfma_f32_16x16x32_bf16 v[12:15], v[168:171], v[220:223], v[12:15]
	s_ashr_i32 s9, s8, 31
	s_lshl_b64 s[14:15], s[8:9], 19
	s_add_u32 s14, s40, s14
	v_mfma_f32_16x16x32_bf16 v[4:7], v[176:179], v[220:223], v[4:7]
	s_addc_u32 s15, s41, s15
	s_and_b64 s[36:37], s[2:3], exec
	s_cselect_b32 s9, s15, s53
	v_mfma_f32_16x16x32_bf16 v[60:63], v[172:175], v[188:191], v[60:63]
	s_cselect_b32 s60, s14, s52
	s_add_i32 s62, s62, 2
	s_add_u32 s46, s46, 0x100
	v_mfma_f32_16x16x32_bf16 v[52:55], v[180:183], v[188:191], v[52:55]
	s_addc_u32 s47, s47, 0
	s_add_u32 s52, s52, 0x100
	s_addc_u32 s53, s53, 0
	v_mfma_f32_16x16x32_bf16 v[44:47], v[172:175], v[196:199], v[44:47]
	s_add_u32 s36, s46, 0xfffc0080
	s_addc_u32 s37, s47, -1
	s_add_i32 s63, 0, 0x10000
	v_mfma_f32_16x16x32_bf16 v[36:39], v[180:183], v[196:199], v[36:39]
	s_cmp_eq_u32 s62, 12
	s_cselect_b32 s37, s11, s37
	v_mfma_f32_16x16x32_bf16 v[28:31], v[172:175], v[216:219], v[28:31]
	s_cselect_b32 s36, s59, s36
	v_add_u32_e32 v148, s63, v151
	v_mfma_f32_16x16x32_bf16 v[20:23], v[180:183], v[216:219], v[20:23]
	s_cselect_b32 s73, s9, s53
	s_cselect_b32 s72, s60, s52
	v_mfma_f32_16x16x32_bf16 v[12:15], v[172:175], v[224:227], v[12:15]
	s_add_i32 s68, 0, 0x14000
	s_cmp_gt_u32 s62, 13
	v_mfma_f32_16x16x32_bf16 v[4:7], v[180:183], v[224:227], v[4:7]
	s_setprio 0
	s_barrier
	s_cbranch_scc1 .Lpeel_done_727
; #define PG8_STAGE(bufoff, gbase, voff) do { _Pragma("unroll") for (int _i = 0; _i < 2; ++_i) \
;         __builtin_amdgcn_global_load_lds((const unsigned*)((const char*)(gbase) + (voff)[_i]), (PG8_LAS unsigned*)(lds + (bufoff) + ldsw + _i * 8192), 16, 0, 0); } while (0)
; #define PG8_LDA(dst, b, h) do { _Pragma("unroll") for (int m = 0; m < 4; ++m) _Pragma("unroll") for (int k = 0; k < 2; ++k) dst[m][k] = *(const PG8_LAS bf16x8*)(lds + PG8_SA(b, h) + aoff + m * 2048 + k * 1024); } while (0)
; #define PG8_LDB(dst, b, h) do { _Pragma("unroll") for (int n = 0; n < 2; ++n) _Pragma("unroll") for (int k = 0; k < 2; ++k) dst[n][k] = *(const PG8_LAS bf16x8*)(lds + PG8_SB(b, h) + boff + n * 2048 + k * 1024); } while (0)
; #define PG8_MMA(ai, bj, At, Bt) do { __builtin_amdgcn_s_setprio(1); _Pragma("unroll") for (int m = 0; m < 4; ++m) _Pragma("unroll") for (int n = 0; n < 2; ++n) _Pragma("unroll") for (int k = 0; k < 2; ++k) \
;         acc[ai][bj][m][n] = __builtin_amdgcn_mfma_f32_16x16x32_bf16(Bt[n][k], At[m][k], acc[ai][bj][m][n], 0, 0, 0); __builtin_amdgcn_s_setprio(0); } while (0)
; #define PG8_WAIT_V(n) asm volatile("s_waitcnt vmcnt(" #n ")" ::: "memory")
; #define PG8_BAR __builtin_amdgcn_s_barrier()
; template <class Epi, class Sched, bool ALIGN_EPI = false, bool SP2 = false>
; __device__ __forceinline__ void gemm_phase(PG8_LAS unsigned char* lds, const Gemm g, const Sched& S, const Epi& E, const int tid) {
;     ...
;         for (int t = 0; t < nt; t += 2) {
;             const bool last = (t == nt - 2);
;             const char* a1 = cA + (size_t)(t + 1) * kstep;
;             const char* a2 = last ? nA : cA + (size_t)(t + 2) * kstep; const char* b2 = last ? nB : cB + (size_t)(t + 2) * kstep;
;             const char* a3 = a2 + kstep; const char* b3 = b2 + kstep;
;             if (last && has_next) S.a_ready(nxt);
;             if constexpr (SP2) {
;             PG8_LDB(B0, 0, 0); PG8_LDB(B1, 0, 1); PG8_SCHED; PG8_LDA(At, 0, 0); PG8_STAGE(PG8_SA(1, 1), a1 + hstep, voffA);
;             PG8_WAIT_V(8); PG8_WAIT_L(0); PG8_BAR; PG8_MMA(0, 0, At, B0); PG8_MMA(0, 1, At, B1); PG8_BAR; PG8_SCHED;
;             PG8_LDA(At, 0, 1); PG8_STAGE(PG8_SB(0, 0), b2, voffB); PG8_STAGE(PG8_SB(0, 1), b2, voffB1); PG8_STAGE(PG8_SA(0, 0), a2, voffA);
;             PG8_WAIT_V(8); PG8_WAIT_L(0); PG8_BAR; PG8_MMA(1, 0, At, B0); PG8_MMA(1, 1, At, B1); PG8_BAR; PG8_SCHED;
.LBB0_727:
	ds_read_b128 v[144:147], v148
	ds_read_b128 v[156:159], v148 offset:1024
	ds_read_b128 v[160:163], v148 offset:2048
	ds_read_b128 v[164:167], v148 offset:3072
	v_add_u32_e32 v148, s68, v151
	ds_read_b128 v[168:171], v148
	ds_read_b128 v[172:175], v148 offset:1024
	ds_read_b128 v[176:179], v148 offset:2048
	ds_read_b128 v[180:183], v148 offset:3072
	v_lshl_add_u64 v[148:149], s[46:47], 0, v[140:141]
	s_add_i32 m0, s43, 0xc000
	ds_read_b128 v[184:187], v154
	ds_read_b128 v[188:191], v154 offset:1024
	ds_read_b128 v[192:195], v154 offset:2048
	ds_read_b128 v[196:199], v154 offset:3072
	ds_read_b128 v[212:215], v154 offset:4096
	ds_read_b128 v[216:219], v154 offset:5120
	ds_read_b128 v[220:223], v154 offset:6144
	ds_read_b128 v[224:227], v154 offset:7168
	global_load_lds_dwordx4 v[148:149], off
	v_lshl_add_u64 v[148:149], s[46:47], 0, v[142:143]
	s_add_i32 m0, s43, 0xe000
	s_nop 0
	global_load_lds_dwordx4 v[148:149], off
	s_waitcnt vmcnt(8)
	s_waitcnt lgkmcnt(0)
	s_barrier
	s_setprio 1
	s_waitcnt lgkmcnt(0)
	v_mfma_f32_16x16x32_bf16 v[128:131], v[144:147], v[184:187], v[128:131]
	v_mfma_f32_16x16x32_bf16 v[120:123], v[160:163], v[184:187], v[120:123]
	v_mfma_f32_16x16x32_bf16 v[112:115], v[144:147], v[192:195], v[112:115]
	v_mfma_f32_16x16x32_bf16 v[104:107], v[160:163], v[192:195], v[104:107]
	v_mfma_f32_16x16x32_bf16 v[96:99], v[144:147], v[212:215], v[96:99]
	v_mfma_f32_16x16x32_bf16 v[88:91], v[160:163], v[212:215], v[88:91]
	v_mfma_f32_16x16x32_bf16 v[80:83], v[144:147], v[220:223], v[80:83]
	v_mfma_f32_16x16x32_bf16 v[72:75], v[160:163], v[220:223], v[72:75]
	v_mfma_f32_16x16x32_bf16 v[128:131], v[156:159], v[188:191], v[128:131]
	v_mfma_f32_16x16x32_bf16 v[120:123], v[164:167], v[188:191], v[120:123]
	v_mfma_f32_16x16x32_bf16 v[112:115], v[156:159], v[196:199], v[112:115]
	v_mfma_f32_16x16x32_bf16 v[104:107], v[164:167], v[196:199], v[104:107]
	v_mfma_f32_16x16x32_bf16 v[96:99], v[156:159], v[216:219], v[96:99]
	v_mfma_f32_16x16x32_bf16 v[88:91], v[164:167], v[216:219], v[88:91]
	v_mfma_f32_16x16x32_bf16 v[80:83], v[156:159], v[224:227], v[80:83]
	v_mfma_f32_16x16x32_bf16 v[72:75], v[164:167], v[224:227], v[72:75]
	s_setprio 0
	s_setprio 1
	v_mfma_f32_16x16x32_bf16 v[124:127], v[168:171], v[184:187], v[124:127]
	v_mfma_f32_16x16x32_bf16 v[116:119], v[176:179], v[184:187], v[116:119]
	v_mfma_f32_16x16x32_bf16 v[108:111], v[168:171], v[192:195], v[108:111]
	v_mfma_f32_16x16x32_bf16 v[100:103], v[176:179], v[192:195], v[100:103]
	v_mfma_f32_16x16x32_bf16 v[92:95], v[168:171], v[212:215], v[92:95]
	v_mfma_f32_16x16x32_bf16 v[84:87], v[176:179], v[212:215], v[84:87]
	v_mfma_f32_16x16x32_bf16 v[76:79], v[168:171], v[220:223], v[76:79]
	v_mfma_f32_16x16x32_bf16 v[68:71], v[176:179], v[220:223], v[68:71]
	v_mfma_f32_16x16x32_bf16 v[124:127], v[172:175], v[188:191], v[124:127]
	v_mfma_f32_16x16x32_bf16 v[116:119], v[180:183], v[188:191], v[116:119]
	v_mfma_f32_16x16x32_bf16 v[108:111], v[172:175], v[196:199], v[108:111]
	v_mfma_f32_16x16x32_bf16 v[100:103], v[180:183], v[196:199], v[100:103]
	v_mfma_f32_16x16x32_bf16 v[92:95], v[172:175], v[216:219], v[92:95]
	v_mfma_f32_16x16x32_bf16 v[84:87], v[180:183], v[216:219], v[84:87]
	v_mfma_f32_16x16x32_bf16 v[76:79], v[172:175], v[224:227], v[76:79]
	v_mfma_f32_16x16x32_bf16 v[68:71], v[180:183], v[224:227], v[68:71]
	s_setprio 0
	s_barrier
	s_add_i32 s63, s63, s33
	v_lshl_add_u64 v[148:149], s[72:73], 0, v[2:3]
	s_mov_b32 m0, s63
	ds_read_b128 v[184:187], v154 offset:16384
	ds_read_b128 v[188:191], v154 offset:17408
	ds_read_b128 v[192:195], v154 offset:18432
	ds_read_b128 v[196:199], v154 offset:19456
	ds_read_b128 v[212:215], v154 offset:20480
	ds_read_b128 v[216:219], v154 offset:21504
	ds_read_b128 v[220:223], v154 offset:22528
	ds_read_b128 v[224:227], v154 offset:23552
	global_load_lds_dwordx4 v[148:149], off
	v_lshl_add_u64 v[200:201], s[72:73], 0, v[132:133]
	s_add_i32 m0, s63, 0x2000
	s_add_i32 s63, s68, s33
	global_load_lds_dwordx4 v[200:201], off
	v_lshl_add_u64 v[202:203], s[72:73], 0, v[136:137]
	s_mov_b32 m0, s63
	v_lshl_add_u64 v[204:205], s[72:73], 0, v[0:1]
	global_load_lds_dwordx4 v[202:203], off
	s_add_i32 m0, s63, 0x2000
	v_lshl_add_u64 v[208:209], s[36:37], 0, v[138:139]
	global_load_lds_dwordx4 v[204:205], off
	s_mov_b32 m0, s43
	v_lshl_add_u64 v[210:211], s[36:37], 0, v[134:135]
	global_load_lds_dwordx4 v[208:209], off
	s_mov_b32 m0, s45
	s_nop 0
	global_load_lds_dwordx4 v[210:211], off
	s_waitcnt vmcnt(8)
	s_waitcnt lgkmcnt(0)
	s_barrier
	s_setprio 1
	s_waitcnt lgkmcnt(0)
	v_mfma_f32_16x16x32_bf16 v[64:67], v[144:147], v[184:187], v[64:67]
	v_mfma_f32_16x16x32_bf16 v[56:59], v[160:163], v[184:187], v[56:59]
	v_mfma_f32_16x16x32_bf16 v[48:51], v[144:147], v[192:195], v[48:51]
	v_mfma_f32_16x16x32_bf16 v[40:43], v[160:163], v[192:195], v[40:43]
	v_mfma_f32_16x16x32_bf16 v[32:35], v[144:147], v[212:215], v[32:35]
	v_mfma_f32_16x16x32_bf16 v[24:27], v[160:163], v[212:215], v[24:27]
	v_mfma_f32_16x16x32_bf16 v[16:19], v[144:147], v[220:223], v[16:19]
	v_mfma_f32_16x16x32_bf16 v[8:11], v[160:163], v[220:223], v[8:11]
	v_mfma_f32_16x16x32_bf16 v[64:67], v[156:159], v[188:191], v[64:67]
	v_mfma_f32_16x16x32_bf16 v[56:59], v[164:167], v[188:191], v[56:59]
	v_mfma_f32_16x16x32_bf16 v[48:51], v[156:159], v[196:199], v[48:51]
	v_mfma_f32_16x16x32_bf16 v[40:43], v[164:167], v[196:199], v[40:43]
	v_mfma_f32_16x16x32_bf16 v[32:35], v[156:159], v[216:219], v[32:35]
	v_mfma_f32_16x16x32_bf16 v[24:27], v[164:167], v[216:219], v[24:27]
	v_mfma_f32_16x16x32_bf16 v[16:19], v[156:159], v[224:227], v[16:19]
	v_mfma_f32_16x16x32_bf16 v[8:11], v[164:167], v[224:227], v[8:11]
	s_setprio 0
	s_setprio 1
	v_mfma_f32_16x16x32_bf16 v[60:63], v[168:171], v[184:187], v[60:63]
	v_mfma_f32_16x16x32_bf16 v[52:55], v[176:179], v[184:187], v[52:55]
	v_mfma_f32_16x16x32_bf16 v[44:47], v[168:171], v[192:195], v[44:47]
	v_mfma_f32_16x16x32_bf16 v[36:39], v[176:179], v[192:195], v[36:39]
	v_mfma_f32_16x16x32_bf16 v[28:31], v[168:171], v[212:215], v[28:31]
	v_mfma_f32_16x16x32_bf16 v[20:23], v[176:179], v[212:215], v[20:23]
	v_mfma_f32_16x16x32_bf16 v[12:15], v[168:171], v[220:223], v[12:15]
	v_mfma_f32_16x16x32_bf16 v[4:7], v[176:179], v[220:223], v[4:7]
	v_mfma_f32_16x16x32_bf16 v[60:63], v[172:175], v[188:191], v[60:63]
	v_mfma_f32_16x16x32_bf16 v[52:55], v[180:183], v[188:191], v[52:55]
	v_mfma_f32_16x16x32_bf16 v[44:47], v[172:175], v[196:199], v[44:47]
	v_mfma_f32_16x16x32_bf16 v[36:39], v[180:183], v[196:199], v[36:39]
	v_mfma_f32_16x16x32_bf16 v[28:31], v[172:175], v[216:219], v[28:31]
	v_mfma_f32_16x16x32_bf16 v[20:23], v[180:183], v[216:219], v[20:23]
	v_mfma_f32_16x16x32_bf16 v[12:15], v[172:175], v[224:227], v[12:15]
	v_mfma_f32_16x16x32_bf16 v[4:7], v[180:183], v[224:227], v[4:7]
	s_setprio 0
	s_barrier
; #define PG8_STAGE(bufoff, gbase, voff) do { _Pragma("unroll") for (int _i = 0; _i < 2; ++_i) \
;         __builtin_amdgcn_global_load_lds((const unsigned*)((const char*)(gbase) + (voff)[_i]), (PG8_LAS unsigned*)(lds + (bufoff) + ldsw + _i * 8192), 16, 0, 0); } while (0)
; #define PG8_LDA(dst, b, h) do { _Pragma("unroll") for (int m = 0; m < 4; ++m) _Pragma("unroll") for (int k = 0; k < 2; ++k) dst[m][k] = *(const PG8_LAS bf16x8*)(lds + PG8_SA(b, h) + aoff + m * 2048 + k * 1024); } while (0)
; #define PG8_LDB(dst, b, h) do { _Pragma("unroll") for (int n = 0; n < 2; ++n) _Pragma("unroll") for (int k = 0; k < 2; ++k) dst[n][k] = *(const PG8_LAS bf16x8*)(lds + PG8_SB(b, h) + boff + n * 2048 + k * 1024); } while (0)
; #define PG8_MMA(ai, bj, At, Bt) do { __builtin_amdgcn_s_setprio(1); _Pragma("unroll") for (int m = 0; m < 4; ++m) _Pragma("unroll") for (int n = 0; n < 2; ++n) _Pragma("unroll") for (int k = 0; k < 2; ++k) \
;         acc[ai][bj][m][n] = __builtin_amdgcn_mfma_f32_16x16x32_bf16(Bt[n][k], At[m][k], acc[ai][bj][m][n], 0, 0, 0); __builtin_amdgcn_s_setprio(0); } while (0)
; #define PG8_WAIT_V(n) asm volatile("s_waitcnt vmcnt(" #n ")" ::: "memory")
; #define PG8_WAIT_L(n) asm volatile("s_waitcnt lgkmcnt(" #n ")" ::: "memory")
; #define PG8_BAR __builtin_amdgcn_s_barrier()
; #define PG8_SCHED __builtin_amdgcn_sched_barrier(0)
; template <class Epi, class Sched, bool ALIGN_EPI = false, bool SP2 = false>
; __device__ __forceinline__ void gemm_phase(PG8_LAS unsigned char* lds, const Gemm g, const Sched& S, const Epi& E, const int tid) {
;     ...
;             PG8_LDB(B0, 1, 0); PG8_LDB(B1, 1, 1); PG8_SCHED; PG8_LDA(At, 1, 0); PG8_STAGE(PG8_SA(0, 1), a2 + hstep, voffA);
;             PG8_WAIT_V(8); PG8_WAIT_L(0); PG8_BAR; PG8_MMA(0, 0, At, B0); PG8_MMA(0, 1, At, B1); PG8_BAR; PG8_SCHED;
	s_add_i32 s63, 0, 0x18000
	v_add_u32_e32 v155, s63, v151
	s_add_i32 s68, 0, 0x1c000
	ds_read_b128 v[144:147], v155
	ds_read_b128 v[156:159], v155 offset:1024
	ds_read_b128 v[160:163], v155 offset:2048
	ds_read_b128 v[164:167], v155 offset:3072
	v_add_u32_e32 v155, s68, v151
	ds_read_b128 v[168:171], v155
	ds_read_b128 v[172:175], v155 offset:1024
	ds_read_b128 v[176:179], v155 offset:2048
	ds_read_b128 v[180:183], v155 offset:3072
	s_add_u32 s36, s36, 0x40000
	s_addc_u32 s37, s37, 0
	s_mov_b32 m0, s48
	v_lshl_add_u64 v[228:229], s[36:37], 0, v[138:139]
	ds_read_b128 v[184:187], v154 offset:32768
	ds_read_b128 v[188:191], v154 offset:33792
	ds_read_b128 v[192:195], v154 offset:34816
	ds_read_b128 v[196:199], v154 offset:35840
	ds_read_b128 v[212:215], v154 offset:36864
	ds_read_b128 v[216:219], v154 offset:37888
	ds_read_b128 v[220:223], v154 offset:38912
	ds_read_b128 v[224:227], v154 offset:39936
	global_load_lds_dwordx4 v[228:229], off
	v_lshl_add_u64 v[228:229], s[36:37], 0, v[134:135]
	s_mov_b32 m0, s49
	s_nop 0
	global_load_lds_dwordx4 v[228:229], off
	s_waitcnt vmcnt(8)
	s_waitcnt lgkmcnt(0)
	s_barrier
	s_setprio 1
	s_waitcnt lgkmcnt(0)
	v_mfma_f32_16x16x32_bf16 v[128:131], v[144:147], v[184:187], v[128:131]
	v_mfma_f32_16x16x32_bf16 v[120:123], v[160:163], v[184:187], v[120:123]
	v_mfma_f32_16x16x32_bf16 v[112:115], v[144:147], v[192:195], v[112:115]
	v_mfma_f32_16x16x32_bf16 v[104:107], v[160:163], v[192:195], v[104:107]
	v_mfma_f32_16x16x32_bf16 v[96:99], v[144:147], v[212:215], v[96:99]
	v_mfma_f32_16x16x32_bf16 v[88:91], v[160:163], v[212:215], v[88:91]
	v_mfma_f32_16x16x32_bf16 v[80:83], v[144:147], v[220:223], v[80:83]
	v_mfma_f32_16x16x32_bf16 v[72:75], v[160:163], v[220:223], v[72:75]
	v_mfma_f32_16x16x32_bf16 v[128:131], v[156:159], v[188:191], v[128:131]
	v_mfma_f32_16x16x32_bf16 v[120:123], v[164:167], v[188:191], v[120:123]
	v_mfma_f32_16x16x32_bf16 v[112:115], v[156:159], v[196:199], v[112:115]
	v_mfma_f32_16x16x32_bf16 v[104:107], v[164:167], v[196:199], v[104:107]
	v_mfma_f32_16x16x32_bf16 v[96:99], v[156:159], v[216:219], v[96:99]
	v_mfma_f32_16x16x32_bf16 v[88:91], v[164:167], v[216:219], v[88:91]
	v_mfma_f32_16x16x32_bf16 v[80:83], v[156:159], v[224:227], v[80:83]
	v_mfma_f32_16x16x32_bf16 v[72:75], v[164:167], v[224:227], v[72:75]
	s_setprio 0
	s_setprio 1
	v_mfma_f32_16x16x32_bf16 v[124:127], v[168:171], v[184:187], v[124:127]
	v_mfma_f32_16x16x32_bf16 v[116:119], v[176:179], v[184:187], v[116:119]
	v_mfma_f32_16x16x32_bf16 v[108:111], v[168:171], v[192:195], v[108:111]
	v_mfma_f32_16x16x32_bf16 v[100:103], v[176:179], v[192:195], v[100:103]
	v_mfma_f32_16x16x32_bf16 v[92:95], v[168:171], v[212:215], v[92:95]
	v_mfma_f32_16x16x32_bf16 v[84:87], v[176:179], v[212:215], v[84:87]
	v_mfma_f32_16x16x32_bf16 v[76:79], v[168:171], v[220:223], v[76:79]
	v_mfma_f32_16x16x32_bf16 v[68:71], v[176:179], v[220:223], v[68:71]
	v_mfma_f32_16x16x32_bf16 v[124:127], v[172:175], v[188:191], v[124:127]
	v_mfma_f32_16x16x32_bf16 v[116:119], v[180:183], v[188:191], v[116:119]
	v_mfma_f32_16x16x32_bf16 v[108:111], v[172:175], v[196:199], v[108:111]
	v_mfma_f32_16x16x32_bf16 v[100:103], v[180:183], v[196:199], v[100:103]
	v_mfma_f32_16x16x32_bf16 v[92:95], v[172:175], v[216:219], v[92:95]
	v_mfma_f32_16x16x32_bf16 v[84:87], v[180:183], v[216:219], v[84:87]
	v_mfma_f32_16x16x32_bf16 v[76:79], v[172:175], v[224:227], v[76:79]
	v_mfma_f32_16x16x32_bf16 v[68:71], v[180:183], v[224:227], v[68:71]
	s_setprio 0
	s_barrier
; #define PG8_STAGE(bufoff, gbase, voff) do { _Pragma("unroll") for (int _i = 0; _i < 2; ++_i) \
;         __builtin_amdgcn_global_load_lds((const unsigned*)((const char*)(gbase) + (voff)[_i]), (PG8_LAS unsigned*)(lds + (bufoff) + ldsw + _i * 8192), 16, 0, 0); } while (0)
; #define PG8_LDA(dst, b, h) do { _Pragma("unroll") for (int m = 0; m < 4; ++m) _Pragma("unroll") for (int k = 0; k < 2; ++k) dst[m][k] = *(const PG8_LAS bf16x8*)(lds + PG8_SA(b, h) + aoff + m * 2048 + k * 1024); } while (0)
; #define PG8_MMA(ai, bj, At, Bt) do { __builtin_amdgcn_s_setprio(1); _Pragma("unroll") for (int m = 0; m < 4; ++m) _Pragma("unroll") for (int n = 0; n < 2; ++n) _Pragma("unroll") for (int k = 0; k < 2; ++k) \
;         acc[ai][bj][m][n] = __builtin_amdgcn_mfma_f32_16x16x32_bf16(Bt[n][k], At[m][k], acc[ai][bj][m][n], 0, 0, 0); __builtin_amdgcn_s_setprio(0); } while (0)
; #define PG8_WAIT_V(n) asm volatile("s_waitcnt vmcnt(" #n ")" ::: "memory")
; #define PG8_WAIT_L(n) asm volatile("s_waitcnt lgkmcnt(" #n ")" ::: "memory")
; #define PG8_BAR __builtin_amdgcn_s_barrier()
; #define PG8_SCHED __builtin_amdgcn_sched_barrier(0)
; template <class Epi, class Sched, bool ALIGN_EPI = false, bool SP2 = false>
; __device__ __forceinline__ void gemm_phase(PG8_LAS unsigned char* lds, const Gemm g, const Sched& S, const Epi& E, const int tid) {
;     ...
;         for (int t = 0; t < nt; t += 2) {
;             const bool last = (t == nt - 2);
;             const char* a1 = cA + (size_t)(t + 1) * kstep;
;             const char* a2 = last ? nA : cA + (size_t)(t + 2) * kstep; const char* b2 = last ? nB : cB + (size_t)(t + 2) * kstep;
;             const char* a3 = a2 + kstep; const char* b3 = b2 + kstep;
;     ...
;             PG8_LDA(At, 1, 1); PG8_STAGE(PG8_SB(1, 0), b3, voffB); PG8_STAGE(PG8_SB(1, 1), b3, voffB1); PG8_STAGE(PG8_SA(1, 0), a3, voffA);
;             PG8_WAIT_V(8); PG8_WAIT_L(0); PG8_BAR; PG8_MMA(1, 0, At, B0); PG8_MMA(1, 1, At, B1); PG8_BAR; PG8_SCHED;
	s_add_i32 s36, s63, s33
	v_lshl_add_u64 v[148:149], v[148:149], 0, s[66:67]
	s_mov_b32 m0, s36
	ds_read_b128 v[184:187], v154 offset:49152
	ds_read_b128 v[188:191], v154 offset:50176
	ds_read_b128 v[192:195], v154 offset:51200
	ds_read_b128 v[196:199], v154 offset:52224
	ds_read_b128 v[212:215], v154 offset:53248
	ds_read_b128 v[216:219], v154 offset:54272
	ds_read_b128 v[220:223], v154 offset:55296
	ds_read_b128 v[224:227], v154 offset:56320
	global_load_lds_dwordx4 v[148:149], off
	v_lshl_add_u64 v[148:149], v[200:201], 0, s[66:67]
	s_add_i32 m0, s36, 0x2000
	s_add_i32 s36, s68, s33
	global_load_lds_dwordx4 v[148:149], off
	v_lshl_add_u64 v[148:149], v[202:203], 0, s[66:67]
	s_mov_b32 m0, s36
	s_nop 0
	global_load_lds_dwordx4 v[148:149], off
	v_lshl_add_u64 v[148:149], v[204:205], 0, s[66:67]
	s_add_i32 m0, s36, 0x2000
	s_nop 0
	global_load_lds_dwordx4 v[148:149], off
	v_lshl_add_u64 v[148:149], v[208:209], 0, s[66:67]
	s_mov_b32 m0, s50
	s_nop 0
	global_load_lds_dwordx4 v[148:149], off
	v_lshl_add_u64 v[148:149], v[210:211], 0, s[66:67]
	s_mov_b32 m0, s51
	s_nop 0
	global_load_lds_dwordx4 v[148:149], off
	s_waitcnt vmcnt(8)
	s_waitcnt lgkmcnt(0)
	s_barrier
	s_setprio 1
	s_waitcnt lgkmcnt(0)
	v_mfma_f32_16x16x32_bf16 v[64:67], v[144:147], v[184:187], v[64:67]
	v_mfma_f32_16x16x32_bf16 v[56:59], v[160:163], v[184:187], v[56:59]
	v_mfma_f32_16x16x32_bf16 v[48:51], v[144:147], v[192:195], v[48:51]
	v_mfma_f32_16x16x32_bf16 v[40:43], v[160:163], v[192:195], v[40:43]
	v_mfma_f32_16x16x32_bf16 v[32:35], v[144:147], v[212:215], v[32:35]
	v_mfma_f32_16x16x32_bf16 v[24:27], v[160:163], v[212:215], v[24:27]
	v_mfma_f32_16x16x32_bf16 v[16:19], v[144:147], v[220:223], v[16:19]
	v_mfma_f32_16x16x32_bf16 v[8:11], v[160:163], v[220:223], v[8:11]
	v_mfma_f32_16x16x32_bf16 v[64:67], v[156:159], v[188:191], v[64:67]
	s_add_i32 s62, s62, 2
	v_mfma_f32_16x16x32_bf16 v[56:59], v[164:167], v[188:191], v[56:59]
	s_add_u32 s46, s46, 0x100
	v_mfma_f32_16x16x32_bf16 v[48:51], v[156:159], v[196:199], v[48:51]
	s_addc_u32 s47, s47, 0
	v_mfma_f32_16x16x32_bf16 v[40:43], v[164:167], v[196:199], v[40:43]
	s_add_u32 s52, s52, 0x100
	v_mfma_f32_16x16x32_bf16 v[32:35], v[156:159], v[216:219], v[32:35]
	s_addc_u32 s53, s53, 0
	v_mfma_f32_16x16x32_bf16 v[24:27], v[164:167], v[216:219], v[24:27]
	s_add_u32 s36, s46, 0xfffc0080
	v_mfma_f32_16x16x32_bf16 v[16:19], v[156:159], v[224:227], v[16:19]
	s_addc_u32 s37, s47, -1
	v_mfma_f32_16x16x32_bf16 v[8:11], v[164:167], v[224:227], v[8:11]
	s_add_i32 s63, 0, 0x10000
	s_setprio 0
	s_setprio 1
	v_mfma_f32_16x16x32_bf16 v[60:63], v[168:171], v[184:187], v[60:63]
	s_cmp_eq_u32 s62, 12
	v_mfma_f32_16x16x32_bf16 v[52:55], v[176:179], v[184:187], v[52:55]
	s_cselect_b32 s37, s11, s37
	v_mfma_f32_16x16x32_bf16 v[44:47], v[168:171], v[192:195], v[44:47]
	s_cselect_b32 s36, s59, s36
	v_mfma_f32_16x16x32_bf16 v[36:39], v[176:179], v[192:195], v[36:39]
	v_add_u32_e32 v148, s63, v151
	v_mfma_f32_16x16x32_bf16 v[28:31], v[168:171], v[212:215], v[28:31]
	s_cselect_b32 s73, s9, s53
	v_mfma_f32_16x16x32_bf16 v[20:23], v[176:179], v[212:215], v[20:23]
	s_cselect_b32 s72, s60, s52
	v_mfma_f32_16x16x32_bf16 v[12:15], v[168:171], v[220:223], v[12:15]
	s_add_i32 s68, 0, 0x14000
	v_mfma_f32_16x16x32_bf16 v[4:7], v[176:179], v[220:223], v[4:7]
	s_cmp_gt_u32 s62, 13
	v_mfma_f32_16x16x32_bf16 v[60:63], v[172:175], v[188:191], v[60:63]
	v_mfma_f32_16x16x32_bf16 v[52:55], v[180:183], v[188:191], v[52:55]
	v_mfma_f32_16x16x32_bf16 v[44:47], v[172:175], v[196:199], v[44:47]
	v_mfma_f32_16x16x32_bf16 v[36:39], v[180:183], v[196:199], v[36:39]
	v_mfma_f32_16x16x32_bf16 v[28:31], v[172:175], v[216:219], v[28:31]
	v_mfma_f32_16x16x32_bf16 v[20:23], v[180:183], v[216:219], v[20:23]
	v_mfma_f32_16x16x32_bf16 v[12:15], v[172:175], v[224:227], v[12:15]
	v_mfma_f32_16x16x32_bf16 v[4:7], v[180:183], v[224:227], v[4:7]
	s_setprio 0
	s_barrier
	s_cbranch_scc0 .LBB0_727
